# removed redundant adjacent s_setprio 0 / s_setprio 1 pairs in the GEMM loops and XNACK-only s_nop 0 pads between back-to-back row loads in the PEER gather prefetch blocks
# speedup vs baseline: 1.0094x; 1.0050x over previous
; #define PG8_STAGE(bufoff, gbase, voff) do { _Pragma("unroll") for (int _i = 0; _i < 2; ++_i) \
;         __builtin_amdgcn_global_load_lds((const unsigned*)((const char*)(gbase) + (voff)[_i]), (PG8_LAS unsigned*)(lds + (bufoff) + ldsw + _i * 8192), 16, 0, 0); } while (0)
; #define PG8_LDA(dst, b, h) do { _Pragma("unroll") for (int m = 0; m < 4; ++m) _Pragma("unroll") for (int k = 0; k < 2; ++k) dst[m][k] = *(const PG8_LAS bf16x8*)(lds + PG8_SA(b, h) + aoff + m * 2048 + k * 1024); } while (0)
; #define PG8_LDB(dst, b, h) do { _Pragma("unroll") for (int n = 0; n < 2; ++n) _Pragma("unroll") for (int k = 0; k < 2; ++k) dst[n][k] = *(const PG8_LAS bf16x8*)(lds + PG8_SB(b, h) + boff + n * 2048 + k * 1024); } while (0)
; #define PG8_MMA(ai, bj, At, Bt) do { __builtin_amdgcn_s_setprio(1); _Pragma("unroll") for (int m = 0; m < 4; ++m) _Pragma("unroll") for (int n = 0; n < 2; ++n) _Pragma("unroll") for (int k = 0; k < 2; ++k) \
;         acc[ai][bj][m][n] = __builtin_amdgcn_mfma_f32_16x16x32_bf16(Bt[n][k], At[m][k], acc[ai][bj][m][n], 0, 0, 0); __builtin_amdgcn_s_setprio(0); } while (0)
; #define PG8_WAIT_V(n) asm volatile("s_waitcnt vmcnt(" #n ")" ::: "memory")
; #define PG8_BAR __builtin_amdgcn_s_barrier()
; template <class Epi, class Sched, bool ALIGN_EPI = false, bool SP2 = false>
; __device__ __forceinline__ void gemm_phase(PG8_LAS unsigned char* lds, const Gemm g, const Sched& S, const Epi& E, const int wave0) {
;     ...
;         for (int t = 0; t < nt; t += 2) {
;             const bool last = (t == nt - 2);
;             const char* a1 = cA + (size_t)(t + 1) * kstep;
;             const char* a2 = last ? nA : cA + (size_t)(t + 2) * kstep; const char* b2 = last ? nB : cB + (size_t)(t + 2) * kstep;
;             const char* a3 = a2 + kstep; const char* b3 = b2 + kstep;
;             if (last && has_next) S.a_ready(nxt);
;             if constexpr (SP2) {
;             PG8_LDB(B0, 0, 0); PG8_LDB(B1, 0, 1); PG8_SCHED; PG8_LDA(At, 0, 0); PG8_STAGE(PG8_SA(1, 1), a1 + hstepA, voffA);
;             PG8_WAIT_V(8); PG8_WAIT_L(0); PG8_BAR; PG8_MMA(0, 0, At, B0); PG8_MMA(0, 1, At, B1); PG8_BAR; PG8_SCHED;
;             PG8_LDA(At, 0, 1); PG8_STAGE(PG8_SB(0, 0), b2, voffB); PG8_STAGE(PG8_SB(0, 1), b2 + hstepB, voffB); PG8_STAGE(PG8_SA(0, 0), a2, voffA);
;             PG8_WAIT_V(8); PG8_WAIT_L(0); PG8_BAR; PG8_MMA(1, 0, At, B0); PG8_MMA(1, 1, At, B1); PG8_BAR; PG8_SCHED;
.LBB0_187:
	s_add_i32 s94, s74, 2
	s_add_u32 s96, s38, 0x80
	s_addc_u32 s75, s39, 0
	s_add_i32 vcc_lo, 0, 0x10000
	s_cmp_eq_u32 s92, s74
	s_cselect_b32 s75, s57, s75
	s_cselect_b32 s74, s56, s96
	s_cselect_b32 s97, s77, s84
	s_cselect_b32 s96, s76, s59
	s_add_i32 vcc_hi, 0, 0x14000
	v_add_u32_e32 v158, vcc_lo, v154
	v_add_u32_e32 v174, vcc_hi, v154
	ds_read_b128 v[142:145], v158
	ds_read_b128 v[146:149], v158 offset:1024
	ds_read_b128 v[150:153], v158 offset:2048
	ds_read_b128 v[158:161], v158 offset:3072
	ds_read_b128 v[162:165], v174
	ds_read_b128 v[166:169], v174 offset:1024
	ds_read_b128 v[170:173], v174 offset:2048
	ds_read_b128 v[174:177], v174 offset:3072
	v_lshl_add_u64 v[206:207], s[38:39], 0, v[140:141]
	s_add_i32 m0, s30, 0xc000
	ds_read_b128 v[178:181], v157
	ds_read_b128 v[182:185], v157 offset:1024
	ds_read_b128 v[186:189], v157 offset:2048
	ds_read_b128 v[190:193], v157 offset:3072
	ds_read_b128 v[194:197], v157 offset:4096
	ds_read_b128 v[198:201], v157 offset:5120
	ds_read_b128 v[202:205], v157 offset:6144
	ds_read_b128 v[224:227], v157 offset:7168
	global_load_lds_dwordx4 v[206:207], off
	v_lshl_add_u64 v[206:207], s[38:39], 0, v[138:139]
	s_add_i32 m0, s30, 0xe000
	s_nop 0
	global_load_lds_dwordx4 v[206:207], off
	s_waitcnt vmcnt(8)
	s_waitcnt lgkmcnt(0)
	s_barrier
	s_setprio 1
	s_waitcnt lgkmcnt(0)
	v_mfma_f32_16x16x32_bf16 v[126:129], v[142:145], v[178:181], v[126:129]
	v_mfma_f32_16x16x32_bf16 v[122:125], v[150:153], v[178:181], v[122:125]
	v_mfma_f32_16x16x32_bf16 v[110:113], v[142:145], v[186:189], v[110:113]
	v_mfma_f32_16x16x32_bf16 v[106:109], v[150:153], v[186:189], v[106:109]
	v_mfma_f32_16x16x32_bf16 v[94:97], v[142:145], v[194:197], v[94:97]
	v_mfma_f32_16x16x32_bf16 v[90:93], v[150:153], v[194:197], v[90:93]
	v_mfma_f32_16x16x32_bf16 v[78:81], v[142:145], v[202:205], v[78:81]
	v_mfma_f32_16x16x32_bf16 v[74:77], v[150:153], v[202:205], v[74:77]
	v_mfma_f32_16x16x32_bf16 v[126:129], v[146:149], v[182:185], v[126:129]
	v_mfma_f32_16x16x32_bf16 v[122:125], v[158:161], v[182:185], v[122:125]
	v_mfma_f32_16x16x32_bf16 v[110:113], v[146:149], v[190:193], v[110:113]
	v_mfma_f32_16x16x32_bf16 v[106:109], v[158:161], v[190:193], v[106:109]
	v_mfma_f32_16x16x32_bf16 v[94:97], v[146:149], v[198:201], v[94:97]
	v_mfma_f32_16x16x32_bf16 v[90:93], v[158:161], v[198:201], v[90:93]
	v_mfma_f32_16x16x32_bf16 v[78:81], v[146:149], v[224:227], v[78:81]
	v_mfma_f32_16x16x32_bf16 v[74:77], v[158:161], v[224:227], v[74:77]
	v_mfma_f32_16x16x32_bf16 v[118:121], v[162:165], v[178:181], v[118:121]
	v_mfma_f32_16x16x32_bf16 v[114:117], v[170:173], v[178:181], v[114:117]
	v_mfma_f32_16x16x32_bf16 v[102:105], v[162:165], v[186:189], v[102:105]
	v_mfma_f32_16x16x32_bf16 v[98:101], v[170:173], v[186:189], v[98:101]
	v_mfma_f32_16x16x32_bf16 v[86:89], v[162:165], v[194:197], v[86:89]
	v_mfma_f32_16x16x32_bf16 v[82:85], v[170:173], v[194:197], v[82:85]
	v_mfma_f32_16x16x32_bf16 v[70:73], v[162:165], v[202:205], v[70:73]
	v_mfma_f32_16x16x32_bf16 v[66:69], v[170:173], v[202:205], v[66:69]
	v_mfma_f32_16x16x32_bf16 v[118:121], v[166:169], v[182:185], v[118:121]
	v_mfma_f32_16x16x32_bf16 v[114:117], v[174:177], v[182:185], v[114:117]
	v_mfma_f32_16x16x32_bf16 v[102:105], v[166:169], v[190:193], v[102:105]
	v_mfma_f32_16x16x32_bf16 v[98:101], v[174:177], v[190:193], v[98:101]
	v_mfma_f32_16x16x32_bf16 v[86:89], v[166:169], v[198:201], v[86:89]
	v_mfma_f32_16x16x32_bf16 v[82:85], v[174:177], v[198:201], v[82:85]
	v_mfma_f32_16x16x32_bf16 v[70:73], v[166:169], v[224:227], v[70:73]
	v_mfma_f32_16x16x32_bf16 v[66:69], v[174:177], v[224:227], v[66:69]
	s_setprio 0
	s_barrier
	s_add_i32 vcc_lo, vcc_lo, s5
	v_lshl_add_u64 v[206:207], s[96:97], 0, v[134:135]
	s_mov_b32 m0, vcc_lo
	ds_read_b128 v[178:181], v157 offset:16384
	ds_read_b128 v[182:185], v157 offset:17408
	ds_read_b128 v[186:189], v157 offset:18432
	ds_read_b128 v[190:193], v157 offset:19456
	ds_read_b128 v[194:197], v157 offset:20480
	ds_read_b128 v[198:201], v157 offset:21504
	ds_read_b128 v[202:205], v157 offset:22528
	ds_read_b128 v[224:227], v157 offset:23552
	global_load_lds_dwordx4 v[206:207], off
	s_add_i32 m0, vcc_lo, 0x2000
	v_lshl_add_u64 v[228:229], s[96:97], 0, v[130:131]
	s_add_u32 s96, s96, s22
	s_addc_u32 s97, s97, s23
	s_add_i32 vcc_lo, vcc_hi, s5
	global_load_lds_dwordx4 v[228:229], off
	v_lshl_add_u64 v[230:231], s[96:97], 0, v[134:135]
	s_mov_b32 m0, vcc_lo
	v_lshl_add_u64 v[232:233], s[96:97], 0, v[130:131]
	global_load_lds_dwordx4 v[230:231], off
	s_add_i32 m0, vcc_lo, 0x2000
	v_lshl_add_u64 v[234:235], s[74:75], 0, v[136:137]
	global_load_lds_dwordx4 v[232:233], off
	s_mov_b32 m0, s30
	v_lshl_add_u64 v[238:239], s[74:75], 0, v[132:133]
	global_load_lds_dwordx4 v[234:235], off
	s_mov_b32 m0, s87
	s_nop 0
	global_load_lds_dwordx4 v[238:239], off
	s_waitcnt vmcnt(8)
	s_waitcnt lgkmcnt(0)
	s_barrier
; #define PG8_STAGE(bufoff, gbase, voff) do { _Pragma("unroll") for (int _i = 0; _i < 2; ++_i) \
;         __builtin_amdgcn_global_load_lds((const unsigned*)((const char*)(gbase) + (voff)[_i]), (PG8_LAS unsigned*)(lds + (bufoff) + ldsw + _i * 8192), 16, 0, 0); } while (0)
; #define PG8_LDA(dst, b, h) do { _Pragma("unroll") for (int m = 0; m < 4; ++m) _Pragma("unroll") for (int k = 0; k < 2; ++k) dst[m][k] = *(const PG8_LAS bf16x8*)(lds + PG8_SA(b, h) + aoff + m * 2048 + k * 1024); } while (0)
; #define PG8_LDB(dst, b, h) do { _Pragma("unroll") for (int n = 0; n < 2; ++n) _Pragma("unroll") for (int k = 0; k < 2; ++k) dst[n][k] = *(const PG8_LAS bf16x8*)(lds + PG8_SB(b, h) + boff + n * 2048 + k * 1024); } while (0)
; #define PG8_MMA(ai, bj, At, Bt) do { __builtin_amdgcn_s_setprio(1); _Pragma("unroll") for (int m = 0; m < 4; ++m) _Pragma("unroll") for (int n = 0; n < 2; ++n) _Pragma("unroll") for (int k = 0; k < 2; ++k) \
;         acc[ai][bj][m][n] = __builtin_amdgcn_mfma_f32_16x16x32_bf16(Bt[n][k], At[m][k], acc[ai][bj][m][n], 0, 0, 0); __builtin_amdgcn_s_setprio(0); } while (0)
; #define PG8_WAIT_V(n) asm volatile("s_waitcnt vmcnt(" #n ")" ::: "memory")
; #define PG8_WAIT_L(n) asm volatile("s_waitcnt lgkmcnt(" #n ")" ::: "memory")
; #define PG8_BAR __builtin_amdgcn_s_barrier()
; #define PG8_SCHED __builtin_amdgcn_sched_barrier(0)
; template <class Epi, class Sched, bool ALIGN_EPI = false, bool SP2 = false>
; __device__ __forceinline__ void gemm_phase(PG8_LAS unsigned char* lds, const Gemm g, const Sched& S, const Epi& E, const int wave0) {
;     ...
;             PG8_WAIT_V(8); PG8_WAIT_L(0); PG8_BAR; PG8_MMA(1, 0, At, B0); PG8_MMA(1, 1, At, B1); PG8_BAR; PG8_SCHED;
;             PG8_LDB(B0, 1, 0); PG8_LDB(B1, 1, 1); PG8_SCHED; PG8_LDA(At, 1, 0); PG8_STAGE(PG8_SA(0, 1), a2 + hstepA, voffA);
;             PG8_WAIT_V(8); PG8_WAIT_L(0); PG8_BAR; PG8_MMA(0, 0, At, B0); PG8_MMA(0, 1, At, B1); PG8_BAR; PG8_SCHED;
	s_setprio 1
	s_waitcnt lgkmcnt(0)
	v_mfma_f32_16x16x32_bf16 v[62:65], v[142:145], v[178:181], v[62:65]
	v_mfma_f32_16x16x32_bf16 v[58:61], v[150:153], v[178:181], v[58:61]
	v_mfma_f32_16x16x32_bf16 v[46:49], v[142:145], v[186:189], v[46:49]
	v_mfma_f32_16x16x32_bf16 v[42:45], v[150:153], v[186:189], v[42:45]
	v_mfma_f32_16x16x32_bf16 v[30:33], v[142:145], v[194:197], v[30:33]
	v_mfma_f32_16x16x32_bf16 v[26:29], v[150:153], v[194:197], v[26:29]
	v_mfma_f32_16x16x32_bf16 v[14:17], v[142:145], v[202:205], v[14:17]
	v_mfma_f32_16x16x32_bf16 v[10:13], v[150:153], v[202:205], v[10:13]
	v_mfma_f32_16x16x32_bf16 v[62:65], v[146:149], v[182:185], v[62:65]
	v_mfma_f32_16x16x32_bf16 v[58:61], v[158:161], v[182:185], v[58:61]
	v_mfma_f32_16x16x32_bf16 v[46:49], v[146:149], v[190:193], v[46:49]
	v_mfma_f32_16x16x32_bf16 v[42:45], v[158:161], v[190:193], v[42:45]
	v_mfma_f32_16x16x32_bf16 v[30:33], v[146:149], v[198:201], v[30:33]
	v_mfma_f32_16x16x32_bf16 v[26:29], v[158:161], v[198:201], v[26:29]
	v_mfma_f32_16x16x32_bf16 v[14:17], v[146:149], v[224:227], v[14:17]
	v_mfma_f32_16x16x32_bf16 v[10:13], v[158:161], v[224:227], v[10:13]
	v_mfma_f32_16x16x32_bf16 v[54:57], v[162:165], v[178:181], v[54:57]
	v_mfma_f32_16x16x32_bf16 v[50:53], v[170:173], v[178:181], v[50:53]
	v_mfma_f32_16x16x32_bf16 v[38:41], v[162:165], v[186:189], v[38:41]
	v_mfma_f32_16x16x32_bf16 v[34:37], v[170:173], v[186:189], v[34:37]
	v_mfma_f32_16x16x32_bf16 v[22:25], v[162:165], v[194:197], v[22:25]
	v_mfma_f32_16x16x32_bf16 v[18:21], v[170:173], v[194:197], v[18:21]
	v_mfma_f32_16x16x32_bf16 v[6:9], v[162:165], v[202:205], v[6:9]
	v_mfma_f32_16x16x32_bf16 v[2:5], v[170:173], v[202:205], v[2:5]
	v_mfma_f32_16x16x32_bf16 v[54:57], v[166:169], v[182:185], v[54:57]
	v_mfma_f32_16x16x32_bf16 v[50:53], v[174:177], v[182:185], v[50:53]
	v_mfma_f32_16x16x32_bf16 v[38:41], v[166:169], v[190:193], v[38:41]
	v_mfma_f32_16x16x32_bf16 v[34:37], v[174:177], v[190:193], v[34:37]
	v_mfma_f32_16x16x32_bf16 v[22:25], v[166:169], v[198:201], v[22:25]
	v_mfma_f32_16x16x32_bf16 v[18:21], v[174:177], v[198:201], v[18:21]
	v_mfma_f32_16x16x32_bf16 v[6:9], v[166:169], v[224:227], v[6:9]
	v_mfma_f32_16x16x32_bf16 v[2:5], v[174:177], v[224:227], v[2:5]
	s_setprio 0
	s_barrier
	s_add_i32 s96, 0, 0x18000
	s_add_i32 s97, 0, 0x1c000
	v_add_u32_e32 v158, s96, v154
	v_add_u32_e32 v174, s97, v154
	ds_read_b128 v[142:145], v158
	ds_read_b128 v[146:149], v158 offset:1024
	ds_read_b128 v[150:153], v158 offset:2048
	ds_read_b128 v[158:161], v158 offset:3072
	ds_read_b128 v[162:165], v174
	ds_read_b128 v[166:169], v174 offset:1024
	ds_read_b128 v[170:173], v174 offset:2048
	ds_read_b128 v[174:177], v174 offset:3072
	s_add_u32 s74, s74, s20
	s_addc_u32 s75, s75, s21
	s_mov_b32 m0, s88
	v_lshl_add_u64 v[240:241], s[74:75], 0, v[136:137]
	ds_read_b128 v[178:181], v157 offset:32768
	ds_read_b128 v[182:185], v157 offset:33792
	ds_read_b128 v[186:189], v157 offset:34816
	ds_read_b128 v[190:193], v157 offset:35840
	ds_read_b128 v[194:197], v157 offset:36864
	ds_read_b128 v[198:201], v157 offset:37888
	ds_read_b128 v[202:205], v157 offset:38912
	ds_read_b128 v[224:227], v157 offset:39936
	global_load_lds_dwordx4 v[240:241], off
	v_lshl_add_u64 v[240:241], s[74:75], 0, v[132:133]
	s_mov_b32 m0, s89
	s_nop 0
	global_load_lds_dwordx4 v[240:241], off
	s_waitcnt vmcnt(8)
	s_waitcnt lgkmcnt(0)
	s_barrier
	s_setprio 1
	s_waitcnt lgkmcnt(0)
	v_mfma_f32_16x16x32_bf16 v[126:129], v[142:145], v[178:181], v[126:129]
	v_mfma_f32_16x16x32_bf16 v[122:125], v[150:153], v[178:181], v[122:125]
	v_mfma_f32_16x16x32_bf16 v[110:113], v[142:145], v[186:189], v[110:113]
	v_mfma_f32_16x16x32_bf16 v[106:109], v[150:153], v[186:189], v[106:109]
	v_mfma_f32_16x16x32_bf16 v[94:97], v[142:145], v[194:197], v[94:97]
	v_mfma_f32_16x16x32_bf16 v[90:93], v[150:153], v[194:197], v[90:93]
	v_mfma_f32_16x16x32_bf16 v[78:81], v[142:145], v[202:205], v[78:81]
	v_mfma_f32_16x16x32_bf16 v[74:77], v[150:153], v[202:205], v[74:77]
	v_mfma_f32_16x16x32_bf16 v[126:129], v[146:149], v[182:185], v[126:129]
	v_mfma_f32_16x16x32_bf16 v[122:125], v[158:161], v[182:185], v[122:125]
	v_mfma_f32_16x16x32_bf16 v[110:113], v[146:149], v[190:193], v[110:113]
	v_mfma_f32_16x16x32_bf16 v[106:109], v[158:161], v[190:193], v[106:109]
	v_mfma_f32_16x16x32_bf16 v[94:97], v[146:149], v[198:201], v[94:97]
	v_mfma_f32_16x16x32_bf16 v[90:93], v[158:161], v[198:201], v[90:93]
	v_mfma_f32_16x16x32_bf16 v[78:81], v[146:149], v[224:227], v[78:81]
	v_mfma_f32_16x16x32_bf16 v[74:77], v[158:161], v[224:227], v[74:77]
	v_mfma_f32_16x16x32_bf16 v[118:121], v[162:165], v[178:181], v[118:121]
	v_mfma_f32_16x16x32_bf16 v[114:117], v[170:173], v[178:181], v[114:117]
	v_mfma_f32_16x16x32_bf16 v[102:105], v[162:165], v[186:189], v[102:105]
	v_mfma_f32_16x16x32_bf16 v[98:101], v[170:173], v[186:189], v[98:101]
	v_mfma_f32_16x16x32_bf16 v[86:89], v[162:165], v[194:197], v[86:89]
	v_mfma_f32_16x16x32_bf16 v[82:85], v[170:173], v[194:197], v[82:85]
	v_mfma_f32_16x16x32_bf16 v[70:73], v[162:165], v[202:205], v[70:73]
	v_mfma_f32_16x16x32_bf16 v[66:69], v[170:173], v[202:205], v[66:69]
	v_mfma_f32_16x16x32_bf16 v[118:121], v[166:169], v[182:185], v[118:121]
	v_mfma_f32_16x16x32_bf16 v[114:117], v[174:177], v[182:185], v[114:117]
	v_mfma_f32_16x16x32_bf16 v[102:105], v[166:169], v[190:193], v[102:105]
	v_mfma_f32_16x16x32_bf16 v[98:101], v[174:177], v[190:193], v[98:101]
	v_mfma_f32_16x16x32_bf16 v[86:89], v[166:169], v[198:201], v[86:89]
	v_mfma_f32_16x16x32_bf16 v[82:85], v[174:177], v[198:201], v[82:85]
	v_mfma_f32_16x16x32_bf16 v[70:73], v[166:169], v[224:227], v[70:73]
	v_mfma_f32_16x16x32_bf16 v[66:69], v[174:177], v[224:227], v[66:69]
	s_setprio 0
	s_barrier
; #define PG8_STAGE(bufoff, gbase, voff) do { _Pragma("unroll") for (int _i = 0; _i < 2; ++_i) \
;         __builtin_amdgcn_global_load_lds((const unsigned*)((const char*)(gbase) + (voff)[_i]), (PG8_LAS unsigned*)(lds + (bufoff) + ldsw + _i * 8192), 16, 0, 0); } while (0)
; #define PG8_LDA(dst, b, h) do { _Pragma("unroll") for (int m = 0; m < 4; ++m) _Pragma("unroll") for (int k = 0; k < 2; ++k) dst[m][k] = *(const PG8_LAS bf16x8*)(lds + PG8_SA(b, h) + aoff + m * 2048 + k * 1024); } while (0)
; #define PG8_MMA(ai, bj, At, Bt) do { __builtin_amdgcn_s_setprio(1); _Pragma("unroll") for (int m = 0; m < 4; ++m) _Pragma("unroll") for (int n = 0; n < 2; ++n) _Pragma("unroll") for (int k = 0; k < 2; ++k) \
;         acc[ai][bj][m][n] = __builtin_amdgcn_mfma_f32_16x16x32_bf16(Bt[n][k], At[m][k], acc[ai][bj][m][n], 0, 0, 0); __builtin_amdgcn_s_setprio(0); } while (0)
; #define PG8_WAIT_V(n) asm volatile("s_waitcnt vmcnt(" #n ")" ::: "memory")
; #define PG8_WAIT_L(n) asm volatile("s_waitcnt lgkmcnt(" #n ")" ::: "memory")
; #define PG8_BAR __builtin_amdgcn_s_barrier()
; #define PG8_SCHED __builtin_amdgcn_sched_barrier(0)
; template <class Epi, class Sched, bool ALIGN_EPI = false, bool SP2 = false>
; __device__ __forceinline__ void gemm_phase(PG8_LAS unsigned char* lds, const Gemm g, const Sched& S, const Epi& E, const int wave0) {
;     ...
;             PG8_LDA(At, 1, 1); PG8_STAGE(PG8_SB(1, 0), b3, voffB); PG8_STAGE(PG8_SB(1, 1), b3 + hstepB, voffB); PG8_STAGE(PG8_SA(1, 0), a3, voffA);
;             PG8_WAIT_V(8); PG8_WAIT_L(0); PG8_BAR; PG8_MMA(1, 0, At, B0); PG8_MMA(1, 1, At, B1); PG8_BAR; PG8_SCHED;
	s_add_i32 s74, s96, s5
	v_lshl_add_u64 v[206:207], v[206:207], 0, s[64:65]
	s_mov_b32 m0, s74
	ds_read_b128 v[178:181], v157 offset:49152
	ds_read_b128 v[182:185], v157 offset:50176
	ds_read_b128 v[186:189], v157 offset:51200
	ds_read_b128 v[190:193], v157 offset:52224
	ds_read_b128 v[194:197], v157 offset:53248
	ds_read_b128 v[198:201], v157 offset:54272
	ds_read_b128 v[202:205], v157 offset:55296
	ds_read_b128 v[224:227], v157 offset:56320
	global_load_lds_dwordx4 v[206:207], off
	v_lshl_add_u64 v[206:207], v[228:229], 0, s[64:65]
	s_add_i32 m0, s74, 0x2000
	s_add_i32 s74, s97, s5
	global_load_lds_dwordx4 v[206:207], off
	v_lshl_add_u64 v[206:207], v[230:231], 0, s[64:65]
	s_mov_b32 m0, s74
	s_nop 0
	global_load_lds_dwordx4 v[206:207], off
	v_lshl_add_u64 v[206:207], v[232:233], 0, s[64:65]
	s_add_i32 m0, s74, 0x2000
	s_nop 0
	global_load_lds_dwordx4 v[206:207], off
	v_lshl_add_u64 v[206:207], v[234:235], 0, s[64:65]
	s_mov_b32 m0, s82
	s_nop 0
	global_load_lds_dwordx4 v[206:207], off
	v_lshl_add_u64 v[206:207], v[238:239], 0, s[64:65]
	s_mov_b32 m0, s90
	s_nop 0
	global_load_lds_dwordx4 v[206:207], off
	s_waitcnt vmcnt(8)
	s_waitcnt lgkmcnt(0)
	s_barrier
	s_setprio 1
	s_waitcnt lgkmcnt(0)
	v_mfma_f32_16x16x32_bf16 v[62:65], v[142:145], v[178:181], v[62:65]
	v_mfma_f32_16x16x32_bf16 v[58:61], v[150:153], v[178:181], v[58:61]
	v_mfma_f32_16x16x32_bf16 v[46:49], v[142:145], v[186:189], v[46:49]
	v_mfma_f32_16x16x32_bf16 v[42:45], v[150:153], v[186:189], v[42:45]
	v_mfma_f32_16x16x32_bf16 v[30:33], v[142:145], v[194:197], v[30:33]
	v_mfma_f32_16x16x32_bf16 v[26:29], v[150:153], v[194:197], v[26:29]
	v_mfma_f32_16x16x32_bf16 v[14:17], v[142:145], v[202:205], v[14:17]
	v_mfma_f32_16x16x32_bf16 v[10:13], v[150:153], v[202:205], v[10:13]
	v_mfma_f32_16x16x32_bf16 v[62:65], v[146:149], v[182:185], v[62:65]
	v_mfma_f32_16x16x32_bf16 v[58:61], v[158:161], v[182:185], v[58:61]
	v_mfma_f32_16x16x32_bf16 v[46:49], v[146:149], v[190:193], v[46:49]
	v_mfma_f32_16x16x32_bf16 v[42:45], v[158:161], v[190:193], v[42:45]
	v_mfma_f32_16x16x32_bf16 v[30:33], v[146:149], v[198:201], v[30:33]
	v_mfma_f32_16x16x32_bf16 v[26:29], v[158:161], v[198:201], v[26:29]
	v_mfma_f32_16x16x32_bf16 v[14:17], v[146:149], v[224:227], v[14:17]
	v_mfma_f32_16x16x32_bf16 v[10:13], v[158:161], v[224:227], v[10:13]
	v_mfma_f32_16x16x32_bf16 v[54:57], v[162:165], v[178:181], v[54:57]
	v_mfma_f32_16x16x32_bf16 v[50:53], v[170:173], v[178:181], v[50:53]
	v_mfma_f32_16x16x32_bf16 v[38:41], v[162:165], v[186:189], v[38:41]
	v_mfma_f32_16x16x32_bf16 v[34:37], v[170:173], v[186:189], v[34:37]
	v_mfma_f32_16x16x32_bf16 v[22:25], v[162:165], v[194:197], v[22:25]
	v_mfma_f32_16x16x32_bf16 v[18:21], v[170:173], v[194:197], v[18:21]
	v_mfma_f32_16x16x32_bf16 v[6:9], v[162:165], v[202:205], v[6:9]
	v_mfma_f32_16x16x32_bf16 v[2:5], v[170:173], v[202:205], v[2:5]
	v_mfma_f32_16x16x32_bf16 v[54:57], v[166:169], v[182:185], v[54:57]
	v_mfma_f32_16x16x32_bf16 v[50:53], v[174:177], v[182:185], v[50:53]
	v_mfma_f32_16x16x32_bf16 v[38:41], v[166:169], v[190:193], v[38:41]
	v_mfma_f32_16x16x32_bf16 v[34:37], v[174:177], v[190:193], v[34:37]
	v_mfma_f32_16x16x32_bf16 v[22:25], v[166:169], v[198:201], v[22:25]
	v_mfma_f32_16x16x32_bf16 v[18:21], v[174:177], v[198:201], v[18:21]
	v_mfma_f32_16x16x32_bf16 v[6:9], v[166:169], v[224:227], v[6:9]
	v_mfma_f32_16x16x32_bf16 v[2:5], v[174:177], v[224:227], v[2:5]
	s_setprio 0
	s_barrier
	s_add_u32 s59, s59, 0x100
	s_addc_u32 s84, s84, 0
	s_add_u32 s38, s38, 0x100
	s_addc_u32 s39, s39, 0
	s_cmp_ge_i32 s94, s91
	s_mov_b32 s74, s94
	s_cbranch_scc0 .LBB0_187

; #define PG8_STAGE(bufoff, gbase, voff) do { _Pragma("unroll") for (int _i = 0; _i < 2; ++_i) \
;         __builtin_amdgcn_global_load_lds((const unsigned*)((const char*)(gbase) + (voff)[_i]), (PG8_LAS unsigned*)(lds + (bufoff) + ldsw + _i * 8192), 16, 0, 0); } while (0)
; #define PG8_LDA(dst, b, h) do { _Pragma("unroll") for (int m = 0; m < 4; ++m) _Pragma("unroll") for (int k = 0; k < 2; ++k) dst[m][k] = *(const PG8_LAS bf16x8*)(lds + PG8_SA(b, h) + aoff + m * 2048 + k * 1024); } while (0)
; #define PG8_LDB(dst, b, h) do { _Pragma("unroll") for (int n = 0; n < 2; ++n) _Pragma("unroll") for (int k = 0; k < 2; ++k) dst[n][k] = *(const PG8_LAS bf16x8*)(lds + PG8_SB(b, h) + boff + n * 2048 + k * 1024); } while (0)
; #define PG8_MMA(ai, bj, At, Bt) do { __builtin_amdgcn_s_setprio(1); _Pragma("unroll") for (int m = 0; m < 4; ++m) _Pragma("unroll") for (int n = 0; n < 2; ++n) _Pragma("unroll") for (int k = 0; k < 2; ++k) \
;         acc[ai][bj][m][n] = __builtin_amdgcn_mfma_f32_16x16x32_bf16(Bt[n][k], At[m][k], acc[ai][bj][m][n], 0, 0, 0); __builtin_amdgcn_s_setprio(0); } while (0)
; #define PG8_WAIT_V(n) asm volatile("s_waitcnt vmcnt(" #n ")" ::: "memory")
; #define PG8_BAR __builtin_amdgcn_s_barrier()
; template <class Epi, class Sched, bool ALIGN_EPI = false, bool SP2 = false>
; __device__ __forceinline__ void gemm_phase(PG8_LAS unsigned char* lds, const Gemm g, const Sched& S, const Epi& E, const int wave0) {
;     ...
;         for (int t = 0; t < nt; t += 2) {
;             const bool last = (t == nt - 2);
;             const char* a1 = cA + (size_t)(t + 1) * kstep;
;             const char* a2 = last ? nA : cA + (size_t)(t + 2) * kstep; const char* b2 = last ? nB : cB + (size_t)(t + 2) * kstep;
;             const char* a3 = a2 + kstep; const char* b3 = b2 + kstep;
;             if (last && has_next) S.a_ready(nxt);
;             if constexpr (SP2) {
;             PG8_LDB(B0, 0, 0); PG8_LDB(B1, 0, 1); PG8_SCHED; PG8_LDA(At, 0, 0); PG8_STAGE(PG8_SA(1, 1), a1 + hstepA, voffA);
;             PG8_WAIT_V(8); PG8_WAIT_L(0); PG8_BAR; PG8_MMA(0, 0, At, B0); PG8_MMA(0, 1, At, B1); PG8_BAR; PG8_SCHED;
;             PG8_LDA(At, 0, 1); PG8_STAGE(PG8_SB(0, 0), b2, voffB); PG8_STAGE(PG8_SB(0, 1), b2 + hstepB, voffB); PG8_STAGE(PG8_SA(0, 0), a2, voffA);
;             PG8_WAIT_V(8); PG8_WAIT_L(0); PG8_BAR; PG8_MMA(1, 0, At, B0); PG8_MMA(1, 1, At, B1); PG8_BAR; PG8_SCHED;
.LBB0_568:
	s_add_i32 s72, s40, 2
	s_add_u32 s73, s38, 0x80
	s_addc_u32 s41, s39, 0
	s_add_i32 s77, 0, 0x10000
	s_cmp_eq_u32 s95, s40
	s_cselect_b32 s41, s61, s41
	s_cselect_b32 s40, s60, s73
	s_cselect_b32 vcc_hi, s71, s76
	s_cselect_b32 vcc_lo, s70, s75
	s_add_i32 s73, 0, 0x14000
	v_add_u32_e32 v86, s77, v164
	v_add_u32_e32 v162, s73, v164
	ds_read_b128 v[74:77], v86
	ds_read_b128 v[78:81], v86 offset:1024
	ds_read_b128 v[82:85], v86 offset:2048
	ds_read_b128 v[86:89], v86 offset:3072
	ds_read_b128 v[158:161], v162
	ds_read_b128 v[168:171], v162 offset:1024
	ds_read_b128 v[172:175], v162 offset:2048
	ds_read_b128 v[176:179], v162 offset:3072
	v_lshl_add_u64 v[162:163], s[38:39], 0, v[156:157]
	s_add_i32 m0, s91, 0xc000
	ds_read_b128 v[180:183], v166
	ds_read_b128 v[184:187], v166 offset:1024
	ds_read_b128 v[188:191], v166 offset:2048
	ds_read_b128 v[192:195], v166 offset:3072
	ds_read_b128 v[196:199], v166 offset:4096
	ds_read_b128 v[200:203], v166 offset:5120
	ds_read_b128 v[204:207], v166 offset:6144
	ds_read_b128 v[224:227], v166 offset:7168
	global_load_lds_dwordx4 v[162:163], off
	v_lshl_add_u64 v[162:163], s[38:39], 0, v[154:155]
	s_add_i32 m0, s91, 0xe000
	s_nop 0
	global_load_lds_dwordx4 v[162:163], off
	s_waitcnt vmcnt(8)
	s_waitcnt lgkmcnt(0)
	s_barrier
	s_setprio 1
	s_waitcnt lgkmcnt(0)
	v_mfma_f32_16x16x32_bf16 v[142:145], v[74:77], v[180:183], v[142:145]
	v_mfma_f32_16x16x32_bf16 v[138:141], v[82:85], v[180:183], v[138:141]
	v_mfma_f32_16x16x32_bf16 v[126:129], v[74:77], v[188:191], v[126:129]
	v_mfma_f32_16x16x32_bf16 v[122:125], v[82:85], v[188:191], v[122:125]
	v_mfma_f32_16x16x32_bf16 v[110:113], v[74:77], v[196:199], v[110:113]
	v_mfma_f32_16x16x32_bf16 v[106:109], v[82:85], v[196:199], v[106:109]
	v_mfma_f32_16x16x32_bf16 v[94:97], v[74:77], v[204:207], v[94:97]
	v_mfma_f32_16x16x32_bf16 v[90:93], v[82:85], v[204:207], v[90:93]
	v_mfma_f32_16x16x32_bf16 v[142:145], v[78:81], v[184:187], v[142:145]
	v_mfma_f32_16x16x32_bf16 v[138:141], v[86:89], v[184:187], v[138:141]
	v_mfma_f32_16x16x32_bf16 v[126:129], v[78:81], v[192:195], v[126:129]
	v_mfma_f32_16x16x32_bf16 v[122:125], v[86:89], v[192:195], v[122:125]
	v_mfma_f32_16x16x32_bf16 v[110:113], v[78:81], v[200:203], v[110:113]
	v_mfma_f32_16x16x32_bf16 v[106:109], v[86:89], v[200:203], v[106:109]
	v_mfma_f32_16x16x32_bf16 v[94:97], v[78:81], v[224:227], v[94:97]
	v_mfma_f32_16x16x32_bf16 v[90:93], v[86:89], v[224:227], v[90:93]
	v_mfma_f32_16x16x32_bf16 v[134:137], v[158:161], v[180:183], v[134:137]
	v_mfma_f32_16x16x32_bf16 v[130:133], v[172:175], v[180:183], v[130:133]
	v_mfma_f32_16x16x32_bf16 v[118:121], v[158:161], v[188:191], v[118:121]
	v_mfma_f32_16x16x32_bf16 v[114:117], v[172:175], v[188:191], v[114:117]
	v_mfma_f32_16x16x32_bf16 v[102:105], v[158:161], v[196:199], v[102:105]
	v_mfma_f32_16x16x32_bf16 v[98:101], v[172:175], v[196:199], v[98:101]
	v_mfma_f32_16x16x32_bf16 v[70:73], v[158:161], v[204:207], v[70:73]
	v_mfma_f32_16x16x32_bf16 v[66:69], v[172:175], v[204:207], v[66:69]
	v_mfma_f32_16x16x32_bf16 v[134:137], v[168:171], v[184:187], v[134:137]
	v_mfma_f32_16x16x32_bf16 v[130:133], v[176:179], v[184:187], v[130:133]
	v_mfma_f32_16x16x32_bf16 v[118:121], v[168:171], v[192:195], v[118:121]
	v_mfma_f32_16x16x32_bf16 v[114:117], v[176:179], v[192:195], v[114:117]
	v_mfma_f32_16x16x32_bf16 v[102:105], v[168:171], v[200:203], v[102:105]
	v_mfma_f32_16x16x32_bf16 v[98:101], v[176:179], v[200:203], v[98:101]
	v_mfma_f32_16x16x32_bf16 v[70:73], v[168:171], v[224:227], v[70:73]
	v_mfma_f32_16x16x32_bf16 v[66:69], v[176:179], v[224:227], v[66:69]
	s_setprio 0
	s_barrier
	s_add_i32 s77, s77, s82
	v_lshl_add_u64 v[162:163], vcc, 0, v[150:151]
	s_mov_b32 m0, s77
	ds_read_b128 v[180:183], v166 offset:16384
	ds_read_b128 v[184:187], v166 offset:17408
	ds_read_b128 v[188:191], v166 offset:18432
	ds_read_b128 v[192:195], v166 offset:19456
	ds_read_b128 v[196:199], v166 offset:20480
	ds_read_b128 v[200:203], v166 offset:21504
	ds_read_b128 v[204:207], v166 offset:22528
	ds_read_b128 v[224:227], v166 offset:23552
	global_load_lds_dwordx4 v[162:163], off
	s_add_i32 m0, s77, 0x2000
	v_lshl_add_u64 v[228:229], vcc, 0, v[146:147]
	s_add_u32 vcc_lo, vcc_lo, s42
	s_addc_u32 vcc_hi, vcc_hi, s43
	s_add_i32 s73, s73, s82
	global_load_lds_dwordx4 v[228:229], off
	v_lshl_add_u64 v[230:231], vcc, 0, v[150:151]
	s_mov_b32 m0, s73
	v_lshl_add_u64 v[232:233], vcc, 0, v[146:147]
	global_load_lds_dwordx4 v[230:231], off
	s_add_i32 m0, s73, 0x2000
	v_lshl_add_u64 v[234:235], s[40:41], 0, v[152:153]
	global_load_lds_dwordx4 v[232:233], off
	s_mov_b32 m0, s91
	v_lshl_add_u64 v[238:239], s[40:41], 0, v[148:149]
	global_load_lds_dwordx4 v[234:235], off
	s_mov_b32 m0, s92
	s_nop 0
	global_load_lds_dwordx4 v[238:239], off
	s_waitcnt vmcnt(8)
	s_waitcnt lgkmcnt(0)
	s_barrier
; #define PG8_STAGE(bufoff, gbase, voff) do { _Pragma("unroll") for (int _i = 0; _i < 2; ++_i) \
;         __builtin_amdgcn_global_load_lds((const unsigned*)((const char*)(gbase) + (voff)[_i]), (PG8_LAS unsigned*)(lds + (bufoff) + ldsw + _i * 8192), 16, 0, 0); } while (0)
; #define PG8_LDA(dst, b, h) do { _Pragma("unroll") for (int m = 0; m < 4; ++m) _Pragma("unroll") for (int k = 0; k < 2; ++k) dst[m][k] = *(const PG8_LAS bf16x8*)(lds + PG8_SA(b, h) + aoff + m * 2048 + k * 1024); } while (0)
; #define PG8_LDB(dst, b, h) do { _Pragma("unroll") for (int n = 0; n < 2; ++n) _Pragma("unroll") for (int k = 0; k < 2; ++k) dst[n][k] = *(const PG8_LAS bf16x8*)(lds + PG8_SB(b, h) + boff + n * 2048 + k * 1024); } while (0)
; #define PG8_MMA(ai, bj, At, Bt) do { __builtin_amdgcn_s_setprio(1); _Pragma("unroll") for (int m = 0; m < 4; ++m) _Pragma("unroll") for (int n = 0; n < 2; ++n) _Pragma("unroll") for (int k = 0; k < 2; ++k) \
;         acc[ai][bj][m][n] = __builtin_amdgcn_mfma_f32_16x16x32_bf16(Bt[n][k], At[m][k], acc[ai][bj][m][n], 0, 0, 0); __builtin_amdgcn_s_setprio(0); } while (0)
; #define PG8_WAIT_V(n) asm volatile("s_waitcnt vmcnt(" #n ")" ::: "memory")
; #define PG8_WAIT_L(n) asm volatile("s_waitcnt lgkmcnt(" #n ")" ::: "memory")
; #define PG8_BAR __builtin_amdgcn_s_barrier()
; #define PG8_SCHED __builtin_amdgcn_sched_barrier(0)
; template <class Epi, class Sched, bool ALIGN_EPI = false, bool SP2 = false>
; __device__ __forceinline__ void gemm_phase(PG8_LAS unsigned char* lds, const Gemm g, const Sched& S, const Epi& E, const int wave0) {
;     ...
;             PG8_WAIT_V(8); PG8_WAIT_L(0); PG8_BAR; PG8_MMA(1, 0, At, B0); PG8_MMA(1, 1, At, B1); PG8_BAR; PG8_SCHED;
;             PG8_LDB(B0, 1, 0); PG8_LDB(B1, 1, 1); PG8_SCHED; PG8_LDA(At, 1, 0); PG8_STAGE(PG8_SA(0, 1), a2 + hstepA, voffA);
;             PG8_WAIT_V(8); PG8_WAIT_L(0); PG8_BAR; PG8_MMA(0, 0, At, B0); PG8_MMA(0, 1, At, B1); PG8_BAR; PG8_SCHED;
	s_setprio 1
	s_waitcnt lgkmcnt(0)
	v_mfma_f32_16x16x32_bf16 v[62:65], v[74:77], v[180:183], v[62:65]
	v_mfma_f32_16x16x32_bf16 v[58:61], v[82:85], v[180:183], v[58:61]
	v_mfma_f32_16x16x32_bf16 v[46:49], v[74:77], v[188:191], v[46:49]
	v_mfma_f32_16x16x32_bf16 v[42:45], v[82:85], v[188:191], v[42:45]
	v_mfma_f32_16x16x32_bf16 v[30:33], v[74:77], v[196:199], v[30:33]
	v_mfma_f32_16x16x32_bf16 v[26:29], v[82:85], v[196:199], v[26:29]
	v_mfma_f32_16x16x32_bf16 v[14:17], v[74:77], v[204:207], v[14:17]
	v_mfma_f32_16x16x32_bf16 v[10:13], v[82:85], v[204:207], v[10:13]
	v_mfma_f32_16x16x32_bf16 v[62:65], v[78:81], v[184:187], v[62:65]
	v_mfma_f32_16x16x32_bf16 v[58:61], v[86:89], v[184:187], v[58:61]
	v_mfma_f32_16x16x32_bf16 v[46:49], v[78:81], v[192:195], v[46:49]
	v_mfma_f32_16x16x32_bf16 v[42:45], v[86:89], v[192:195], v[42:45]
	v_mfma_f32_16x16x32_bf16 v[30:33], v[78:81], v[200:203], v[30:33]
	v_mfma_f32_16x16x32_bf16 v[26:29], v[86:89], v[200:203], v[26:29]
	v_mfma_f32_16x16x32_bf16 v[14:17], v[78:81], v[224:227], v[14:17]
	v_mfma_f32_16x16x32_bf16 v[10:13], v[86:89], v[224:227], v[10:13]
	v_mfma_f32_16x16x32_bf16 v[54:57], v[158:161], v[180:183], v[54:57]
	v_mfma_f32_16x16x32_bf16 v[50:53], v[172:175], v[180:183], v[50:53]
	v_mfma_f32_16x16x32_bf16 v[38:41], v[158:161], v[188:191], v[38:41]
	v_mfma_f32_16x16x32_bf16 v[34:37], v[172:175], v[188:191], v[34:37]
	v_mfma_f32_16x16x32_bf16 v[22:25], v[158:161], v[196:199], v[22:25]
	v_mfma_f32_16x16x32_bf16 v[18:21], v[172:175], v[196:199], v[18:21]
	v_mfma_f32_16x16x32_bf16 v[6:9], v[158:161], v[204:207], v[6:9]
	v_mfma_f32_16x16x32_bf16 v[2:5], v[172:175], v[204:207], v[2:5]
	v_mfma_f32_16x16x32_bf16 v[54:57], v[168:171], v[184:187], v[54:57]
	v_mfma_f32_16x16x32_bf16 v[50:53], v[176:179], v[184:187], v[50:53]
	v_mfma_f32_16x16x32_bf16 v[38:41], v[168:171], v[192:195], v[38:41]
	v_mfma_f32_16x16x32_bf16 v[34:37], v[176:179], v[192:195], v[34:37]
	v_mfma_f32_16x16x32_bf16 v[22:25], v[168:171], v[200:203], v[22:25]
	v_mfma_f32_16x16x32_bf16 v[18:21], v[176:179], v[200:203], v[18:21]
	v_mfma_f32_16x16x32_bf16 v[6:9], v[168:171], v[224:227], v[6:9]
	v_mfma_f32_16x16x32_bf16 v[2:5], v[176:179], v[224:227], v[2:5]
	s_setprio 0
	s_barrier
	s_add_i32 s73, 0, 0x18000
	s_add_i32 s77, 0, 0x1c000
	v_add_u32_e32 v86, s73, v164
	v_add_u32_e32 v167, s77, v164
	ds_read_b128 v[74:77], v86
	ds_read_b128 v[78:81], v86 offset:1024
	ds_read_b128 v[82:85], v86 offset:2048
	ds_read_b128 v[86:89], v86 offset:3072
	ds_read_b128 v[158:161], v167
	ds_read_b128 v[168:171], v167 offset:1024
	ds_read_b128 v[172:175], v167 offset:2048
	ds_read_b128 v[176:179], v167 offset:3072
	s_add_u32 s40, s40, s22
	s_addc_u32 s41, s41, s23
	s_mov_b32 m0, s93
	v_lshl_add_u64 v[240:241], s[40:41], 0, v[152:153]
	ds_read_b128 v[180:183], v166 offset:32768
	ds_read_b128 v[184:187], v166 offset:33792
	ds_read_b128 v[188:191], v166 offset:34816
	ds_read_b128 v[192:195], v166 offset:35840
	ds_read_b128 v[196:199], v166 offset:36864
	ds_read_b128 v[200:203], v166 offset:37888
	ds_read_b128 v[204:207], v166 offset:38912
	ds_read_b128 v[224:227], v166 offset:39936
	global_load_lds_dwordx4 v[240:241], off
	v_lshl_add_u64 v[240:241], s[40:41], 0, v[148:149]
	s_mov_b32 m0, s94
	s_nop 0
	global_load_lds_dwordx4 v[240:241], off
	s_waitcnt vmcnt(8)
	s_waitcnt lgkmcnt(0)
	s_barrier
	s_setprio 1
	s_waitcnt lgkmcnt(0)
	v_mfma_f32_16x16x32_bf16 v[142:145], v[74:77], v[180:183], v[142:145]
	v_mfma_f32_16x16x32_bf16 v[138:141], v[82:85], v[180:183], v[138:141]
	v_mfma_f32_16x16x32_bf16 v[126:129], v[74:77], v[188:191], v[126:129]
	v_mfma_f32_16x16x32_bf16 v[122:125], v[82:85], v[188:191], v[122:125]
	v_mfma_f32_16x16x32_bf16 v[110:113], v[74:77], v[196:199], v[110:113]
	v_mfma_f32_16x16x32_bf16 v[106:109], v[82:85], v[196:199], v[106:109]
	v_mfma_f32_16x16x32_bf16 v[94:97], v[74:77], v[204:207], v[94:97]
	v_mfma_f32_16x16x32_bf16 v[90:93], v[82:85], v[204:207], v[90:93]
	v_mfma_f32_16x16x32_bf16 v[142:145], v[78:81], v[184:187], v[142:145]
	v_mfma_f32_16x16x32_bf16 v[138:141], v[86:89], v[184:187], v[138:141]
	v_mfma_f32_16x16x32_bf16 v[126:129], v[78:81], v[192:195], v[126:129]
	v_mfma_f32_16x16x32_bf16 v[122:125], v[86:89], v[192:195], v[122:125]
	v_mfma_f32_16x16x32_bf16 v[110:113], v[78:81], v[200:203], v[110:113]
	v_mfma_f32_16x16x32_bf16 v[106:109], v[86:89], v[200:203], v[106:109]
	v_mfma_f32_16x16x32_bf16 v[94:97], v[78:81], v[224:227], v[94:97]
	v_mfma_f32_16x16x32_bf16 v[90:93], v[86:89], v[224:227], v[90:93]
	v_mfma_f32_16x16x32_bf16 v[134:137], v[158:161], v[180:183], v[134:137]
	v_mfma_f32_16x16x32_bf16 v[130:133], v[172:175], v[180:183], v[130:133]
	v_mfma_f32_16x16x32_bf16 v[118:121], v[158:161], v[188:191], v[118:121]
	v_mfma_f32_16x16x32_bf16 v[114:117], v[172:175], v[188:191], v[114:117]
	v_mfma_f32_16x16x32_bf16 v[102:105], v[158:161], v[196:199], v[102:105]
	v_mfma_f32_16x16x32_bf16 v[98:101], v[172:175], v[196:199], v[98:101]
	v_mfma_f32_16x16x32_bf16 v[70:73], v[158:161], v[204:207], v[70:73]
	v_mfma_f32_16x16x32_bf16 v[66:69], v[172:175], v[204:207], v[66:69]
	v_mfma_f32_16x16x32_bf16 v[134:137], v[168:171], v[184:187], v[134:137]
	v_mfma_f32_16x16x32_bf16 v[130:133], v[176:179], v[184:187], v[130:133]
	v_mfma_f32_16x16x32_bf16 v[118:121], v[168:171], v[192:195], v[118:121]
	v_mfma_f32_16x16x32_bf16 v[114:117], v[176:179], v[192:195], v[114:117]
	v_mfma_f32_16x16x32_bf16 v[102:105], v[168:171], v[200:203], v[102:105]
	v_mfma_f32_16x16x32_bf16 v[98:101], v[176:179], v[200:203], v[98:101]
	v_mfma_f32_16x16x32_bf16 v[70:73], v[168:171], v[224:227], v[70:73]
	v_mfma_f32_16x16x32_bf16 v[66:69], v[176:179], v[224:227], v[66:69]
	s_setprio 0
	s_barrier
; #define PG8_STAGE(bufoff, gbase, voff) do { _Pragma("unroll") for (int _i = 0; _i < 2; ++_i) \
;         __builtin_amdgcn_global_load_lds((const unsigned*)((const char*)(gbase) + (voff)[_i]), (PG8_LAS unsigned*)(lds + (bufoff) + ldsw + _i * 8192), 16, 0, 0); } while (0)
; #define PG8_LDA(dst, b, h) do { _Pragma("unroll") for (int m = 0; m < 4; ++m) _Pragma("unroll") for (int k = 0; k < 2; ++k) dst[m][k] = *(const PG8_LAS bf16x8*)(lds + PG8_SA(b, h) + aoff + m * 2048 + k * 1024); } while (0)
; #define PG8_MMA(ai, bj, At, Bt) do { __builtin_amdgcn_s_setprio(1); _Pragma("unroll") for (int m = 0; m < 4; ++m) _Pragma("unroll") for (int n = 0; n < 2; ++n) _Pragma("unroll") for (int k = 0; k < 2; ++k) \
;         acc[ai][bj][m][n] = __builtin_amdgcn_mfma_f32_16x16x32_bf16(Bt[n][k], At[m][k], acc[ai][bj][m][n], 0, 0, 0); __builtin_amdgcn_s_setprio(0); } while (0)
; #define PG8_WAIT_V(n) asm volatile("s_waitcnt vmcnt(" #n ")" ::: "memory")
; #define PG8_WAIT_L(n) asm volatile("s_waitcnt lgkmcnt(" #n ")" ::: "memory")
; #define PG8_BAR __builtin_amdgcn_s_barrier()
; #define PG8_SCHED __builtin_amdgcn_sched_barrier(0)
; template <class Epi, class Sched, bool ALIGN_EPI = false, bool SP2 = false>
; __device__ __forceinline__ void gemm_phase(PG8_LAS unsigned char* lds, const Gemm g, const Sched& S, const Epi& E, const int wave0) {
;     ...
;             PG8_LDA(At, 1, 1); PG8_STAGE(PG8_SB(1, 0), b3, voffB); PG8_STAGE(PG8_SB(1, 1), b3 + hstepB, voffB); PG8_STAGE(PG8_SA(1, 0), a3, voffA);
;             PG8_WAIT_V(8); PG8_WAIT_L(0); PG8_BAR; PG8_MMA(1, 0, At, B0); PG8_MMA(1, 1, At, B1); PG8_BAR; PG8_SCHED;
	s_add_i32 s40, s73, s82
	v_lshl_add_u64 v[162:163], v[162:163], 0, s[64:65]
	s_mov_b32 m0, s40
	ds_read_b128 v[180:183], v166 offset:49152
	ds_read_b128 v[184:187], v166 offset:50176
	ds_read_b128 v[188:191], v166 offset:51200
	ds_read_b128 v[192:195], v166 offset:52224
	ds_read_b128 v[196:199], v166 offset:53248
	ds_read_b128 v[200:203], v166 offset:54272
	ds_read_b128 v[204:207], v166 offset:55296
	ds_read_b128 v[224:227], v166 offset:56320
	global_load_lds_dwordx4 v[162:163], off
	v_lshl_add_u64 v[162:163], v[228:229], 0, s[64:65]
	s_add_i32 m0, s40, 0x2000
	s_add_i32 s40, s77, s82
	global_load_lds_dwordx4 v[162:163], off
	v_lshl_add_u64 v[162:163], v[230:231], 0, s[64:65]
	s_mov_b32 m0, s40
	s_nop 0
	global_load_lds_dwordx4 v[162:163], off
	v_lshl_add_u64 v[162:163], v[232:233], 0, s[64:65]
	s_add_i32 m0, s40, 0x2000
	s_nop 0
	global_load_lds_dwordx4 v[162:163], off
	v_lshl_add_u64 v[162:163], v[234:235], 0, s[64:65]
	s_mov_b32 m0, s96
	s_nop 0
	global_load_lds_dwordx4 v[162:163], off
	v_lshl_add_u64 v[162:163], v[238:239], 0, s[64:65]
	s_mov_b32 m0, s97
	s_nop 0
	global_load_lds_dwordx4 v[162:163], off
	s_waitcnt vmcnt(8)
	s_waitcnt lgkmcnt(0)
	s_barrier
	s_setprio 1
	s_waitcnt lgkmcnt(0)
	v_mfma_f32_16x16x32_bf16 v[62:65], v[74:77], v[180:183], v[62:65]
	v_mfma_f32_16x16x32_bf16 v[58:61], v[82:85], v[180:183], v[58:61]
	v_mfma_f32_16x16x32_bf16 v[46:49], v[74:77], v[188:191], v[46:49]
	v_mfma_f32_16x16x32_bf16 v[42:45], v[82:85], v[188:191], v[42:45]
	v_mfma_f32_16x16x32_bf16 v[30:33], v[74:77], v[196:199], v[30:33]
	v_mfma_f32_16x16x32_bf16 v[26:29], v[82:85], v[196:199], v[26:29]
	v_mfma_f32_16x16x32_bf16 v[14:17], v[74:77], v[204:207], v[14:17]
	v_mfma_f32_16x16x32_bf16 v[10:13], v[82:85], v[204:207], v[10:13]
	v_mfma_f32_16x16x32_bf16 v[62:65], v[78:81], v[184:187], v[62:65]
	v_mfma_f32_16x16x32_bf16 v[58:61], v[86:89], v[184:187], v[58:61]
	v_mfma_f32_16x16x32_bf16 v[46:49], v[78:81], v[192:195], v[46:49]
	v_mfma_f32_16x16x32_bf16 v[42:45], v[86:89], v[192:195], v[42:45]
	v_mfma_f32_16x16x32_bf16 v[30:33], v[78:81], v[200:203], v[30:33]
	v_mfma_f32_16x16x32_bf16 v[26:29], v[86:89], v[200:203], v[26:29]
	v_mfma_f32_16x16x32_bf16 v[14:17], v[78:81], v[224:227], v[14:17]
	v_mfma_f32_16x16x32_bf16 v[10:13], v[86:89], v[224:227], v[10:13]
	v_mfma_f32_16x16x32_bf16 v[54:57], v[158:161], v[180:183], v[54:57]
	v_mfma_f32_16x16x32_bf16 v[50:53], v[172:175], v[180:183], v[50:53]
	v_mfma_f32_16x16x32_bf16 v[38:41], v[158:161], v[188:191], v[38:41]
	v_mfma_f32_16x16x32_bf16 v[34:37], v[172:175], v[188:191], v[34:37]
	v_mfma_f32_16x16x32_bf16 v[22:25], v[158:161], v[196:199], v[22:25]
	v_mfma_f32_16x16x32_bf16 v[18:21], v[172:175], v[196:199], v[18:21]
	v_mfma_f32_16x16x32_bf16 v[6:9], v[158:161], v[204:207], v[6:9]
	v_mfma_f32_16x16x32_bf16 v[2:5], v[172:175], v[204:207], v[2:5]
	v_mfma_f32_16x16x32_bf16 v[54:57], v[168:171], v[184:187], v[54:57]
	v_mfma_f32_16x16x32_bf16 v[50:53], v[176:179], v[184:187], v[50:53]
	v_mfma_f32_16x16x32_bf16 v[38:41], v[168:171], v[192:195], v[38:41]
	v_mfma_f32_16x16x32_bf16 v[34:37], v[176:179], v[192:195], v[34:37]
	v_mfma_f32_16x16x32_bf16 v[22:25], v[168:171], v[200:203], v[22:25]
	v_mfma_f32_16x16x32_bf16 v[18:21], v[176:179], v[200:203], v[18:21]
	v_mfma_f32_16x16x32_bf16 v[6:9], v[168:171], v[224:227], v[6:9]
	v_mfma_f32_16x16x32_bf16 v[2:5], v[176:179], v[224:227], v[2:5]
	s_setprio 0
	s_barrier
	s_add_u32 s75, s75, 0x100
	s_addc_u32 s76, s76, 0
	s_add_u32 s38, s38, 0x100
	s_addc_u32 s39, s39, 0
	s_cmp_ge_i32 s72, s83
	s_mov_b32 s40, s72
	s_cbranch_scc0 .LBB0_568

; #define PG8_STAGE(bufoff, gbase, voff) do { _Pragma("unroll") for (int _i = 0; _i < 2; ++_i) \
;         __builtin_amdgcn_global_load_lds((const unsigned*)((const char*)(gbase) + (voff)[_i]), (PG8_LAS unsigned*)(lds + (bufoff) + ldsw + _i * 8192), 16, 0, 0); } while (0)
; #define PG8_LDA(dst, b, h) do { _Pragma("unroll") for (int m = 0; m < 4; ++m) _Pragma("unroll") for (int k = 0; k < 2; ++k) dst[m][k] = *(const PG8_LAS bf16x8*)(lds + PG8_SA(b, h) + aoff + m * 2048 + k * 1024); } while (0)
; #define PG8_LDB(dst, b, h) do { _Pragma("unroll") for (int n = 0; n < 2; ++n) _Pragma("unroll") for (int k = 0; k < 2; ++k) dst[n][k] = *(const PG8_LAS bf16x8*)(lds + PG8_SB(b, h) + boff + n * 2048 + k * 1024); } while (0)
; #define PG8_MMA(ai, bj, At, Bt) do { __builtin_amdgcn_s_setprio(1); _Pragma("unroll") for (int m = 0; m < 4; ++m) _Pragma("unroll") for (int n = 0; n < 2; ++n) _Pragma("unroll") for (int k = 0; k < 2; ++k) \
;         acc[ai][bj][m][n] = __builtin_amdgcn_mfma_f32_16x16x32_bf16(Bt[n][k], At[m][k], acc[ai][bj][m][n], 0, 0, 0); __builtin_amdgcn_s_setprio(0); } while (0)
; #define PG8_WAIT_V(n) asm volatile("s_waitcnt vmcnt(" #n ")" ::: "memory")
; #define PG8_BAR __builtin_amdgcn_s_barrier()
; template <class Epi, class Sched, bool ALIGN_EPI = false, bool SP2 = false>
; __device__ __forceinline__ void gemm_phase(PG8_LAS unsigned char* lds, const Gemm g, const Sched& S, const Epi& E, const int wave0) {
;     ...
;         for (int t = 0; t < nt; t += 2) {
;             const bool last = (t == nt - 2);
;             const char* a1 = cA + (size_t)(t + 1) * kstep;
;             const char* a2 = last ? nA : cA + (size_t)(t + 2) * kstep; const char* b2 = last ? nB : cB + (size_t)(t + 2) * kstep;
;             const char* a3 = a2 + kstep; const char* b3 = b2 + kstep;
;             if (last && has_next) S.a_ready(nxt);
;             if constexpr (SP2) {
;             PG8_LDB(B0, 0, 0); PG8_LDB(B1, 0, 1); PG8_SCHED; PG8_LDA(At, 0, 0); PG8_STAGE(PG8_SA(1, 1), a1 + hstepA, voffA);
;             PG8_WAIT_V(8); PG8_WAIT_L(0); PG8_BAR; PG8_MMA(0, 0, At, B0); PG8_MMA(0, 1, At, B1); PG8_BAR; PG8_SCHED;
;             PG8_LDA(At, 0, 1); PG8_STAGE(PG8_SB(0, 0), b2, voffB); PG8_STAGE(PG8_SB(0, 1), b2 + hstepB, voffB); PG8_STAGE(PG8_SA(0, 0), a2, voffA);
;             PG8_WAIT_V(8); PG8_WAIT_L(0); PG8_BAR; PG8_MMA(1, 0, At, B0); PG8_MMA(1, 1, At, B1); PG8_BAR; PG8_SCHED;
.LBB0_665:
	s_add_i32 s70, s42, 2
	s_add_u32 s71, s40, 0x80
	s_addc_u32 s43, s41, 0
	s_add_i32 s97, 0, 0x10000
	s_cmp_eq_u32 s96, s42
	s_cselect_b32 s43, s59, s43
	s_cselect_b32 s42, s58, s71
	s_cselect_b32 s75, s61, s73
	s_cselect_b32 s74, s60, s72
	s_add_i32 s71, 0, 0x14000
	v_add_u32_e32 v86, s97, v164
	v_add_u32_e32 v162, s71, v164
	ds_read_b128 v[74:77], v86
	ds_read_b128 v[78:81], v86 offset:1024
	ds_read_b128 v[82:85], v86 offset:2048
	ds_read_b128 v[86:89], v86 offset:3072
	ds_read_b128 v[158:161], v162
	ds_read_b128 v[168:171], v162 offset:1024
	ds_read_b128 v[172:175], v162 offset:2048
	ds_read_b128 v[176:179], v162 offset:3072
	v_lshl_add_u64 v[162:163], s[40:41], 0, v[156:157]
	s_add_i32 m0, s77, 0xc000
	ds_read_b128 v[180:183], v166
	ds_read_b128 v[184:187], v166 offset:1024
	ds_read_b128 v[188:191], v166 offset:2048
	ds_read_b128 v[192:195], v166 offset:3072
	ds_read_b128 v[196:199], v166 offset:4096
	ds_read_b128 v[200:203], v166 offset:5120
	ds_read_b128 v[204:207], v166 offset:6144
	ds_read_b128 v[224:227], v166 offset:7168
	global_load_lds_dwordx4 v[162:163], off
	v_lshl_add_u64 v[162:163], s[40:41], 0, v[154:155]
	s_add_i32 m0, s77, 0xe000
	s_nop 0
	global_load_lds_dwordx4 v[162:163], off
	s_waitcnt vmcnt(8)
	s_waitcnt lgkmcnt(0)
	s_barrier
	s_setprio 1
	s_waitcnt lgkmcnt(0)
	v_mfma_f32_16x16x32_bf16 v[142:145], v[74:77], v[180:183], v[142:145]
	v_mfma_f32_16x16x32_bf16 v[138:141], v[82:85], v[180:183], v[138:141]
	v_mfma_f32_16x16x32_bf16 v[126:129], v[74:77], v[188:191], v[126:129]
	v_mfma_f32_16x16x32_bf16 v[122:125], v[82:85], v[188:191], v[122:125]
	v_mfma_f32_16x16x32_bf16 v[110:113], v[74:77], v[196:199], v[110:113]
	v_mfma_f32_16x16x32_bf16 v[106:109], v[82:85], v[196:199], v[106:109]
	v_mfma_f32_16x16x32_bf16 v[94:97], v[74:77], v[204:207], v[94:97]
	v_mfma_f32_16x16x32_bf16 v[90:93], v[82:85], v[204:207], v[90:93]
	v_mfma_f32_16x16x32_bf16 v[142:145], v[78:81], v[184:187], v[142:145]
	v_mfma_f32_16x16x32_bf16 v[138:141], v[86:89], v[184:187], v[138:141]
	v_mfma_f32_16x16x32_bf16 v[126:129], v[78:81], v[192:195], v[126:129]
	v_mfma_f32_16x16x32_bf16 v[122:125], v[86:89], v[192:195], v[122:125]
	v_mfma_f32_16x16x32_bf16 v[110:113], v[78:81], v[200:203], v[110:113]
	v_mfma_f32_16x16x32_bf16 v[106:109], v[86:89], v[200:203], v[106:109]
	v_mfma_f32_16x16x32_bf16 v[94:97], v[78:81], v[224:227], v[94:97]
	v_mfma_f32_16x16x32_bf16 v[90:93], v[86:89], v[224:227], v[90:93]
	v_mfma_f32_16x16x32_bf16 v[134:137], v[158:161], v[180:183], v[134:137]
	v_mfma_f32_16x16x32_bf16 v[130:133], v[172:175], v[180:183], v[130:133]
	v_mfma_f32_16x16x32_bf16 v[118:121], v[158:161], v[188:191], v[118:121]
	v_mfma_f32_16x16x32_bf16 v[114:117], v[172:175], v[188:191], v[114:117]
	v_mfma_f32_16x16x32_bf16 v[102:105], v[158:161], v[196:199], v[102:105]
	v_mfma_f32_16x16x32_bf16 v[98:101], v[172:175], v[196:199], v[98:101]
	v_mfma_f32_16x16x32_bf16 v[70:73], v[158:161], v[204:207], v[70:73]
	v_mfma_f32_16x16x32_bf16 v[66:69], v[172:175], v[204:207], v[66:69]
	v_mfma_f32_16x16x32_bf16 v[134:137], v[168:171], v[184:187], v[134:137]
	v_mfma_f32_16x16x32_bf16 v[130:133], v[176:179], v[184:187], v[130:133]
	v_mfma_f32_16x16x32_bf16 v[118:121], v[168:171], v[192:195], v[118:121]
	v_mfma_f32_16x16x32_bf16 v[114:117], v[176:179], v[192:195], v[114:117]
	v_mfma_f32_16x16x32_bf16 v[102:105], v[168:171], v[200:203], v[102:105]
	v_mfma_f32_16x16x32_bf16 v[98:101], v[176:179], v[200:203], v[98:101]
	v_mfma_f32_16x16x32_bf16 v[70:73], v[168:171], v[224:227], v[70:73]
	v_mfma_f32_16x16x32_bf16 v[66:69], v[176:179], v[224:227], v[66:69]
	s_setprio 0
	s_barrier
	s_add_i32 s97, s97, s76
	v_lshl_add_u64 v[162:163], s[74:75], 0, v[150:151]
	s_mov_b32 m0, s97
	ds_read_b128 v[180:183], v166 offset:16384
	ds_read_b128 v[184:187], v166 offset:17408
	ds_read_b128 v[188:191], v166 offset:18432
	ds_read_b128 v[192:195], v166 offset:19456
	ds_read_b128 v[196:199], v166 offset:20480
	ds_read_b128 v[200:203], v166 offset:21504
	ds_read_b128 v[204:207], v166 offset:22528
	ds_read_b128 v[224:227], v166 offset:23552
	global_load_lds_dwordx4 v[162:163], off
	s_add_i32 m0, s97, 0x2000
	v_lshl_add_u64 v[228:229], s[74:75], 0, v[146:147]
	s_add_u32 s74, s74, s22
	s_addc_u32 s75, s75, s23
	s_add_i32 s71, s71, s76
	global_load_lds_dwordx4 v[228:229], off
	v_lshl_add_u64 v[230:231], s[74:75], 0, v[150:151]
	s_mov_b32 m0, s71
	v_lshl_add_u64 v[232:233], s[74:75], 0, v[146:147]
	global_load_lds_dwordx4 v[230:231], off
	s_add_i32 m0, s71, 0x2000
	v_lshl_add_u64 v[234:235], s[42:43], 0, v[152:153]
	global_load_lds_dwordx4 v[232:233], off
	s_mov_b32 m0, s77
	v_lshl_add_u64 v[238:239], s[42:43], 0, v[148:149]
	global_load_lds_dwordx4 v[234:235], off
	s_mov_b32 m0, s82
	s_nop 0
	global_load_lds_dwordx4 v[238:239], off
	s_waitcnt vmcnt(8)
	s_waitcnt lgkmcnt(0)
	s_barrier
; #define PG8_STAGE(bufoff, gbase, voff) do { _Pragma("unroll") for (int _i = 0; _i < 2; ++_i) \
;         __builtin_amdgcn_global_load_lds((const unsigned*)((const char*)(gbase) + (voff)[_i]), (PG8_LAS unsigned*)(lds + (bufoff) + ldsw + _i * 8192), 16, 0, 0); } while (0)
; #define PG8_LDA(dst, b, h) do { _Pragma("unroll") for (int m = 0; m < 4; ++m) _Pragma("unroll") for (int k = 0; k < 2; ++k) dst[m][k] = *(const PG8_LAS bf16x8*)(lds + PG8_SA(b, h) + aoff + m * 2048 + k * 1024); } while (0)
; #define PG8_LDB(dst, b, h) do { _Pragma("unroll") for (int n = 0; n < 2; ++n) _Pragma("unroll") for (int k = 0; k < 2; ++k) dst[n][k] = *(const PG8_LAS bf16x8*)(lds + PG8_SB(b, h) + boff + n * 2048 + k * 1024); } while (0)
; #define PG8_MMA(ai, bj, At, Bt) do { __builtin_amdgcn_s_setprio(1); _Pragma("unroll") for (int m = 0; m < 4; ++m) _Pragma("unroll") for (int n = 0; n < 2; ++n) _Pragma("unroll") for (int k = 0; k < 2; ++k) \
;         acc[ai][bj][m][n] = __builtin_amdgcn_mfma_f32_16x16x32_bf16(Bt[n][k], At[m][k], acc[ai][bj][m][n], 0, 0, 0); __builtin_amdgcn_s_setprio(0); } while (0)
; #define PG8_WAIT_V(n) asm volatile("s_waitcnt vmcnt(" #n ")" ::: "memory")
; #define PG8_WAIT_L(n) asm volatile("s_waitcnt lgkmcnt(" #n ")" ::: "memory")
; #define PG8_BAR __builtin_amdgcn_s_barrier()
; #define PG8_SCHED __builtin_amdgcn_sched_barrier(0)
; template <class Epi, class Sched, bool ALIGN_EPI = false, bool SP2 = false>
; __device__ __forceinline__ void gemm_phase(PG8_LAS unsigned char* lds, const Gemm g, const Sched& S, const Epi& E, const int wave0) {
;     ...
;             PG8_WAIT_V(8); PG8_WAIT_L(0); PG8_BAR; PG8_MMA(1, 0, At, B0); PG8_MMA(1, 1, At, B1); PG8_BAR; PG8_SCHED;
;             PG8_LDB(B0, 1, 0); PG8_LDB(B1, 1, 1); PG8_SCHED; PG8_LDA(At, 1, 0); PG8_STAGE(PG8_SA(0, 1), a2 + hstepA, voffA);
;             PG8_WAIT_V(8); PG8_WAIT_L(0); PG8_BAR; PG8_MMA(0, 0, At, B0); PG8_MMA(0, 1, At, B1); PG8_BAR; PG8_SCHED;
	s_setprio 1
	s_waitcnt lgkmcnt(0)
	v_mfma_f32_16x16x32_bf16 v[62:65], v[74:77], v[180:183], v[62:65]
	v_mfma_f32_16x16x32_bf16 v[58:61], v[82:85], v[180:183], v[58:61]
	v_mfma_f32_16x16x32_bf16 v[46:49], v[74:77], v[188:191], v[46:49]
	v_mfma_f32_16x16x32_bf16 v[42:45], v[82:85], v[188:191], v[42:45]
	v_mfma_f32_16x16x32_bf16 v[30:33], v[74:77], v[196:199], v[30:33]
	v_mfma_f32_16x16x32_bf16 v[26:29], v[82:85], v[196:199], v[26:29]
	v_mfma_f32_16x16x32_bf16 v[14:17], v[74:77], v[204:207], v[14:17]
	v_mfma_f32_16x16x32_bf16 v[10:13], v[82:85], v[204:207], v[10:13]
	v_mfma_f32_16x16x32_bf16 v[62:65], v[78:81], v[184:187], v[62:65]
	v_mfma_f32_16x16x32_bf16 v[58:61], v[86:89], v[184:187], v[58:61]
	v_mfma_f32_16x16x32_bf16 v[46:49], v[78:81], v[192:195], v[46:49]
	v_mfma_f32_16x16x32_bf16 v[42:45], v[86:89], v[192:195], v[42:45]
	v_mfma_f32_16x16x32_bf16 v[30:33], v[78:81], v[200:203], v[30:33]
	v_mfma_f32_16x16x32_bf16 v[26:29], v[86:89], v[200:203], v[26:29]
	v_mfma_f32_16x16x32_bf16 v[14:17], v[78:81], v[224:227], v[14:17]
	v_mfma_f32_16x16x32_bf16 v[10:13], v[86:89], v[224:227], v[10:13]
	v_mfma_f32_16x16x32_bf16 v[54:57], v[158:161], v[180:183], v[54:57]
	v_mfma_f32_16x16x32_bf16 v[50:53], v[172:175], v[180:183], v[50:53]
	v_mfma_f32_16x16x32_bf16 v[38:41], v[158:161], v[188:191], v[38:41]
	v_mfma_f32_16x16x32_bf16 v[34:37], v[172:175], v[188:191], v[34:37]
	v_mfma_f32_16x16x32_bf16 v[22:25], v[158:161], v[196:199], v[22:25]
	v_mfma_f32_16x16x32_bf16 v[18:21], v[172:175], v[196:199], v[18:21]
	v_mfma_f32_16x16x32_bf16 v[6:9], v[158:161], v[204:207], v[6:9]
	v_mfma_f32_16x16x32_bf16 v[2:5], v[172:175], v[204:207], v[2:5]
	v_mfma_f32_16x16x32_bf16 v[54:57], v[168:171], v[184:187], v[54:57]
	v_mfma_f32_16x16x32_bf16 v[50:53], v[176:179], v[184:187], v[50:53]
	v_mfma_f32_16x16x32_bf16 v[38:41], v[168:171], v[192:195], v[38:41]
	v_mfma_f32_16x16x32_bf16 v[34:37], v[176:179], v[192:195], v[34:37]
	v_mfma_f32_16x16x32_bf16 v[22:25], v[168:171], v[200:203], v[22:25]
	v_mfma_f32_16x16x32_bf16 v[18:21], v[176:179], v[200:203], v[18:21]
	v_mfma_f32_16x16x32_bf16 v[6:9], v[168:171], v[224:227], v[6:9]
	v_mfma_f32_16x16x32_bf16 v[2:5], v[176:179], v[224:227], v[2:5]
	s_setprio 0
	s_barrier
	s_add_i32 s71, 0, 0x18000
	s_add_i32 s74, 0, 0x1c000
	v_add_u32_e32 v86, s71, v164
	v_add_u32_e32 v167, s74, v164
	ds_read_b128 v[74:77], v86
	ds_read_b128 v[78:81], v86 offset:1024
	ds_read_b128 v[82:85], v86 offset:2048
	ds_read_b128 v[86:89], v86 offset:3072
	ds_read_b128 v[158:161], v167
	ds_read_b128 v[168:171], v167 offset:1024
	ds_read_b128 v[172:175], v167 offset:2048
	ds_read_b128 v[176:179], v167 offset:3072
	s_add_u32 s42, s42, s20
	s_addc_u32 s43, s43, s21
	s_mov_b32 m0, s91
	v_lshl_add_u64 v[240:241], s[42:43], 0, v[152:153]
	ds_read_b128 v[180:183], v166 offset:32768
	ds_read_b128 v[184:187], v166 offset:33792
	ds_read_b128 v[188:191], v166 offset:34816
	ds_read_b128 v[192:195], v166 offset:35840
	ds_read_b128 v[196:199], v166 offset:36864
	ds_read_b128 v[200:203], v166 offset:37888
	ds_read_b128 v[204:207], v166 offset:38912
	ds_read_b128 v[224:227], v166 offset:39936
	global_load_lds_dwordx4 v[240:241], off
	v_lshl_add_u64 v[240:241], s[42:43], 0, v[148:149]
	s_mov_b32 m0, s92
	s_nop 0
	global_load_lds_dwordx4 v[240:241], off
	s_waitcnt vmcnt(8)
	s_waitcnt lgkmcnt(0)
	s_barrier
	s_setprio 1
	s_waitcnt lgkmcnt(0)
	v_mfma_f32_16x16x32_bf16 v[142:145], v[74:77], v[180:183], v[142:145]
	v_mfma_f32_16x16x32_bf16 v[138:141], v[82:85], v[180:183], v[138:141]
	v_mfma_f32_16x16x32_bf16 v[126:129], v[74:77], v[188:191], v[126:129]
	v_mfma_f32_16x16x32_bf16 v[122:125], v[82:85], v[188:191], v[122:125]
	v_mfma_f32_16x16x32_bf16 v[110:113], v[74:77], v[196:199], v[110:113]
	v_mfma_f32_16x16x32_bf16 v[106:109], v[82:85], v[196:199], v[106:109]
	v_mfma_f32_16x16x32_bf16 v[94:97], v[74:77], v[204:207], v[94:97]
	v_mfma_f32_16x16x32_bf16 v[90:93], v[82:85], v[204:207], v[90:93]
	v_mfma_f32_16x16x32_bf16 v[142:145], v[78:81], v[184:187], v[142:145]
	v_mfma_f32_16x16x32_bf16 v[138:141], v[86:89], v[184:187], v[138:141]
	v_mfma_f32_16x16x32_bf16 v[126:129], v[78:81], v[192:195], v[126:129]
	v_mfma_f32_16x16x32_bf16 v[122:125], v[86:89], v[192:195], v[122:125]
	v_mfma_f32_16x16x32_bf16 v[110:113], v[78:81], v[200:203], v[110:113]
	v_mfma_f32_16x16x32_bf16 v[106:109], v[86:89], v[200:203], v[106:109]
	v_mfma_f32_16x16x32_bf16 v[94:97], v[78:81], v[224:227], v[94:97]
	v_mfma_f32_16x16x32_bf16 v[90:93], v[86:89], v[224:227], v[90:93]
	v_mfma_f32_16x16x32_bf16 v[134:137], v[158:161], v[180:183], v[134:137]
	v_mfma_f32_16x16x32_bf16 v[130:133], v[172:175], v[180:183], v[130:133]
	v_mfma_f32_16x16x32_bf16 v[118:121], v[158:161], v[188:191], v[118:121]
	v_mfma_f32_16x16x32_bf16 v[114:117], v[172:175], v[188:191], v[114:117]
	v_mfma_f32_16x16x32_bf16 v[102:105], v[158:161], v[196:199], v[102:105]
	v_mfma_f32_16x16x32_bf16 v[98:101], v[172:175], v[196:199], v[98:101]
	v_mfma_f32_16x16x32_bf16 v[70:73], v[158:161], v[204:207], v[70:73]
	v_mfma_f32_16x16x32_bf16 v[66:69], v[172:175], v[204:207], v[66:69]
	v_mfma_f32_16x16x32_bf16 v[134:137], v[168:171], v[184:187], v[134:137]
	v_mfma_f32_16x16x32_bf16 v[130:133], v[176:179], v[184:187], v[130:133]
	v_mfma_f32_16x16x32_bf16 v[118:121], v[168:171], v[192:195], v[118:121]
	v_mfma_f32_16x16x32_bf16 v[114:117], v[176:179], v[192:195], v[114:117]
	v_mfma_f32_16x16x32_bf16 v[102:105], v[168:171], v[200:203], v[102:105]
	v_mfma_f32_16x16x32_bf16 v[98:101], v[176:179], v[200:203], v[98:101]
	v_mfma_f32_16x16x32_bf16 v[70:73], v[168:171], v[224:227], v[70:73]
	v_mfma_f32_16x16x32_bf16 v[66:69], v[176:179], v[224:227], v[66:69]
	s_setprio 0
	s_barrier
; #define PG8_STAGE(bufoff, gbase, voff) do { _Pragma("unroll") for (int _i = 0; _i < 2; ++_i) \
;         __builtin_amdgcn_global_load_lds((const unsigned*)((const char*)(gbase) + (voff)[_i]), (PG8_LAS unsigned*)(lds + (bufoff) + ldsw + _i * 8192), 16, 0, 0); } while (0)
; #define PG8_LDA(dst, b, h) do { _Pragma("unroll") for (int m = 0; m < 4; ++m) _Pragma("unroll") for (int k = 0; k < 2; ++k) dst[m][k] = *(const PG8_LAS bf16x8*)(lds + PG8_SA(b, h) + aoff + m * 2048 + k * 1024); } while (0)
; #define PG8_MMA(ai, bj, At, Bt) do { __builtin_amdgcn_s_setprio(1); _Pragma("unroll") for (int m = 0; m < 4; ++m) _Pragma("unroll") for (int n = 0; n < 2; ++n) _Pragma("unroll") for (int k = 0; k < 2; ++k) \
;         acc[ai][bj][m][n] = __builtin_amdgcn_mfma_f32_16x16x32_bf16(Bt[n][k], At[m][k], acc[ai][bj][m][n], 0, 0, 0); __builtin_amdgcn_s_setprio(0); } while (0)
; #define PG8_WAIT_V(n) asm volatile("s_waitcnt vmcnt(" #n ")" ::: "memory")
; #define PG8_WAIT_L(n) asm volatile("s_waitcnt lgkmcnt(" #n ")" ::: "memory")
; #define PG8_BAR __builtin_amdgcn_s_barrier()
; #define PG8_SCHED __builtin_amdgcn_sched_barrier(0)
; template <class Epi, class Sched, bool ALIGN_EPI = false, bool SP2 = false>
; __device__ __forceinline__ void gemm_phase(PG8_LAS unsigned char* lds, const Gemm g, const Sched& S, const Epi& E, const int wave0) {
;     ...
;             PG8_LDA(At, 1, 1); PG8_STAGE(PG8_SB(1, 0), b3, voffB); PG8_STAGE(PG8_SB(1, 1), b3 + hstepB, voffB); PG8_STAGE(PG8_SA(1, 0), a3, voffA);
;             PG8_WAIT_V(8); PG8_WAIT_L(0); PG8_BAR; PG8_MMA(1, 0, At, B0); PG8_MMA(1, 1, At, B1); PG8_BAR; PG8_SCHED;
	s_add_i32 s42, s71, s76
	v_lshl_add_u64 v[162:163], v[162:163], 0, s[64:65]
	s_mov_b32 m0, s42
	ds_read_b128 v[180:183], v166 offset:49152
	ds_read_b128 v[184:187], v166 offset:50176
	ds_read_b128 v[188:191], v166 offset:51200
	ds_read_b128 v[192:195], v166 offset:52224
	ds_read_b128 v[196:199], v166 offset:53248
	ds_read_b128 v[200:203], v166 offset:54272
	ds_read_b128 v[204:207], v166 offset:55296
	ds_read_b128 v[224:227], v166 offset:56320
	global_load_lds_dwordx4 v[162:163], off
	v_lshl_add_u64 v[162:163], v[228:229], 0, s[64:65]
	s_add_i32 m0, s42, 0x2000
	s_add_i32 s42, s74, s76
	global_load_lds_dwordx4 v[162:163], off
	v_lshl_add_u64 v[162:163], v[230:231], 0, s[64:65]
	s_mov_b32 m0, s42
	s_nop 0
	global_load_lds_dwordx4 v[162:163], off
	v_lshl_add_u64 v[162:163], v[232:233], 0, s[64:65]
	s_add_i32 m0, s42, 0x2000
	s_nop 0
	global_load_lds_dwordx4 v[162:163], off
	v_lshl_add_u64 v[162:163], v[234:235], 0, s[64:65]
	s_mov_b32 m0, s94
	s_nop 0
	global_load_lds_dwordx4 v[162:163], off
	v_lshl_add_u64 v[162:163], v[238:239], 0, s[64:65]
	s_mov_b32 m0, s95
	s_nop 0
	global_load_lds_dwordx4 v[162:163], off
	s_waitcnt vmcnt(8)
	s_waitcnt lgkmcnt(0)
	s_barrier
	s_setprio 1
	s_waitcnt lgkmcnt(0)
	v_mfma_f32_16x16x32_bf16 v[62:65], v[74:77], v[180:183], v[62:65]
	v_mfma_f32_16x16x32_bf16 v[58:61], v[82:85], v[180:183], v[58:61]
	v_mfma_f32_16x16x32_bf16 v[46:49], v[74:77], v[188:191], v[46:49]
	v_mfma_f32_16x16x32_bf16 v[42:45], v[82:85], v[188:191], v[42:45]
	v_mfma_f32_16x16x32_bf16 v[30:33], v[74:77], v[196:199], v[30:33]
	v_mfma_f32_16x16x32_bf16 v[26:29], v[82:85], v[196:199], v[26:29]
	v_mfma_f32_16x16x32_bf16 v[14:17], v[74:77], v[204:207], v[14:17]
	v_mfma_f32_16x16x32_bf16 v[10:13], v[82:85], v[204:207], v[10:13]
	v_mfma_f32_16x16x32_bf16 v[62:65], v[78:81], v[184:187], v[62:65]
	v_mfma_f32_16x16x32_bf16 v[58:61], v[86:89], v[184:187], v[58:61]
	v_mfma_f32_16x16x32_bf16 v[46:49], v[78:81], v[192:195], v[46:49]
	v_mfma_f32_16x16x32_bf16 v[42:45], v[86:89], v[192:195], v[42:45]
	v_mfma_f32_16x16x32_bf16 v[30:33], v[78:81], v[200:203], v[30:33]
	v_mfma_f32_16x16x32_bf16 v[26:29], v[86:89], v[200:203], v[26:29]
	v_mfma_f32_16x16x32_bf16 v[14:17], v[78:81], v[224:227], v[14:17]
	v_mfma_f32_16x16x32_bf16 v[10:13], v[86:89], v[224:227], v[10:13]
	v_mfma_f32_16x16x32_bf16 v[54:57], v[158:161], v[180:183], v[54:57]
	v_mfma_f32_16x16x32_bf16 v[50:53], v[172:175], v[180:183], v[50:53]
	v_mfma_f32_16x16x32_bf16 v[38:41], v[158:161], v[188:191], v[38:41]
	v_mfma_f32_16x16x32_bf16 v[34:37], v[172:175], v[188:191], v[34:37]
	v_mfma_f32_16x16x32_bf16 v[22:25], v[158:161], v[196:199], v[22:25]
	v_mfma_f32_16x16x32_bf16 v[18:21], v[172:175], v[196:199], v[18:21]
	v_mfma_f32_16x16x32_bf16 v[6:9], v[158:161], v[204:207], v[6:9]
	v_mfma_f32_16x16x32_bf16 v[2:5], v[172:175], v[204:207], v[2:5]
	v_mfma_f32_16x16x32_bf16 v[54:57], v[168:171], v[184:187], v[54:57]
	v_mfma_f32_16x16x32_bf16 v[50:53], v[176:179], v[184:187], v[50:53]
	v_mfma_f32_16x16x32_bf16 v[38:41], v[168:171], v[192:195], v[38:41]
	v_mfma_f32_16x16x32_bf16 v[34:37], v[176:179], v[192:195], v[34:37]
	v_mfma_f32_16x16x32_bf16 v[22:25], v[168:171], v[200:203], v[22:25]
	v_mfma_f32_16x16x32_bf16 v[18:21], v[176:179], v[200:203], v[18:21]
	v_mfma_f32_16x16x32_bf16 v[6:9], v[168:171], v[224:227], v[6:9]
	v_mfma_f32_16x16x32_bf16 v[2:5], v[176:179], v[224:227], v[2:5]
	s_setprio 0
	s_barrier
	s_add_u32 s72, s72, 0x100
	s_addc_u32 s73, s73, 0
	s_add_u32 s40, s40, 0x100
	s_addc_u32 s41, s41, 0
	s_cmp_ge_i32 s70, s93
	s_mov_b32 s42, s70
	s_cbranch_scc0 .LBB0_665

; #define PG8_STAGE(bufoff, gbase, voff) do { _Pragma("unroll") for (int _i = 0; _i < 2; ++_i) \
;         __builtin_amdgcn_global_load_lds((const unsigned*)((const char*)(gbase) + (voff)[_i]), (PG8_LAS unsigned*)(lds + (bufoff) + ldsw + _i * 8192), 16, 0, 0); } while (0)
; #define PG8_LDA(dst, b, h) do { _Pragma("unroll") for (int m = 0; m < 4; ++m) _Pragma("unroll") for (int k = 0; k < 2; ++k) dst[m][k] = *(const PG8_LAS bf16x8*)(lds + PG8_SA(b, h) + aoff + m * 2048 + k * 1024); } while (0)
; #define PG8_LDB(dst, b, h) do { _Pragma("unroll") for (int n = 0; n < 2; ++n) _Pragma("unroll") for (int k = 0; k < 2; ++k) dst[n][k] = *(const PG8_LAS bf16x8*)(lds + PG8_SB(b, h) + boff + n * 2048 + k * 1024); } while (0)
; #define PG8_MMA(ai, bj, At, Bt) do { __builtin_amdgcn_s_setprio(1); _Pragma("unroll") for (int m = 0; m < 4; ++m) _Pragma("unroll") for (int n = 0; n < 2; ++n) _Pragma("unroll") for (int k = 0; k < 2; ++k) \
;         acc[ai][bj][m][n] = __builtin_amdgcn_mfma_f32_16x16x32_bf16(Bt[n][k], At[m][k], acc[ai][bj][m][n], 0, 0, 0); __builtin_amdgcn_s_setprio(0); } while (0)
; #define PG8_WAIT_V(n) asm volatile("s_waitcnt vmcnt(" #n ")" ::: "memory")
; #define PG8_BAR __builtin_amdgcn_s_barrier()
; template <class Epi, class Sched, bool ALIGN_EPI = false, bool SP2 = false>
; __device__ __forceinline__ void gemm_phase(PG8_LAS unsigned char* lds, const Gemm g, const Sched& S, const Epi& E, const int wave0) {
;     ...
;         for (int t = 0; t < nt; t += 2) {
;             const bool last = (t == nt - 2);
;             const char* a1 = cA + (size_t)(t + 1) * kstep;
;             const char* a2 = last ? nA : cA + (size_t)(t + 2) * kstep; const char* b2 = last ? nB : cB + (size_t)(t + 2) * kstep;
;             const char* a3 = a2 + kstep; const char* b3 = b2 + kstep;
;             if (last && has_next) S.a_ready(nxt);
;             if constexpr (SP2) {
;             PG8_LDB(B0, 0, 0); PG8_LDB(B1, 0, 1); PG8_SCHED; PG8_LDA(At, 0, 0); PG8_STAGE(PG8_SA(1, 1), a1 + hstepA, voffA);
;             PG8_WAIT_V(8); PG8_WAIT_L(0); PG8_BAR; PG8_MMA(0, 0, At, B0); PG8_MMA(0, 1, At, B1); PG8_BAR; PG8_SCHED;
;             PG8_LDA(At, 0, 1); PG8_STAGE(PG8_SB(0, 0), b2, voffB); PG8_STAGE(PG8_SB(0, 1), b2 + hstepB, voffB); PG8_STAGE(PG8_SA(0, 0), a2, voffA);
;             PG8_WAIT_V(8); PG8_WAIT_L(0); PG8_BAR; PG8_MMA(1, 0, At, B0); PG8_MMA(1, 1, At, B1); PG8_BAR; PG8_SCHED;
.LBB0_763:
	s_add_i32 s91, s70, 2
	s_add_u32 s92, s60, 0x80
	s_addc_u32 s71, s61, 0
	s_add_i32 s94, 0, 0x10000
	s_cmp_eq_u32 s87, s70
	s_cselect_b32 s71, s41, s71
	s_cselect_b32 s70, s40, s92
	s_cselect_b32 s93, s59, s84
	s_cselect_b32 s92, s58, s83
	s_add_i32 s95, 0, 0x14000
	v_add_u32_e32 v42, s94, v176
	v_add_u32_e32 v170, s95, v176
	ds_read_b128 v[18:21], v42
	ds_read_b128 v[22:25], v42 offset:1024
	ds_read_b128 v[34:37], v42 offset:2048
	ds_read_b128 v[42:45], v42 offset:3072
	ds_read_b128 v[158:161], v170
	ds_read_b128 v[162:165], v170 offset:1024
	ds_read_b128 v[166:169], v170 offset:2048
	ds_read_b128 v[170:173], v170 offset:3072
	v_lshl_add_u64 v[174:175], s[60:61], 0, v[156:157]
	s_add_i32 m0, s72, 0xc000
	ds_read_b128 v[180:183], v178
	ds_read_b128 v[184:187], v178 offset:1024
	ds_read_b128 v[188:191], v178 offset:2048
	ds_read_b128 v[192:195], v178 offset:3072
	ds_read_b128 v[196:199], v178 offset:4096
	ds_read_b128 v[200:203], v178 offset:5120
	ds_read_b128 v[204:207], v178 offset:6144
	ds_read_b128 v[224:227], v178 offset:7168
	global_load_lds_dwordx4 v[174:175], off
	v_lshl_add_u64 v[174:175], s[60:61], 0, v[154:155]
	s_add_i32 m0, s72, 0xe000
	s_nop 0
	global_load_lds_dwordx4 v[174:175], off
	s_waitcnt vmcnt(8)
	s_waitcnt lgkmcnt(0)
	s_barrier
	s_setprio 1
	s_waitcnt lgkmcnt(0)
	v_mfma_f32_16x16x32_bf16 v[142:145], v[18:21], v[180:183], v[142:145]
	v_mfma_f32_16x16x32_bf16 v[138:141], v[34:37], v[180:183], v[138:141]
	v_mfma_f32_16x16x32_bf16 v[126:129], v[18:21], v[188:191], v[126:129]
	v_mfma_f32_16x16x32_bf16 v[122:125], v[34:37], v[188:191], v[122:125]
	v_mfma_f32_16x16x32_bf16 v[110:113], v[18:21], v[196:199], v[110:113]
	v_mfma_f32_16x16x32_bf16 v[106:109], v[34:37], v[196:199], v[106:109]
	v_mfma_f32_16x16x32_bf16 v[94:97], v[18:21], v[204:207], v[94:97]
	v_mfma_f32_16x16x32_bf16 v[90:93], v[34:37], v[204:207], v[90:93]
	v_mfma_f32_16x16x32_bf16 v[142:145], v[22:25], v[184:187], v[142:145]
	v_mfma_f32_16x16x32_bf16 v[138:141], v[42:45], v[184:187], v[138:141]
	v_mfma_f32_16x16x32_bf16 v[126:129], v[22:25], v[192:195], v[126:129]
	v_mfma_f32_16x16x32_bf16 v[122:125], v[42:45], v[192:195], v[122:125]
	v_mfma_f32_16x16x32_bf16 v[110:113], v[22:25], v[200:203], v[110:113]
	v_mfma_f32_16x16x32_bf16 v[106:109], v[42:45], v[200:203], v[106:109]
	v_mfma_f32_16x16x32_bf16 v[94:97], v[22:25], v[224:227], v[94:97]
	v_mfma_f32_16x16x32_bf16 v[90:93], v[42:45], v[224:227], v[90:93]
	v_mfma_f32_16x16x32_bf16 v[134:137], v[158:161], v[180:183], v[134:137]
	v_mfma_f32_16x16x32_bf16 v[130:133], v[166:169], v[180:183], v[130:133]
	v_mfma_f32_16x16x32_bf16 v[118:121], v[158:161], v[188:191], v[118:121]
	v_mfma_f32_16x16x32_bf16 v[114:117], v[166:169], v[188:191], v[114:117]
	v_mfma_f32_16x16x32_bf16 v[102:105], v[158:161], v[196:199], v[102:105]
	v_mfma_f32_16x16x32_bf16 v[98:101], v[166:169], v[196:199], v[98:101]
	v_mfma_f32_16x16x32_bf16 v[86:89], v[158:161], v[204:207], v[86:89]
	v_mfma_f32_16x16x32_bf16 v[82:85], v[166:169], v[204:207], v[82:85]
	v_mfma_f32_16x16x32_bf16 v[134:137], v[162:165], v[184:187], v[134:137]
	v_mfma_f32_16x16x32_bf16 v[130:133], v[170:173], v[184:187], v[130:133]
	v_mfma_f32_16x16x32_bf16 v[118:121], v[162:165], v[192:195], v[118:121]
	v_mfma_f32_16x16x32_bf16 v[114:117], v[170:173], v[192:195], v[114:117]
	v_mfma_f32_16x16x32_bf16 v[102:105], v[162:165], v[200:203], v[102:105]
	v_mfma_f32_16x16x32_bf16 v[98:101], v[170:173], v[200:203], v[98:101]
	v_mfma_f32_16x16x32_bf16 v[86:89], v[162:165], v[224:227], v[86:89]
	v_mfma_f32_16x16x32_bf16 v[82:85], v[170:173], v[224:227], v[82:85]
	s_setprio 0
	s_barrier
	s_add_i32 s94, s94, s5
	v_lshl_add_u64 v[174:175], s[92:93], 0, v[150:151]
	s_mov_b32 m0, s94
	ds_read_b128 v[180:183], v178 offset:16384
	ds_read_b128 v[184:187], v178 offset:17408
	ds_read_b128 v[188:191], v178 offset:18432
	ds_read_b128 v[192:195], v178 offset:19456
	ds_read_b128 v[196:199], v178 offset:20480
	ds_read_b128 v[200:203], v178 offset:21504
	ds_read_b128 v[204:207], v178 offset:22528
	ds_read_b128 v[224:227], v178 offset:23552
	global_load_lds_dwordx4 v[174:175], off
	s_add_i32 m0, s94, 0x2000
	v_lshl_add_u64 v[228:229], s[92:93], 0, v[146:147]
	s_add_u32 s92, s92, s20
	s_addc_u32 s93, s93, s21
	s_add_i32 s94, s95, s5
	global_load_lds_dwordx4 v[228:229], off
	v_lshl_add_u64 v[230:231], s[92:93], 0, v[150:151]
	s_mov_b32 m0, s94
	v_lshl_add_u64 v[232:233], s[92:93], 0, v[146:147]
	global_load_lds_dwordx4 v[230:231], off
	s_add_i32 m0, s94, 0x2000
	v_lshl_add_u64 v[234:235], s[70:71], 0, v[152:153]
	global_load_lds_dwordx4 v[232:233], off
	s_mov_b32 m0, s72
	v_lshl_add_u64 v[238:239], s[70:71], 0, v[148:149]
	global_load_lds_dwordx4 v[234:235], off
	s_mov_b32 m0, s73
	s_nop 0
	global_load_lds_dwordx4 v[238:239], off
	s_waitcnt vmcnt(8)
	s_waitcnt lgkmcnt(0)
	s_barrier
; #define PG8_STAGE(bufoff, gbase, voff) do { _Pragma("unroll") for (int _i = 0; _i < 2; ++_i) \
;         __builtin_amdgcn_global_load_lds((const unsigned*)((const char*)(gbase) + (voff)[_i]), (PG8_LAS unsigned*)(lds + (bufoff) + ldsw + _i * 8192), 16, 0, 0); } while (0)
; #define PG8_LDA(dst, b, h) do { _Pragma("unroll") for (int m = 0; m < 4; ++m) _Pragma("unroll") for (int k = 0; k < 2; ++k) dst[m][k] = *(const PG8_LAS bf16x8*)(lds + PG8_SA(b, h) + aoff + m * 2048 + k * 1024); } while (0)
; #define PG8_LDB(dst, b, h) do { _Pragma("unroll") for (int n = 0; n < 2; ++n) _Pragma("unroll") for (int k = 0; k < 2; ++k) dst[n][k] = *(const PG8_LAS bf16x8*)(lds + PG8_SB(b, h) + boff + n * 2048 + k * 1024); } while (0)
; #define PG8_MMA(ai, bj, At, Bt) do { __builtin_amdgcn_s_setprio(1); _Pragma("unroll") for (int m = 0; m < 4; ++m) _Pragma("unroll") for (int n = 0; n < 2; ++n) _Pragma("unroll") for (int k = 0; k < 2; ++k) \
;         acc[ai][bj][m][n] = __builtin_amdgcn_mfma_f32_16x16x32_bf16(Bt[n][k], At[m][k], acc[ai][bj][m][n], 0, 0, 0); __builtin_amdgcn_s_setprio(0); } while (0)
; #define PG8_WAIT_V(n) asm volatile("s_waitcnt vmcnt(" #n ")" ::: "memory")
; #define PG8_WAIT_L(n) asm volatile("s_waitcnt lgkmcnt(" #n ")" ::: "memory")
; #define PG8_BAR __builtin_amdgcn_s_barrier()
; #define PG8_SCHED __builtin_amdgcn_sched_barrier(0)
; template <class Epi, class Sched, bool ALIGN_EPI = false, bool SP2 = false>
; __device__ __forceinline__ void gemm_phase(PG8_LAS unsigned char* lds, const Gemm g, const Sched& S, const Epi& E, const int wave0) {
;     ...
;             PG8_WAIT_V(8); PG8_WAIT_L(0); PG8_BAR; PG8_MMA(1, 0, At, B0); PG8_MMA(1, 1, At, B1); PG8_BAR; PG8_SCHED;
;             PG8_LDB(B0, 1, 0); PG8_LDB(B1, 1, 1); PG8_SCHED; PG8_LDA(At, 1, 0); PG8_STAGE(PG8_SA(0, 1), a2 + hstepA, voffA);
;             PG8_WAIT_V(8); PG8_WAIT_L(0); PG8_BAR; PG8_MMA(0, 0, At, B0); PG8_MMA(0, 1, At, B1); PG8_BAR; PG8_SCHED;
	s_setprio 1
	s_waitcnt lgkmcnt(0)
	v_mfma_f32_16x16x32_bf16 v[78:81], v[18:21], v[180:183], v[78:81]
	v_mfma_f32_16x16x32_bf16 v[74:77], v[34:37], v[180:183], v[74:77]
	v_mfma_f32_16x16x32_bf16 v[62:65], v[18:21], v[188:191], v[62:65]
	v_mfma_f32_16x16x32_bf16 v[58:61], v[34:37], v[188:191], v[58:61]
	v_mfma_f32_16x16x32_bf16 v[46:49], v[18:21], v[196:199], v[46:49]
	v_mfma_f32_16x16x32_bf16 v[38:41], v[34:37], v[196:199], v[38:41]
	v_mfma_f32_16x16x32_bf16 v[14:17], v[18:21], v[204:207], v[14:17]
	v_mfma_f32_16x16x32_bf16 v[10:13], v[34:37], v[204:207], v[10:13]
	v_mfma_f32_16x16x32_bf16 v[78:81], v[22:25], v[184:187], v[78:81]
	v_mfma_f32_16x16x32_bf16 v[74:77], v[42:45], v[184:187], v[74:77]
	v_mfma_f32_16x16x32_bf16 v[62:65], v[22:25], v[192:195], v[62:65]
	v_mfma_f32_16x16x32_bf16 v[58:61], v[42:45], v[192:195], v[58:61]
	v_mfma_f32_16x16x32_bf16 v[46:49], v[22:25], v[200:203], v[46:49]
	v_mfma_f32_16x16x32_bf16 v[38:41], v[42:45], v[200:203], v[38:41]
	v_mfma_f32_16x16x32_bf16 v[14:17], v[22:25], v[224:227], v[14:17]
	v_mfma_f32_16x16x32_bf16 v[10:13], v[42:45], v[224:227], v[10:13]
	v_mfma_f32_16x16x32_bf16 v[30:33], v[158:161], v[196:199], v[30:33]
	v_mfma_f32_16x16x32_bf16 v[26:29], v[166:169], v[196:199], v[26:29]
	v_mfma_f32_16x16x32_bf16 v[6:9], v[158:161], v[204:207], v[6:9]
	v_mfma_f32_16x16x32_bf16 v[2:5], v[166:169], v[204:207], v[2:5]
	v_mfma_f32_16x16x32_bf16 v[18:21], v[158:161], v[180:183], v[70:73]
	v_mfma_f32_16x16x32_bf16 v[22:25], v[166:169], v[180:183], v[66:69]
	v_mfma_f32_16x16x32_bf16 v[34:37], v[158:161], v[188:191], v[54:57]
	v_mfma_f32_16x16x32_bf16 v[42:45], v[166:169], v[188:191], v[50:53]
	v_mfma_f32_16x16x32_bf16 v[30:33], v[162:165], v[200:203], v[30:33]
	v_mfma_f32_16x16x32_bf16 v[26:29], v[170:173], v[200:203], v[26:29]
	v_mfma_f32_16x16x32_bf16 v[6:9], v[162:165], v[224:227], v[6:9]
	v_mfma_f32_16x16x32_bf16 v[2:5], v[170:173], v[224:227], v[2:5]
	v_mfma_f32_16x16x32_bf16 v[18:21], v[162:165], v[184:187], v[18:21]
	v_mfma_f32_16x16x32_bf16 v[22:25], v[170:173], v[184:187], v[22:25]
	v_mfma_f32_16x16x32_bf16 v[34:37], v[162:165], v[192:195], v[34:37]
	v_mfma_f32_16x16x32_bf16 v[42:45], v[170:173], v[192:195], v[42:45]
	s_setprio 0
	s_barrier
	s_add_i32 s92, 0, 0x18000
	s_add_i32 s93, 0, 0x1c000
	v_add_u32_e32 v70, s92, v176
	v_add_u32_e32 v170, s93, v176
	ds_read_b128 v[50:53], v70
	ds_read_b128 v[54:57], v70 offset:1024
	ds_read_b128 v[66:69], v70 offset:2048
	ds_read_b128 v[70:73], v70 offset:3072
	ds_read_b128 v[158:161], v170
	ds_read_b128 v[162:165], v170 offset:1024
	ds_read_b128 v[166:169], v170 offset:2048
	ds_read_b128 v[170:173], v170 offset:3072
	s_add_u32 s70, s70, s6
	s_addc_u32 s71, s71, s7
	s_mov_b32 m0, s74
	v_lshl_add_u64 v[240:241], s[70:71], 0, v[152:153]
	ds_read_b128 v[180:183], v178 offset:32768
	ds_read_b128 v[184:187], v178 offset:33792
	ds_read_b128 v[188:191], v178 offset:34816
	ds_read_b128 v[192:195], v178 offset:35840
	ds_read_b128 v[196:199], v178 offset:36864
	ds_read_b128 v[200:203], v178 offset:37888
	ds_read_b128 v[204:207], v178 offset:38912
	ds_read_b128 v[224:227], v178 offset:39936
	global_load_lds_dwordx4 v[240:241], off
	v_lshl_add_u64 v[240:241], s[70:71], 0, v[148:149]
	s_mov_b32 m0, s75
	s_nop 0
	global_load_lds_dwordx4 v[240:241], off
	s_waitcnt vmcnt(8)
	s_waitcnt lgkmcnt(0)
	s_barrier
	s_setprio 1
	s_waitcnt lgkmcnt(0)
	v_mfma_f32_16x16x32_bf16 v[142:145], v[50:53], v[180:183], v[142:145]
	v_mfma_f32_16x16x32_bf16 v[138:141], v[66:69], v[180:183], v[138:141]
	v_mfma_f32_16x16x32_bf16 v[126:129], v[50:53], v[188:191], v[126:129]
	v_mfma_f32_16x16x32_bf16 v[122:125], v[66:69], v[188:191], v[122:125]
	v_mfma_f32_16x16x32_bf16 v[110:113], v[50:53], v[196:199], v[110:113]
	v_mfma_f32_16x16x32_bf16 v[106:109], v[66:69], v[196:199], v[106:109]
	v_mfma_f32_16x16x32_bf16 v[94:97], v[50:53], v[204:207], v[94:97]
	v_mfma_f32_16x16x32_bf16 v[90:93], v[66:69], v[204:207], v[90:93]
	v_mfma_f32_16x16x32_bf16 v[142:145], v[54:57], v[184:187], v[142:145]
	v_mfma_f32_16x16x32_bf16 v[138:141], v[70:73], v[184:187], v[138:141]
	v_mfma_f32_16x16x32_bf16 v[126:129], v[54:57], v[192:195], v[126:129]
	v_mfma_f32_16x16x32_bf16 v[122:125], v[70:73], v[192:195], v[122:125]
	v_mfma_f32_16x16x32_bf16 v[110:113], v[54:57], v[200:203], v[110:113]
	v_mfma_f32_16x16x32_bf16 v[106:109], v[70:73], v[200:203], v[106:109]
	v_mfma_f32_16x16x32_bf16 v[94:97], v[54:57], v[224:227], v[94:97]
	v_mfma_f32_16x16x32_bf16 v[90:93], v[70:73], v[224:227], v[90:93]
	v_mfma_f32_16x16x32_bf16 v[134:137], v[158:161], v[180:183], v[134:137]
	v_mfma_f32_16x16x32_bf16 v[130:133], v[166:169], v[180:183], v[130:133]
	v_mfma_f32_16x16x32_bf16 v[118:121], v[158:161], v[188:191], v[118:121]
	v_mfma_f32_16x16x32_bf16 v[114:117], v[166:169], v[188:191], v[114:117]
	v_mfma_f32_16x16x32_bf16 v[102:105], v[158:161], v[196:199], v[102:105]
	v_mfma_f32_16x16x32_bf16 v[98:101], v[166:169], v[196:199], v[98:101]
	v_mfma_f32_16x16x32_bf16 v[86:89], v[158:161], v[204:207], v[86:89]
	v_mfma_f32_16x16x32_bf16 v[82:85], v[166:169], v[204:207], v[82:85]
	v_mfma_f32_16x16x32_bf16 v[134:137], v[162:165], v[184:187], v[134:137]
	v_mfma_f32_16x16x32_bf16 v[130:133], v[170:173], v[184:187], v[130:133]
	v_mfma_f32_16x16x32_bf16 v[118:121], v[162:165], v[192:195], v[118:121]
	v_mfma_f32_16x16x32_bf16 v[114:117], v[170:173], v[192:195], v[114:117]
	v_mfma_f32_16x16x32_bf16 v[102:105], v[162:165], v[200:203], v[102:105]
	v_mfma_f32_16x16x32_bf16 v[98:101], v[170:173], v[200:203], v[98:101]
	v_mfma_f32_16x16x32_bf16 v[86:89], v[162:165], v[224:227], v[86:89]
	v_mfma_f32_16x16x32_bf16 v[82:85], v[170:173], v[224:227], v[82:85]
	s_setprio 0
	s_barrier
; #define PG8_STAGE(bufoff, gbase, voff) do { _Pragma("unroll") for (int _i = 0; _i < 2; ++_i) \
;         __builtin_amdgcn_global_load_lds((const unsigned*)((const char*)(gbase) + (voff)[_i]), (PG8_LAS unsigned*)(lds + (bufoff) + ldsw + _i * 8192), 16, 0, 0); } while (0)
; #define PG8_LDA(dst, b, h) do { _Pragma("unroll") for (int m = 0; m < 4; ++m) _Pragma("unroll") for (int k = 0; k < 2; ++k) dst[m][k] = *(const PG8_LAS bf16x8*)(lds + PG8_SA(b, h) + aoff + m * 2048 + k * 1024); } while (0)
; #define PG8_MMA(ai, bj, At, Bt) do { __builtin_amdgcn_s_setprio(1); _Pragma("unroll") for (int m = 0; m < 4; ++m) _Pragma("unroll") for (int n = 0; n < 2; ++n) _Pragma("unroll") for (int k = 0; k < 2; ++k) \
;         acc[ai][bj][m][n] = __builtin_amdgcn_mfma_f32_16x16x32_bf16(Bt[n][k], At[m][k], acc[ai][bj][m][n], 0, 0, 0); __builtin_amdgcn_s_setprio(0); } while (0)
; #define PG8_WAIT_V(n) asm volatile("s_waitcnt vmcnt(" #n ")" ::: "memory")
; #define PG8_WAIT_L(n) asm volatile("s_waitcnt lgkmcnt(" #n ")" ::: "memory")
; #define PG8_BAR __builtin_amdgcn_s_barrier()
; #define PG8_SCHED __builtin_amdgcn_sched_barrier(0)
; template <class Epi, class Sched, bool ALIGN_EPI = false, bool SP2 = false>
; __device__ __forceinline__ void gemm_phase(PG8_LAS unsigned char* lds, const Gemm g, const Sched& S, const Epi& E, const int wave0) {
;     ...
;             PG8_LDA(At, 1, 1); PG8_STAGE(PG8_SB(1, 0), b3, voffB); PG8_STAGE(PG8_SB(1, 1), b3 + hstepB, voffB); PG8_STAGE(PG8_SA(1, 0), a3, voffA);
;             PG8_WAIT_V(8); PG8_WAIT_L(0); PG8_BAR; PG8_MMA(1, 0, At, B0); PG8_MMA(1, 1, At, B1); PG8_BAR; PG8_SCHED;
	s_add_i32 s70, s92, s5
	v_lshl_add_u64 v[174:175], v[174:175], 0, s[64:65]
	s_mov_b32 m0, s70
	ds_read_b128 v[180:183], v178 offset:49152
	ds_read_b128 v[184:187], v178 offset:50176
	ds_read_b128 v[188:191], v178 offset:51200
	ds_read_b128 v[192:195], v178 offset:52224
	ds_read_b128 v[196:199], v178 offset:53248
	ds_read_b128 v[200:203], v178 offset:54272
	ds_read_b128 v[204:207], v178 offset:55296
	ds_read_b128 v[224:227], v178 offset:56320
	global_load_lds_dwordx4 v[174:175], off
	v_lshl_add_u64 v[174:175], v[228:229], 0, s[64:65]
	s_add_i32 m0, s70, 0x2000
	s_add_i32 s70, s93, s5
	global_load_lds_dwordx4 v[174:175], off
	v_lshl_add_u64 v[174:175], v[230:231], 0, s[64:65]
	s_mov_b32 m0, s70
	s_nop 0
	global_load_lds_dwordx4 v[174:175], off
	v_lshl_add_u64 v[174:175], v[232:233], 0, s[64:65]
	s_add_i32 m0, s70, 0x2000
	s_nop 0
	global_load_lds_dwordx4 v[174:175], off
	v_lshl_add_u64 v[174:175], v[234:235], 0, s[64:65]
	s_mov_b32 m0, s76
	s_nop 0
	global_load_lds_dwordx4 v[174:175], off
	v_lshl_add_u64 v[174:175], v[238:239], 0, s[64:65]
	s_mov_b32 m0, s77
	s_nop 0
	global_load_lds_dwordx4 v[174:175], off
	s_waitcnt vmcnt(8)
	s_waitcnt lgkmcnt(0)
	s_barrier
	s_setprio 1
	s_waitcnt lgkmcnt(0)
	v_mfma_f32_16x16x32_bf16 v[78:81], v[50:53], v[180:183], v[78:81]
	v_mfma_f32_16x16x32_bf16 v[74:77], v[66:69], v[180:183], v[74:77]
	v_mfma_f32_16x16x32_bf16 v[62:65], v[50:53], v[188:191], v[62:65]
	v_mfma_f32_16x16x32_bf16 v[58:61], v[66:69], v[188:191], v[58:61]
	v_mfma_f32_16x16x32_bf16 v[46:49], v[50:53], v[196:199], v[46:49]
	v_mfma_f32_16x16x32_bf16 v[38:41], v[66:69], v[196:199], v[38:41]
	v_mfma_f32_16x16x32_bf16 v[14:17], v[50:53], v[204:207], v[14:17]
	v_mfma_f32_16x16x32_bf16 v[10:13], v[66:69], v[204:207], v[10:13]
	v_mfma_f32_16x16x32_bf16 v[78:81], v[54:57], v[184:187], v[78:81]
	v_mfma_f32_16x16x32_bf16 v[74:77], v[70:73], v[184:187], v[74:77]
	v_mfma_f32_16x16x32_bf16 v[62:65], v[54:57], v[192:195], v[62:65]
	v_mfma_f32_16x16x32_bf16 v[58:61], v[70:73], v[192:195], v[58:61]
	v_mfma_f32_16x16x32_bf16 v[46:49], v[54:57], v[200:203], v[46:49]
	v_mfma_f32_16x16x32_bf16 v[38:41], v[70:73], v[200:203], v[38:41]
	v_mfma_f32_16x16x32_bf16 v[14:17], v[54:57], v[224:227], v[14:17]
	v_mfma_f32_16x16x32_bf16 v[10:13], v[70:73], v[224:227], v[10:13]
	v_mfma_f32_16x16x32_bf16 v[18:21], v[158:161], v[180:183], v[18:21]
	v_mfma_f32_16x16x32_bf16 v[70:73], v[162:165], v[184:187], v[18:21]
	v_mfma_f32_16x16x32_bf16 v[18:21], v[166:169], v[180:183], v[22:25]
	v_mfma_f32_16x16x32_bf16 v[66:69], v[170:173], v[184:187], v[18:21]
	v_mfma_f32_16x16x32_bf16 v[18:21], v[158:161], v[188:191], v[34:37]
	v_mfma_f32_16x16x32_bf16 v[54:57], v[162:165], v[192:195], v[18:21]
	v_mfma_f32_16x16x32_bf16 v[18:21], v[166:169], v[188:191], v[42:45]
	v_mfma_f32_16x16x32_bf16 v[50:53], v[170:173], v[192:195], v[18:21]
	v_mfma_f32_16x16x32_bf16 v[18:21], v[158:161], v[196:199], v[30:33]
	v_mfma_f32_16x16x32_bf16 v[30:33], v[162:165], v[200:203], v[18:21]
	v_mfma_f32_16x16x32_bf16 v[18:21], v[166:169], v[196:199], v[26:29]
	v_mfma_f32_16x16x32_bf16 v[6:9], v[158:161], v[204:207], v[6:9]
	v_mfma_f32_16x16x32_bf16 v[2:5], v[166:169], v[204:207], v[2:5]
	v_mfma_f32_16x16x32_bf16 v[26:29], v[170:173], v[200:203], v[18:21]
	v_mfma_f32_16x16x32_bf16 v[6:9], v[162:165], v[224:227], v[6:9]
	v_mfma_f32_16x16x32_bf16 v[2:5], v[170:173], v[224:227], v[2:5]
	s_setprio 0
	s_barrier
	s_add_u32 s83, s83, 0x100
	s_addc_u32 s84, s84, 0
	s_add_u32 s60, s60, 0x100
	s_addc_u32 s61, s61, 0
	s_cmp_ge_i32 s91, s30
	s_mov_b32 s70, s91
	s_cbranch_scc0 .LBB0_763
	v_readlane_b32 s95, v255, 18

; #define PG8_STAGE(bufoff, gbase, voff) do { _Pragma("unroll") for (int _i = 0; _i < 2; ++_i) \
;         __builtin_amdgcn_global_load_lds((const unsigned*)((const char*)(gbase) + (voff)[_i]), (PG8_LAS unsigned*)(lds + (bufoff) + ldsw + _i * 8192), 16, 0, 0); } while (0)
; #define PG8_LDA(dst, b, h) do { _Pragma("unroll") for (int m = 0; m < 4; ++m) _Pragma("unroll") for (int k = 0; k < 2; ++k) dst[m][k] = *(const PG8_LAS bf16x8*)(lds + PG8_SA(b, h) + aoff + m * 2048 + k * 1024); } while (0)
; #define PG8_LDB(dst, b, h) do { _Pragma("unroll") for (int n = 0; n < 2; ++n) _Pragma("unroll") for (int k = 0; k < 2; ++k) dst[n][k] = *(const PG8_LAS bf16x8*)(lds + PG8_SB(b, h) + boff + n * 2048 + k * 1024); } while (0)
; #define PG8_MMA(ai, bj, At, Bt) do { __builtin_amdgcn_s_setprio(1); _Pragma("unroll") for (int m = 0; m < 4; ++m) _Pragma("unroll") for (int n = 0; n < 2; ++n) _Pragma("unroll") for (int k = 0; k < 2; ++k) \
;         acc[ai][bj][m][n] = __builtin_amdgcn_mfma_f32_16x16x32_bf16(Bt[n][k], At[m][k], acc[ai][bj][m][n], 0, 0, 0); __builtin_amdgcn_s_setprio(0); } while (0)
; #define PG8_WAIT_V(n) asm volatile("s_waitcnt vmcnt(" #n ")" ::: "memory")
; #define PG8_BAR __builtin_amdgcn_s_barrier()
; template <class Epi, class Sched, bool ALIGN_EPI = false, bool SP2 = false>
; __device__ __forceinline__ void gemm_phase(PG8_LAS unsigned char* lds, const Gemm g, const Sched& S, const Epi& E, const int wave0) {
;     ...
;         for (int t = 0; t < nt; t += 2) {
;             const bool last = (t == nt - 2);
;             const char* a1 = cA + (size_t)(t + 1) * kstep;
;             const char* a2 = last ? nA : cA + (size_t)(t + 2) * kstep; const char* b2 = last ? nB : cB + (size_t)(t + 2) * kstep;
;             const char* a3 = a2 + kstep; const char* b3 = b2 + kstep;
;             if (last && has_next) S.a_ready(nxt);
;             if constexpr (SP2) {
;             PG8_LDB(B0, 0, 0); PG8_LDB(B1, 0, 1); PG8_SCHED; PG8_LDA(At, 0, 0); PG8_STAGE(PG8_SA(1, 1), a1 + hstepA, voffA);
;             PG8_WAIT_V(8); PG8_WAIT_L(0); PG8_BAR; PG8_MMA(0, 0, At, B0); PG8_MMA(0, 1, At, B1); PG8_BAR; PG8_SCHED;
;             PG8_LDA(At, 0, 1); PG8_STAGE(PG8_SB(0, 0), b2, voffB); PG8_STAGE(PG8_SB(0, 1), b2 + hstepB, voffB); PG8_STAGE(PG8_SA(0, 0), a2, voffA);
;             PG8_WAIT_V(8); PG8_WAIT_L(0); PG8_BAR; PG8_MMA(1, 0, At, B0); PG8_MMA(1, 1, At, B1); PG8_BAR; PG8_SCHED;
.LBB0_853:
	s_add_i32 s94, s74, 2
	s_add_u32 s95, s72, 0x80
	s_addc_u32 s75, s73, 0
	s_add_i32 vcc_lo, 0, 0x10000
	s_cmp_eq_u32 s84, s74
	s_cselect_b32 s75, s61, s75
	s_cselect_b32 s74, s60, s95
	s_cselect_b32 s97, s71, s93
	s_cselect_b32 s96, s70, s92
	s_add_i32 s95, 0, 0x14000
	v_add_u32_e32 v142, vcc_lo, v172
	v_add_u32_e32 v170, s95, v172
	ds_read_b128 v[130:133], v142
	ds_read_b128 v[134:137], v142 offset:1024
	ds_read_b128 v[138:141], v142 offset:2048
	ds_read_b128 v[142:145], v142 offset:3072
	ds_read_b128 v[146:149], v170
	ds_read_b128 v[162:165], v170 offset:1024
	ds_read_b128 v[166:169], v170 offset:2048
	ds_read_b128 v[176:179], v170 offset:3072
	v_lshl_add_u64 v[170:171], s[72:73], 0, v[160:161]
	s_add_i32 m0, s1, 0xc000
	ds_read_b128 v[180:183], v173
	ds_read_b128 v[184:187], v173 offset:1024
	ds_read_b128 v[188:191], v173 offset:2048
	ds_read_b128 v[192:195], v173 offset:3072
	ds_read_b128 v[196:199], v173 offset:4096
	ds_read_b128 v[200:203], v173 offset:5120
	ds_read_b128 v[204:207], v173 offset:6144
	ds_read_b128 v[224:227], v173 offset:7168
	global_load_lds_dwordx4 v[170:171], off
	v_lshl_add_u64 v[170:171], s[72:73], 0, v[158:159]
	s_add_i32 m0, s1, 0xe000
	s_nop 0
	global_load_lds_dwordx4 v[170:171], off
	s_waitcnt vmcnt(8)
	s_waitcnt lgkmcnt(0)
	s_barrier
	s_setprio 1
	s_waitcnt lgkmcnt(0)
	v_mfma_f32_16x16x32_bf16 v[122:125], v[130:133], v[180:183], v[122:125]
	v_mfma_f32_16x16x32_bf16 v[126:129], v[138:141], v[180:183], v[126:129]
	v_mfma_f32_16x16x32_bf16 v[110:113], v[130:133], v[188:191], v[110:113]
	v_mfma_f32_16x16x32_bf16 v[106:109], v[138:141], v[188:191], v[106:109]
	v_mfma_f32_16x16x32_bf16 v[94:97], v[130:133], v[196:199], v[94:97]
	v_mfma_f32_16x16x32_bf16 v[90:93], v[138:141], v[196:199], v[90:93]
	v_mfma_f32_16x16x32_bf16 v[78:81], v[130:133], v[204:207], v[78:81]
	v_mfma_f32_16x16x32_bf16 v[74:77], v[138:141], v[204:207], v[74:77]
	v_mfma_f32_16x16x32_bf16 v[122:125], v[134:137], v[184:187], v[122:125]
	v_mfma_f32_16x16x32_bf16 v[126:129], v[142:145], v[184:187], v[126:129]
	v_mfma_f32_16x16x32_bf16 v[110:113], v[134:137], v[192:195], v[110:113]
	v_mfma_f32_16x16x32_bf16 v[106:109], v[142:145], v[192:195], v[106:109]
	v_mfma_f32_16x16x32_bf16 v[94:97], v[134:137], v[200:203], v[94:97]
	v_mfma_f32_16x16x32_bf16 v[90:93], v[142:145], v[200:203], v[90:93]
	v_mfma_f32_16x16x32_bf16 v[78:81], v[134:137], v[224:227], v[78:81]
	v_mfma_f32_16x16x32_bf16 v[74:77], v[142:145], v[224:227], v[74:77]
	v_mfma_f32_16x16x32_bf16 v[118:121], v[146:149], v[180:183], v[118:121]
	v_mfma_f32_16x16x32_bf16 v[114:117], v[166:169], v[180:183], v[114:117]
	v_mfma_f32_16x16x32_bf16 v[102:105], v[146:149], v[188:191], v[102:105]
	v_mfma_f32_16x16x32_bf16 v[98:101], v[166:169], v[188:191], v[98:101]
	v_mfma_f32_16x16x32_bf16 v[86:89], v[146:149], v[196:199], v[86:89]
	v_mfma_f32_16x16x32_bf16 v[82:85], v[166:169], v[196:199], v[82:85]
	v_mfma_f32_16x16x32_bf16 v[70:73], v[146:149], v[204:207], v[70:73]
	v_mfma_f32_16x16x32_bf16 v[66:69], v[166:169], v[204:207], v[66:69]
	v_mfma_f32_16x16x32_bf16 v[118:121], v[162:165], v[184:187], v[118:121]
	v_mfma_f32_16x16x32_bf16 v[114:117], v[176:179], v[184:187], v[114:117]
	v_mfma_f32_16x16x32_bf16 v[102:105], v[162:165], v[192:195], v[102:105]
	v_mfma_f32_16x16x32_bf16 v[98:101], v[176:179], v[192:195], v[98:101]
	v_mfma_f32_16x16x32_bf16 v[86:89], v[162:165], v[200:203], v[86:89]
	v_mfma_f32_16x16x32_bf16 v[82:85], v[176:179], v[200:203], v[82:85]
	v_mfma_f32_16x16x32_bf16 v[70:73], v[162:165], v[224:227], v[70:73]
	v_mfma_f32_16x16x32_bf16 v[66:69], v[176:179], v[224:227], v[66:69]
	s_setprio 0
	s_barrier
	s_add_i32 vcc_lo, vcc_lo, s0
	v_lshl_add_u64 v[170:171], s[96:97], 0, v[154:155]
	s_mov_b32 m0, vcc_lo
	ds_read_b128 v[180:183], v173 offset:16384
	ds_read_b128 v[184:187], v173 offset:17408
	ds_read_b128 v[188:191], v173 offset:18432
	ds_read_b128 v[192:195], v173 offset:19456
	ds_read_b128 v[196:199], v173 offset:20480
	ds_read_b128 v[200:203], v173 offset:21504
	ds_read_b128 v[204:207], v173 offset:22528
	ds_read_b128 v[224:227], v173 offset:23552
	global_load_lds_dwordx4 v[170:171], off
	s_add_i32 m0, vcc_lo, 0x2000
	v_lshl_add_u64 v[228:229], s[96:97], 0, v[150:151]
	s_add_u32 s96, s96, s38
	s_addc_u32 s97, s97, s39
	s_add_i32 s95, s95, s0
	global_load_lds_dwordx4 v[228:229], off
	v_lshl_add_u64 v[230:231], s[96:97], 0, v[154:155]
	s_mov_b32 m0, s95
	v_lshl_add_u64 v[232:233], s[96:97], 0, v[150:151]
	global_load_lds_dwordx4 v[230:231], off
	s_add_i32 m0, s95, 0x2000
	v_lshl_add_u64 v[234:235], s[74:75], 0, v[156:157]
	global_load_lds_dwordx4 v[232:233], off
	s_mov_b32 m0, s1
	v_lshl_add_u64 v[238:239], s[74:75], 0, v[152:153]
	global_load_lds_dwordx4 v[234:235], off
	s_mov_b32 m0, s5
	s_nop 0
	global_load_lds_dwordx4 v[238:239], off
	s_waitcnt vmcnt(8)
	s_waitcnt lgkmcnt(0)
	s_barrier
; #define PG8_STAGE(bufoff, gbase, voff) do { _Pragma("unroll") for (int _i = 0; _i < 2; ++_i) \
;         __builtin_amdgcn_global_load_lds((const unsigned*)((const char*)(gbase) + (voff)[_i]), (PG8_LAS unsigned*)(lds + (bufoff) + ldsw + _i * 8192), 16, 0, 0); } while (0)
; #define PG8_LDA(dst, b, h) do { _Pragma("unroll") for (int m = 0; m < 4; ++m) _Pragma("unroll") for (int k = 0; k < 2; ++k) dst[m][k] = *(const PG8_LAS bf16x8*)(lds + PG8_SA(b, h) + aoff + m * 2048 + k * 1024); } while (0)
; #define PG8_LDB(dst, b, h) do { _Pragma("unroll") for (int n = 0; n < 2; ++n) _Pragma("unroll") for (int k = 0; k < 2; ++k) dst[n][k] = *(const PG8_LAS bf16x8*)(lds + PG8_SB(b, h) + boff + n * 2048 + k * 1024); } while (0)
; #define PG8_MMA(ai, bj, At, Bt) do { __builtin_amdgcn_s_setprio(1); _Pragma("unroll") for (int m = 0; m < 4; ++m) _Pragma("unroll") for (int n = 0; n < 2; ++n) _Pragma("unroll") for (int k = 0; k < 2; ++k) \
;         acc[ai][bj][m][n] = __builtin_amdgcn_mfma_f32_16x16x32_bf16(Bt[n][k], At[m][k], acc[ai][bj][m][n], 0, 0, 0); __builtin_amdgcn_s_setprio(0); } while (0)
; #define PG8_WAIT_V(n) asm volatile("s_waitcnt vmcnt(" #n ")" ::: "memory")
; #define PG8_WAIT_L(n) asm volatile("s_waitcnt lgkmcnt(" #n ")" ::: "memory")
; #define PG8_BAR __builtin_amdgcn_s_barrier()
; #define PG8_SCHED __builtin_amdgcn_sched_barrier(0)
; template <class Epi, class Sched, bool ALIGN_EPI = false, bool SP2 = false>
; __device__ __forceinline__ void gemm_phase(PG8_LAS unsigned char* lds, const Gemm g, const Sched& S, const Epi& E, const int wave0) {
;     ...
;             PG8_WAIT_V(8); PG8_WAIT_L(0); PG8_BAR; PG8_MMA(1, 0, At, B0); PG8_MMA(1, 1, At, B1); PG8_BAR; PG8_SCHED;
;             PG8_LDB(B0, 1, 0); PG8_LDB(B1, 1, 1); PG8_SCHED; PG8_LDA(At, 1, 0); PG8_STAGE(PG8_SA(0, 1), a2 + hstepA, voffA);
;             PG8_WAIT_V(8); PG8_WAIT_L(0); PG8_BAR; PG8_MMA(0, 0, At, B0); PG8_MMA(0, 1, At, B1); PG8_BAR; PG8_SCHED;
	s_setprio 1
	s_waitcnt lgkmcnt(0)
	v_mfma_f32_16x16x32_bf16 v[62:65], v[130:133], v[180:183], v[62:65]
	v_mfma_f32_16x16x32_bf16 v[58:61], v[138:141], v[180:183], v[58:61]
	v_mfma_f32_16x16x32_bf16 v[46:49], v[130:133], v[188:191], v[46:49]
	v_mfma_f32_16x16x32_bf16 v[42:45], v[138:141], v[188:191], v[42:45]
	v_mfma_f32_16x16x32_bf16 v[30:33], v[130:133], v[196:199], v[30:33]
	v_mfma_f32_16x16x32_bf16 v[26:29], v[138:141], v[196:199], v[26:29]
	v_mfma_f32_16x16x32_bf16 v[14:17], v[130:133], v[204:207], v[14:17]
	v_mfma_f32_16x16x32_bf16 v[10:13], v[138:141], v[204:207], v[10:13]
	v_mfma_f32_16x16x32_bf16 v[62:65], v[134:137], v[184:187], v[62:65]
	v_mfma_f32_16x16x32_bf16 v[58:61], v[142:145], v[184:187], v[58:61]
	v_mfma_f32_16x16x32_bf16 v[46:49], v[134:137], v[192:195], v[46:49]
	v_mfma_f32_16x16x32_bf16 v[42:45], v[142:145], v[192:195], v[42:45]
	v_mfma_f32_16x16x32_bf16 v[30:33], v[134:137], v[200:203], v[30:33]
	v_mfma_f32_16x16x32_bf16 v[26:29], v[142:145], v[200:203], v[26:29]
	v_mfma_f32_16x16x32_bf16 v[14:17], v[134:137], v[224:227], v[14:17]
	v_mfma_f32_16x16x32_bf16 v[10:13], v[142:145], v[224:227], v[10:13]
	v_mfma_f32_16x16x32_bf16 v[54:57], v[146:149], v[180:183], v[54:57]
	v_mfma_f32_16x16x32_bf16 v[50:53], v[166:169], v[180:183], v[50:53]
	v_mfma_f32_16x16x32_bf16 v[38:41], v[146:149], v[188:191], v[38:41]
	v_mfma_f32_16x16x32_bf16 v[34:37], v[166:169], v[188:191], v[34:37]
	v_mfma_f32_16x16x32_bf16 v[22:25], v[146:149], v[196:199], v[22:25]
	v_mfma_f32_16x16x32_bf16 v[18:21], v[166:169], v[196:199], v[18:21]
	v_mfma_f32_16x16x32_bf16 v[6:9], v[146:149], v[204:207], v[6:9]
	v_mfma_f32_16x16x32_bf16 v[2:5], v[166:169], v[204:207], v[2:5]
	v_mfma_f32_16x16x32_bf16 v[54:57], v[162:165], v[184:187], v[54:57]
	v_mfma_f32_16x16x32_bf16 v[50:53], v[176:179], v[184:187], v[50:53]
	v_mfma_f32_16x16x32_bf16 v[38:41], v[162:165], v[192:195], v[38:41]
	v_mfma_f32_16x16x32_bf16 v[34:37], v[176:179], v[192:195], v[34:37]
	v_mfma_f32_16x16x32_bf16 v[22:25], v[162:165], v[200:203], v[22:25]
	v_mfma_f32_16x16x32_bf16 v[18:21], v[176:179], v[200:203], v[18:21]
	v_mfma_f32_16x16x32_bf16 v[6:9], v[162:165], v[224:227], v[6:9]
	v_mfma_f32_16x16x32_bf16 v[2:5], v[176:179], v[224:227], v[2:5]
	s_setprio 0
	s_barrier
	s_add_i32 s95, 0, 0x18000
	s_add_i32 s96, 0, 0x1c000
	v_add_u32_e32 v142, s95, v172
	v_add_u32_e32 v175, s96, v172
	ds_read_b128 v[130:133], v142
	ds_read_b128 v[134:137], v142 offset:1024
	ds_read_b128 v[138:141], v142 offset:2048
	ds_read_b128 v[142:145], v142 offset:3072
	ds_read_b128 v[146:149], v175
	ds_read_b128 v[162:165], v175 offset:1024
	ds_read_b128 v[166:169], v175 offset:2048
	ds_read_b128 v[176:179], v175 offset:3072
	s_add_u32 s74, s74, s36
	s_addc_u32 s75, s75, s37
	s_mov_b32 m0, s30
	v_lshl_add_u64 v[240:241], s[74:75], 0, v[156:157]
	ds_read_b128 v[180:183], v173 offset:32768
	ds_read_b128 v[184:187], v173 offset:33792
	ds_read_b128 v[188:191], v173 offset:34816
	ds_read_b128 v[192:195], v173 offset:35840
	ds_read_b128 v[196:199], v173 offset:36864
	ds_read_b128 v[200:203], v173 offset:37888
	ds_read_b128 v[204:207], v173 offset:38912
	ds_read_b128 v[224:227], v173 offset:39936
	global_load_lds_dwordx4 v[240:241], off
	v_lshl_add_u64 v[240:241], s[74:75], 0, v[152:153]
	s_mov_b32 m0, s48
	s_nop 0
	global_load_lds_dwordx4 v[240:241], off
	s_waitcnt vmcnt(8)
	s_waitcnt lgkmcnt(0)
	s_barrier
	s_setprio 1
	s_waitcnt lgkmcnt(0)
	v_mfma_f32_16x16x32_bf16 v[122:125], v[130:133], v[180:183], v[122:125]
	v_mfma_f32_16x16x32_bf16 v[126:129], v[138:141], v[180:183], v[126:129]
	v_mfma_f32_16x16x32_bf16 v[110:113], v[130:133], v[188:191], v[110:113]
	v_mfma_f32_16x16x32_bf16 v[106:109], v[138:141], v[188:191], v[106:109]
	v_mfma_f32_16x16x32_bf16 v[94:97], v[130:133], v[196:199], v[94:97]
	v_mfma_f32_16x16x32_bf16 v[90:93], v[138:141], v[196:199], v[90:93]
	v_mfma_f32_16x16x32_bf16 v[78:81], v[130:133], v[204:207], v[78:81]
	v_mfma_f32_16x16x32_bf16 v[74:77], v[138:141], v[204:207], v[74:77]
	v_mfma_f32_16x16x32_bf16 v[122:125], v[134:137], v[184:187], v[122:125]
	v_mfma_f32_16x16x32_bf16 v[126:129], v[142:145], v[184:187], v[126:129]
	v_mfma_f32_16x16x32_bf16 v[110:113], v[134:137], v[192:195], v[110:113]
	v_mfma_f32_16x16x32_bf16 v[106:109], v[142:145], v[192:195], v[106:109]
	v_mfma_f32_16x16x32_bf16 v[94:97], v[134:137], v[200:203], v[94:97]
	v_mfma_f32_16x16x32_bf16 v[90:93], v[142:145], v[200:203], v[90:93]
	v_mfma_f32_16x16x32_bf16 v[78:81], v[134:137], v[224:227], v[78:81]
	v_mfma_f32_16x16x32_bf16 v[74:77], v[142:145], v[224:227], v[74:77]
	v_mfma_f32_16x16x32_bf16 v[118:121], v[146:149], v[180:183], v[118:121]
	v_mfma_f32_16x16x32_bf16 v[114:117], v[166:169], v[180:183], v[114:117]
	v_mfma_f32_16x16x32_bf16 v[102:105], v[146:149], v[188:191], v[102:105]
	v_mfma_f32_16x16x32_bf16 v[98:101], v[166:169], v[188:191], v[98:101]
	v_mfma_f32_16x16x32_bf16 v[86:89], v[146:149], v[196:199], v[86:89]
	v_mfma_f32_16x16x32_bf16 v[82:85], v[166:169], v[196:199], v[82:85]
	v_mfma_f32_16x16x32_bf16 v[70:73], v[146:149], v[204:207], v[70:73]
	v_mfma_f32_16x16x32_bf16 v[66:69], v[166:169], v[204:207], v[66:69]
	v_mfma_f32_16x16x32_bf16 v[118:121], v[162:165], v[184:187], v[118:121]
	v_mfma_f32_16x16x32_bf16 v[114:117], v[176:179], v[184:187], v[114:117]
	v_mfma_f32_16x16x32_bf16 v[102:105], v[162:165], v[192:195], v[102:105]
	v_mfma_f32_16x16x32_bf16 v[98:101], v[176:179], v[192:195], v[98:101]
	v_mfma_f32_16x16x32_bf16 v[86:89], v[162:165], v[200:203], v[86:89]
	v_mfma_f32_16x16x32_bf16 v[82:85], v[176:179], v[200:203], v[82:85]
	v_mfma_f32_16x16x32_bf16 v[70:73], v[162:165], v[224:227], v[70:73]
	v_mfma_f32_16x16x32_bf16 v[66:69], v[176:179], v[224:227], v[66:69]
	s_setprio 0
	s_barrier
; #define PG8_STAGE(bufoff, gbase, voff) do { _Pragma("unroll") for (int _i = 0; _i < 2; ++_i) \
;         __builtin_amdgcn_global_load_lds((const unsigned*)((const char*)(gbase) + (voff)[_i]), (PG8_LAS unsigned*)(lds + (bufoff) + ldsw + _i * 8192), 16, 0, 0); } while (0)
; #define PG8_LDA(dst, b, h) do { _Pragma("unroll") for (int m = 0; m < 4; ++m) _Pragma("unroll") for (int k = 0; k < 2; ++k) dst[m][k] = *(const PG8_LAS bf16x8*)(lds + PG8_SA(b, h) + aoff + m * 2048 + k * 1024); } while (0)
; #define PG8_MMA(ai, bj, At, Bt) do { __builtin_amdgcn_s_setprio(1); _Pragma("unroll") for (int m = 0; m < 4; ++m) _Pragma("unroll") for (int n = 0; n < 2; ++n) _Pragma("unroll") for (int k = 0; k < 2; ++k) \
;         acc[ai][bj][m][n] = __builtin_amdgcn_mfma_f32_16x16x32_bf16(Bt[n][k], At[m][k], acc[ai][bj][m][n], 0, 0, 0); __builtin_amdgcn_s_setprio(0); } while (0)
; #define PG8_WAIT_V(n) asm volatile("s_waitcnt vmcnt(" #n ")" ::: "memory")
; #define PG8_WAIT_L(n) asm volatile("s_waitcnt lgkmcnt(" #n ")" ::: "memory")
; #define PG8_BAR __builtin_amdgcn_s_barrier()
; #define PG8_SCHED __builtin_amdgcn_sched_barrier(0)
; template <class Epi, class Sched, bool ALIGN_EPI = false, bool SP2 = false>
; __device__ __forceinline__ void gemm_phase(PG8_LAS unsigned char* lds, const Gemm g, const Sched& S, const Epi& E, const int wave0) {
;     ...
;             PG8_LDA(At, 1, 1); PG8_STAGE(PG8_SB(1, 0), b3, voffB); PG8_STAGE(PG8_SB(1, 1), b3 + hstepB, voffB); PG8_STAGE(PG8_SA(1, 0), a3, voffA);
;             PG8_WAIT_V(8); PG8_WAIT_L(0); PG8_BAR; PG8_MMA(1, 0, At, B0); PG8_MMA(1, 1, At, B1); PG8_BAR; PG8_SCHED;
	s_add_i32 s74, s95, s0
	v_lshl_add_u64 v[170:171], v[170:171], 0, s[64:65]
	s_mov_b32 m0, s74
	ds_read_b128 v[180:183], v173 offset:49152
	ds_read_b128 v[184:187], v173 offset:50176
	ds_read_b128 v[188:191], v173 offset:51200
	ds_read_b128 v[192:195], v173 offset:52224
	ds_read_b128 v[196:199], v173 offset:53248
	ds_read_b128 v[200:203], v173 offset:54272
	ds_read_b128 v[204:207], v173 offset:55296
	ds_read_b128 v[224:227], v173 offset:56320
	global_load_lds_dwordx4 v[170:171], off
	v_lshl_add_u64 v[170:171], v[228:229], 0, s[64:65]
	s_add_i32 m0, s74, 0x2000
	s_add_i32 s74, s96, s0
	global_load_lds_dwordx4 v[170:171], off
	v_lshl_add_u64 v[170:171], v[230:231], 0, s[64:65]
	s_mov_b32 m0, s74
	s_nop 0
	global_load_lds_dwordx4 v[170:171], off
	v_lshl_add_u64 v[170:171], v[232:233], 0, s[64:65]
	s_add_i32 m0, s74, 0x2000
	s_nop 0
	global_load_lds_dwordx4 v[170:171], off
	v_lshl_add_u64 v[170:171], v[234:235], 0, s[64:65]
	s_mov_b32 m0, s82
	s_nop 0
	global_load_lds_dwordx4 v[170:171], off
	v_lshl_add_u64 v[170:171], v[238:239], 0, s[64:65]
	s_mov_b32 m0, s83
	s_nop 0
	global_load_lds_dwordx4 v[170:171], off
	s_waitcnt vmcnt(8)
	s_waitcnt lgkmcnt(0)
	s_barrier
	s_setprio 1
	s_waitcnt lgkmcnt(0)
	v_mfma_f32_16x16x32_bf16 v[62:65], v[130:133], v[180:183], v[62:65]
	v_mfma_f32_16x16x32_bf16 v[58:61], v[138:141], v[180:183], v[58:61]
	v_mfma_f32_16x16x32_bf16 v[46:49], v[130:133], v[188:191], v[46:49]
	v_mfma_f32_16x16x32_bf16 v[42:45], v[138:141], v[188:191], v[42:45]
	v_mfma_f32_16x16x32_bf16 v[30:33], v[130:133], v[196:199], v[30:33]
	v_mfma_f32_16x16x32_bf16 v[26:29], v[138:141], v[196:199], v[26:29]
	v_mfma_f32_16x16x32_bf16 v[14:17], v[130:133], v[204:207], v[14:17]
	v_mfma_f32_16x16x32_bf16 v[10:13], v[138:141], v[204:207], v[10:13]
	v_mfma_f32_16x16x32_bf16 v[62:65], v[134:137], v[184:187], v[62:65]
	v_mfma_f32_16x16x32_bf16 v[58:61], v[142:145], v[184:187], v[58:61]
	v_mfma_f32_16x16x32_bf16 v[46:49], v[134:137], v[192:195], v[46:49]
	v_mfma_f32_16x16x32_bf16 v[42:45], v[142:145], v[192:195], v[42:45]
	v_mfma_f32_16x16x32_bf16 v[30:33], v[134:137], v[200:203], v[30:33]
	v_mfma_f32_16x16x32_bf16 v[26:29], v[142:145], v[200:203], v[26:29]
	v_mfma_f32_16x16x32_bf16 v[14:17], v[134:137], v[224:227], v[14:17]
	v_mfma_f32_16x16x32_bf16 v[10:13], v[142:145], v[224:227], v[10:13]
	v_mfma_f32_16x16x32_bf16 v[54:57], v[146:149], v[180:183], v[54:57]
	v_mfma_f32_16x16x32_bf16 v[50:53], v[166:169], v[180:183], v[50:53]
	v_mfma_f32_16x16x32_bf16 v[38:41], v[146:149], v[188:191], v[38:41]
	v_mfma_f32_16x16x32_bf16 v[34:37], v[166:169], v[188:191], v[34:37]
	v_mfma_f32_16x16x32_bf16 v[22:25], v[146:149], v[196:199], v[22:25]
	v_mfma_f32_16x16x32_bf16 v[18:21], v[166:169], v[196:199], v[18:21]
	v_mfma_f32_16x16x32_bf16 v[6:9], v[146:149], v[204:207], v[6:9]
	v_mfma_f32_16x16x32_bf16 v[2:5], v[166:169], v[204:207], v[2:5]
	v_mfma_f32_16x16x32_bf16 v[54:57], v[162:165], v[184:187], v[54:57]
	v_mfma_f32_16x16x32_bf16 v[50:53], v[176:179], v[184:187], v[50:53]
	v_mfma_f32_16x16x32_bf16 v[38:41], v[162:165], v[192:195], v[38:41]
	v_mfma_f32_16x16x32_bf16 v[34:37], v[176:179], v[192:195], v[34:37]
	v_mfma_f32_16x16x32_bf16 v[22:25], v[162:165], v[200:203], v[22:25]
	v_mfma_f32_16x16x32_bf16 v[18:21], v[176:179], v[200:203], v[18:21]
	v_mfma_f32_16x16x32_bf16 v[6:9], v[162:165], v[224:227], v[6:9]
	v_mfma_f32_16x16x32_bf16 v[2:5], v[176:179], v[224:227], v[2:5]
	s_setprio 0
	s_barrier
	s_add_u32 s92, s92, 0x100
	s_addc_u32 s93, s93, 0
	s_add_u32 s72, s72, 0x100
	s_addc_u32 s73, s73, 0
	s_cmp_ge_i32 s94, s77
	s_mov_b32 s74, s94
	s_cbranch_scc0 .LBB0_853
	v_readlane_b32 s96, v255, 16
	v_readlane_b32 s94, v255, 15
	v_readlane_b32 s97, v255, 17
	v_readlane_b32 s95, v255, 18

; #define PG8_STAGE(bufoff, gbase, voff) do { _Pragma("unroll") for (int _i = 0; _i < 2; ++_i) \
;         __builtin_amdgcn_global_load_lds((const unsigned*)((const char*)(gbase) + (voff)[_i]), (PG8_LAS unsigned*)(lds + (bufoff) + ldsw + _i * 8192), 16, 0, 0); } while (0)
; #define PG8_LDA(dst, b, h) do { _Pragma("unroll") for (int m = 0; m < 4; ++m) _Pragma("unroll") for (int k = 0; k < 2; ++k) dst[m][k] = *(const PG8_LAS bf16x8*)(lds + PG8_SA(b, h) + aoff + m * 2048 + k * 1024); } while (0)
; #define PG8_LDB(dst, b, h) do { _Pragma("unroll") for (int n = 0; n < 2; ++n) _Pragma("unroll") for (int k = 0; k < 2; ++k) dst[n][k] = *(const PG8_LAS bf16x8*)(lds + PG8_SB(b, h) + boff + n * 2048 + k * 1024); } while (0)
; #define PG8_MMA(ai, bj, At, Bt) do { __builtin_amdgcn_s_setprio(1); _Pragma("unroll") for (int m = 0; m < 4; ++m) _Pragma("unroll") for (int n = 0; n < 2; ++n) _Pragma("unroll") for (int k = 0; k < 2; ++k) \
;         acc[ai][bj][m][n] = __builtin_amdgcn_mfma_f32_16x16x32_bf16(Bt[n][k], At[m][k], acc[ai][bj][m][n], 0, 0, 0); __builtin_amdgcn_s_setprio(0); } while (0)
; #define PG8_WAIT_V(n) asm volatile("s_waitcnt vmcnt(" #n ")" ::: "memory")
; #define PG8_BAR __builtin_amdgcn_s_barrier()
; template <class Epi, class Sched, bool ALIGN_EPI = false, bool SP2 = false>
; __device__ __forceinline__ void gemm_phase(PG8_LAS unsigned char* lds, const Gemm g, const Sched& S, const Epi& E, const int wave0) {
;     ...
;         for (int t = 0; t < nt; t += 2) {
;             const bool last = (t == nt - 2);
;             const char* a1 = cA + (size_t)(t + 1) * kstep;
;             const char* a2 = last ? nA : cA + (size_t)(t + 2) * kstep; const char* b2 = last ? nB : cB + (size_t)(t + 2) * kstep;
;             const char* a3 = a2 + kstep; const char* b3 = b2 + kstep;
;             if (last && has_next) S.a_ready(nxt);
;             if constexpr (SP2) {
;             PG8_LDB(B0, 0, 0); PG8_LDB(B1, 0, 1); PG8_SCHED; PG8_LDA(At, 0, 0); PG8_STAGE(PG8_SA(1, 1), a1 + hstepA, voffA);
;             PG8_WAIT_V(8); PG8_WAIT_L(0); PG8_BAR; PG8_MMA(0, 0, At, B0); PG8_MMA(0, 1, At, B1); PG8_BAR; PG8_SCHED;
;             PG8_LDA(At, 0, 1); PG8_STAGE(PG8_SB(0, 0), b2, voffB); PG8_STAGE(PG8_SB(0, 1), b2 + hstepB, voffB); PG8_STAGE(PG8_SA(0, 0), a2, voffA);
;             PG8_WAIT_V(8); PG8_WAIT_L(0); PG8_BAR; PG8_MMA(1, 0, At, B0); PG8_MMA(1, 1, At, B1); PG8_BAR; PG8_SCHED;
.LBB0_879:
	s_add_i32 vcc_lo, s88, 2
	s_add_u32 s58, s76, 0x80
	s_addc_u32 s59, s77, 0
	s_add_i32 s61, 0, 0x10000
	s_cmp_eq_u32 s94, s88
	s_cselect_b32 s97, s45, s59
	s_cselect_b32 s96, s44, s58
	v_add_u32_e32 v149, s61, v146
	s_cselect_b32 s59, s75, s87
	s_cselect_b32 s58, s74, s84
	s_add_i32 s83, 0, 0x14000
	ds_read_b128 v[142:145], v149
	ds_read_b128 v[150:153], v149 offset:1024
	ds_read_b128 v[154:157], v149 offset:2048
	ds_read_b128 v[158:161], v149 offset:3072
	v_add_u32_e32 v149, s83, v146
	ds_read_b128 v[162:165], v149
	ds_read_b128 v[166:169], v149 offset:1024
	ds_read_b128 v[170:173], v149 offset:2048
	ds_read_b128 v[174:177], v149 offset:3072
	v_lshl_add_u64 v[206:207], s[76:77], 0, v[140:141]
	s_add_i32 m0, s90, 0xc000
	ds_read_b128 v[178:181], v148
	ds_read_b128 v[182:185], v148 offset:1024
	ds_read_b128 v[186:189], v148 offset:2048
	ds_read_b128 v[190:193], v148 offset:3072
	ds_read_b128 v[194:197], v148 offset:4096
	ds_read_b128 v[198:201], v148 offset:5120
	ds_read_b128 v[202:205], v148 offset:6144
	ds_read_b128 v[224:227], v148 offset:7168
	global_load_lds_dwordx4 v[206:207], off
	v_lshl_add_u64 v[206:207], s[76:77], 0, v[138:139]
	s_add_i32 m0, s90, 0xe000
	s_nop 0
	global_load_lds_dwordx4 v[206:207], off
	s_waitcnt vmcnt(8)
	s_waitcnt lgkmcnt(0)
	s_barrier
	s_setprio 1
	s_waitcnt lgkmcnt(0)
	v_mfma_f32_16x16x32_bf16 v[126:129], v[142:145], v[178:181], v[126:129]
	v_mfma_f32_16x16x32_bf16 v[122:125], v[154:157], v[178:181], v[122:125]
	v_mfma_f32_16x16x32_bf16 v[110:113], v[142:145], v[186:189], v[110:113]
	v_mfma_f32_16x16x32_bf16 v[106:109], v[154:157], v[186:189], v[106:109]
	v_mfma_f32_16x16x32_bf16 v[94:97], v[142:145], v[194:197], v[94:97]
	v_mfma_f32_16x16x32_bf16 v[90:93], v[154:157], v[194:197], v[90:93]
	v_mfma_f32_16x16x32_bf16 v[78:81], v[142:145], v[202:205], v[78:81]
	v_mfma_f32_16x16x32_bf16 v[74:77], v[154:157], v[202:205], v[74:77]
	v_mfma_f32_16x16x32_bf16 v[126:129], v[150:153], v[182:185], v[126:129]
	v_mfma_f32_16x16x32_bf16 v[122:125], v[158:161], v[182:185], v[122:125]
	v_mfma_f32_16x16x32_bf16 v[110:113], v[150:153], v[190:193], v[110:113]
	v_mfma_f32_16x16x32_bf16 v[106:109], v[158:161], v[190:193], v[106:109]
	v_mfma_f32_16x16x32_bf16 v[94:97], v[150:153], v[198:201], v[94:97]
	v_mfma_f32_16x16x32_bf16 v[90:93], v[158:161], v[198:201], v[90:93]
	v_mfma_f32_16x16x32_bf16 v[78:81], v[150:153], v[224:227], v[78:81]
	v_mfma_f32_16x16x32_bf16 v[74:77], v[158:161], v[224:227], v[74:77]
	v_mfma_f32_16x16x32_bf16 v[118:121], v[162:165], v[178:181], v[118:121]
	v_mfma_f32_16x16x32_bf16 v[114:117], v[170:173], v[178:181], v[114:117]
	v_mfma_f32_16x16x32_bf16 v[102:105], v[162:165], v[186:189], v[102:105]
	v_mfma_f32_16x16x32_bf16 v[98:101], v[170:173], v[186:189], v[98:101]
	v_mfma_f32_16x16x32_bf16 v[86:89], v[162:165], v[194:197], v[86:89]
	v_mfma_f32_16x16x32_bf16 v[82:85], v[170:173], v[194:197], v[82:85]
	v_mfma_f32_16x16x32_bf16 v[70:73], v[162:165], v[202:205], v[70:73]
	v_mfma_f32_16x16x32_bf16 v[66:69], v[170:173], v[202:205], v[66:69]
	v_mfma_f32_16x16x32_bf16 v[118:121], v[166:169], v[182:185], v[118:121]
	v_mfma_f32_16x16x32_bf16 v[114:117], v[174:177], v[182:185], v[114:117]
	v_mfma_f32_16x16x32_bf16 v[102:105], v[166:169], v[190:193], v[102:105]
	v_mfma_f32_16x16x32_bf16 v[98:101], v[174:177], v[190:193], v[98:101]
	v_mfma_f32_16x16x32_bf16 v[86:89], v[166:169], v[198:201], v[86:89]
	v_mfma_f32_16x16x32_bf16 v[82:85], v[174:177], v[198:201], v[82:85]
	v_mfma_f32_16x16x32_bf16 v[70:73], v[166:169], v[224:227], v[70:73]
	v_mfma_f32_16x16x32_bf16 v[66:69], v[174:177], v[224:227], v[66:69]
	s_setprio 0
	s_barrier
	s_add_i32 s61, s61, s89
	v_lshl_add_u64 v[206:207], s[58:59], 0, v[134:135]
	s_mov_b32 m0, s61
	ds_read_b128 v[178:181], v148 offset:16384
	ds_read_b128 v[182:185], v148 offset:17408
	ds_read_b128 v[186:189], v148 offset:18432
	ds_read_b128 v[190:193], v148 offset:19456
	ds_read_b128 v[194:197], v148 offset:20480
	ds_read_b128 v[198:201], v148 offset:21504
	ds_read_b128 v[202:205], v148 offset:22528
	ds_read_b128 v[224:227], v148 offset:23552
	global_load_lds_dwordx4 v[206:207], off
	s_add_i32 m0, s61, 0x2000
	v_lshl_add_u64 v[228:229], s[58:59], 0, v[130:131]
	s_add_u32 s58, s58, s38
	s_addc_u32 s59, s59, s39
	s_add_i32 s61, s83, s89
	global_load_lds_dwordx4 v[228:229], off
	v_lshl_add_u64 v[230:231], s[58:59], 0, v[134:135]
	s_mov_b32 m0, s61
	v_lshl_add_u64 v[232:233], s[58:59], 0, v[130:131]
	global_load_lds_dwordx4 v[230:231], off
	s_add_i32 m0, s61, 0x2000
	v_lshl_add_u64 v[234:235], s[96:97], 0, v[136:137]
	global_load_lds_dwordx4 v[232:233], off
	s_mov_b32 m0, s90
	v_lshl_add_u64 v[238:239], s[96:97], 0, v[132:133]
	global_load_lds_dwordx4 v[234:235], off
	s_mov_b32 m0, s91
	s_nop 0
	global_load_lds_dwordx4 v[238:239], off
	s_waitcnt vmcnt(8)
	s_waitcnt lgkmcnt(0)
	s_barrier
; #define PG8_STAGE(bufoff, gbase, voff) do { _Pragma("unroll") for (int _i = 0; _i < 2; ++_i) \
;         __builtin_amdgcn_global_load_lds((const unsigned*)((const char*)(gbase) + (voff)[_i]), (PG8_LAS unsigned*)(lds + (bufoff) + ldsw + _i * 8192), 16, 0, 0); } while (0)
; #define PG8_LDA(dst, b, h) do { _Pragma("unroll") for (int m = 0; m < 4; ++m) _Pragma("unroll") for (int k = 0; k < 2; ++k) dst[m][k] = *(const PG8_LAS bf16x8*)(lds + PG8_SA(b, h) + aoff + m * 2048 + k * 1024); } while (0)
; #define PG8_LDB(dst, b, h) do { _Pragma("unroll") for (int n = 0; n < 2; ++n) _Pragma("unroll") for (int k = 0; k < 2; ++k) dst[n][k] = *(const PG8_LAS bf16x8*)(lds + PG8_SB(b, h) + boff + n * 2048 + k * 1024); } while (0)
; #define PG8_MMA(ai, bj, At, Bt) do { __builtin_amdgcn_s_setprio(1); _Pragma("unroll") for (int m = 0; m < 4; ++m) _Pragma("unroll") for (int n = 0; n < 2; ++n) _Pragma("unroll") for (int k = 0; k < 2; ++k) \
;         acc[ai][bj][m][n] = __builtin_amdgcn_mfma_f32_16x16x32_bf16(Bt[n][k], At[m][k], acc[ai][bj][m][n], 0, 0, 0); __builtin_amdgcn_s_setprio(0); } while (0)
; #define PG8_WAIT_V(n) asm volatile("s_waitcnt vmcnt(" #n ")" ::: "memory")
; #define PG8_WAIT_L(n) asm volatile("s_waitcnt lgkmcnt(" #n ")" ::: "memory")
; #define PG8_BAR __builtin_amdgcn_s_barrier()
; #define PG8_SCHED __builtin_amdgcn_sched_barrier(0)
; template <class Epi, class Sched, bool ALIGN_EPI = false, bool SP2 = false>
; __device__ __forceinline__ void gemm_phase(PG8_LAS unsigned char* lds, const Gemm g, const Sched& S, const Epi& E, const int wave0) {
;     ...
;             PG8_WAIT_V(8); PG8_WAIT_L(0); PG8_BAR; PG8_MMA(1, 0, At, B0); PG8_MMA(1, 1, At, B1); PG8_BAR; PG8_SCHED;
;             PG8_LDB(B0, 1, 0); PG8_LDB(B1, 1, 1); PG8_SCHED; PG8_LDA(At, 1, 0); PG8_STAGE(PG8_SA(0, 1), a2 + hstepA, voffA);
;             PG8_WAIT_V(8); PG8_WAIT_L(0); PG8_BAR; PG8_MMA(0, 0, At, B0); PG8_MMA(0, 1, At, B1); PG8_BAR; PG8_SCHED;
	s_setprio 1
	s_waitcnt lgkmcnt(0)
	v_mfma_f32_16x16x32_bf16 v[62:65], v[142:145], v[178:181], v[62:65]
	v_mfma_f32_16x16x32_bf16 v[58:61], v[154:157], v[178:181], v[58:61]
	v_mfma_f32_16x16x32_bf16 v[46:49], v[142:145], v[186:189], v[46:49]
	v_mfma_f32_16x16x32_bf16 v[42:45], v[154:157], v[186:189], v[42:45]
	v_mfma_f32_16x16x32_bf16 v[30:33], v[142:145], v[194:197], v[30:33]
	v_mfma_f32_16x16x32_bf16 v[26:29], v[154:157], v[194:197], v[26:29]
	v_mfma_f32_16x16x32_bf16 v[14:17], v[142:145], v[202:205], v[14:17]
	v_mfma_f32_16x16x32_bf16 v[10:13], v[154:157], v[202:205], v[10:13]
	v_mfma_f32_16x16x32_bf16 v[62:65], v[150:153], v[182:185], v[62:65]
	v_mfma_f32_16x16x32_bf16 v[58:61], v[158:161], v[182:185], v[58:61]
	v_mfma_f32_16x16x32_bf16 v[46:49], v[150:153], v[190:193], v[46:49]
	v_mfma_f32_16x16x32_bf16 v[42:45], v[158:161], v[190:193], v[42:45]
	v_mfma_f32_16x16x32_bf16 v[30:33], v[150:153], v[198:201], v[30:33]
	v_mfma_f32_16x16x32_bf16 v[26:29], v[158:161], v[198:201], v[26:29]
	v_mfma_f32_16x16x32_bf16 v[14:17], v[150:153], v[224:227], v[14:17]
	v_mfma_f32_16x16x32_bf16 v[10:13], v[158:161], v[224:227], v[10:13]
	v_mfma_f32_16x16x32_bf16 v[54:57], v[162:165], v[178:181], v[54:57]
	v_mfma_f32_16x16x32_bf16 v[50:53], v[170:173], v[178:181], v[50:53]
	v_mfma_f32_16x16x32_bf16 v[38:41], v[162:165], v[186:189], v[38:41]
	v_mfma_f32_16x16x32_bf16 v[34:37], v[170:173], v[186:189], v[34:37]
	v_mfma_f32_16x16x32_bf16 v[22:25], v[162:165], v[194:197], v[22:25]
	v_mfma_f32_16x16x32_bf16 v[18:21], v[170:173], v[194:197], v[18:21]
	v_mfma_f32_16x16x32_bf16 v[6:9], v[162:165], v[202:205], v[6:9]
	v_mfma_f32_16x16x32_bf16 v[2:5], v[170:173], v[202:205], v[2:5]
	v_mfma_f32_16x16x32_bf16 v[54:57], v[166:169], v[182:185], v[54:57]
	v_mfma_f32_16x16x32_bf16 v[50:53], v[174:177], v[182:185], v[50:53]
	v_mfma_f32_16x16x32_bf16 v[38:41], v[166:169], v[190:193], v[38:41]
	v_mfma_f32_16x16x32_bf16 v[34:37], v[174:177], v[190:193], v[34:37]
	v_mfma_f32_16x16x32_bf16 v[22:25], v[166:169], v[198:201], v[22:25]
	v_mfma_f32_16x16x32_bf16 v[18:21], v[174:177], v[198:201], v[18:21]
	v_mfma_f32_16x16x32_bf16 v[6:9], v[166:169], v[224:227], v[6:9]
	v_mfma_f32_16x16x32_bf16 v[2:5], v[174:177], v[224:227], v[2:5]
	s_setprio 0
	s_barrier
	s_add_i32 s61, 0, 0x18000
	v_add_u32_e32 v149, s61, v146
	s_add_i32 s83, 0, 0x1c000
	ds_read_b128 v[142:145], v149
	ds_read_b128 v[150:153], v149 offset:1024
	ds_read_b128 v[154:157], v149 offset:2048
	ds_read_b128 v[158:161], v149 offset:3072
	v_add_u32_e32 v149, s83, v146
	ds_read_b128 v[162:165], v149
	ds_read_b128 v[166:169], v149 offset:1024
	ds_read_b128 v[170:173], v149 offset:2048
	ds_read_b128 v[174:177], v149 offset:3072
	s_add_u32 s58, s96, s36
	s_addc_u32 s59, s97, s37
	s_mov_b32 m0, s92
	v_lshl_add_u64 v[240:241], s[58:59], 0, v[136:137]
	ds_read_b128 v[178:181], v148 offset:32768
	ds_read_b128 v[182:185], v148 offset:33792
	ds_read_b128 v[186:189], v148 offset:34816
	ds_read_b128 v[190:193], v148 offset:35840
	ds_read_b128 v[194:197], v148 offset:36864
	ds_read_b128 v[198:201], v148 offset:37888
	ds_read_b128 v[202:205], v148 offset:38912
	ds_read_b128 v[224:227], v148 offset:39936
	global_load_lds_dwordx4 v[240:241], off
	v_lshl_add_u64 v[240:241], s[58:59], 0, v[132:133]
	s_mov_b32 m0, s93
	s_nop 0
	global_load_lds_dwordx4 v[240:241], off
	s_waitcnt vmcnt(8)
	s_waitcnt lgkmcnt(0)
	s_barrier
	s_setprio 1
	s_waitcnt lgkmcnt(0)
	v_mfma_f32_16x16x32_bf16 v[126:129], v[142:145], v[178:181], v[126:129]
	v_mfma_f32_16x16x32_bf16 v[122:125], v[154:157], v[178:181], v[122:125]
	v_mfma_f32_16x16x32_bf16 v[110:113], v[142:145], v[186:189], v[110:113]
	v_mfma_f32_16x16x32_bf16 v[106:109], v[154:157], v[186:189], v[106:109]
	v_mfma_f32_16x16x32_bf16 v[94:97], v[142:145], v[194:197], v[94:97]
	v_mfma_f32_16x16x32_bf16 v[90:93], v[154:157], v[194:197], v[90:93]
	v_mfma_f32_16x16x32_bf16 v[78:81], v[142:145], v[202:205], v[78:81]
	v_mfma_f32_16x16x32_bf16 v[74:77], v[154:157], v[202:205], v[74:77]
	v_mfma_f32_16x16x32_bf16 v[126:129], v[150:153], v[182:185], v[126:129]
	v_mfma_f32_16x16x32_bf16 v[122:125], v[158:161], v[182:185], v[122:125]
	v_mfma_f32_16x16x32_bf16 v[110:113], v[150:153], v[190:193], v[110:113]
	v_mfma_f32_16x16x32_bf16 v[106:109], v[158:161], v[190:193], v[106:109]
	v_mfma_f32_16x16x32_bf16 v[94:97], v[150:153], v[198:201], v[94:97]
	v_mfma_f32_16x16x32_bf16 v[90:93], v[158:161], v[198:201], v[90:93]
	v_mfma_f32_16x16x32_bf16 v[78:81], v[150:153], v[224:227], v[78:81]
	v_mfma_f32_16x16x32_bf16 v[74:77], v[158:161], v[224:227], v[74:77]
	v_mfma_f32_16x16x32_bf16 v[118:121], v[162:165], v[178:181], v[118:121]
	v_mfma_f32_16x16x32_bf16 v[114:117], v[170:173], v[178:181], v[114:117]
	v_mfma_f32_16x16x32_bf16 v[102:105], v[162:165], v[186:189], v[102:105]
	v_mfma_f32_16x16x32_bf16 v[98:101], v[170:173], v[186:189], v[98:101]
	v_mfma_f32_16x16x32_bf16 v[86:89], v[162:165], v[194:197], v[86:89]
	v_mfma_f32_16x16x32_bf16 v[82:85], v[170:173], v[194:197], v[82:85]
	v_mfma_f32_16x16x32_bf16 v[70:73], v[162:165], v[202:205], v[70:73]
	v_mfma_f32_16x16x32_bf16 v[66:69], v[170:173], v[202:205], v[66:69]
	v_mfma_f32_16x16x32_bf16 v[118:121], v[166:169], v[182:185], v[118:121]
	v_mfma_f32_16x16x32_bf16 v[114:117], v[174:177], v[182:185], v[114:117]
	v_mfma_f32_16x16x32_bf16 v[102:105], v[166:169], v[190:193], v[102:105]
	v_mfma_f32_16x16x32_bf16 v[98:101], v[174:177], v[190:193], v[98:101]
	v_mfma_f32_16x16x32_bf16 v[86:89], v[166:169], v[198:201], v[86:89]
	v_mfma_f32_16x16x32_bf16 v[82:85], v[174:177], v[198:201], v[82:85]
	v_mfma_f32_16x16x32_bf16 v[70:73], v[166:169], v[224:227], v[70:73]
	v_mfma_f32_16x16x32_bf16 v[66:69], v[174:177], v[224:227], v[66:69]
	s_setprio 0
	s_barrier
; #define PG8_STAGE(bufoff, gbase, voff) do { _Pragma("unroll") for (int _i = 0; _i < 2; ++_i) \
;         __builtin_amdgcn_global_load_lds((const unsigned*)((const char*)(gbase) + (voff)[_i]), (PG8_LAS unsigned*)(lds + (bufoff) + ldsw + _i * 8192), 16, 0, 0); } while (0)
; #define PG8_LDA(dst, b, h) do { _Pragma("unroll") for (int m = 0; m < 4; ++m) _Pragma("unroll") for (int k = 0; k < 2; ++k) dst[m][k] = *(const PG8_LAS bf16x8*)(lds + PG8_SA(b, h) + aoff + m * 2048 + k * 1024); } while (0)
; #define PG8_MMA(ai, bj, At, Bt) do { __builtin_amdgcn_s_setprio(1); _Pragma("unroll") for (int m = 0; m < 4; ++m) _Pragma("unroll") for (int n = 0; n < 2; ++n) _Pragma("unroll") for (int k = 0; k < 2; ++k) \
;         acc[ai][bj][m][n] = __builtin_amdgcn_mfma_f32_16x16x32_bf16(Bt[n][k], At[m][k], acc[ai][bj][m][n], 0, 0, 0); __builtin_amdgcn_s_setprio(0); } while (0)
; #define PG8_WAIT_V(n) asm volatile("s_waitcnt vmcnt(" #n ")" ::: "memory")
; #define PG8_WAIT_L(n) asm volatile("s_waitcnt lgkmcnt(" #n ")" ::: "memory")
; #define PG8_BAR __builtin_amdgcn_s_barrier()
; #define PG8_SCHED __builtin_amdgcn_sched_barrier(0)
; template <class Epi, class Sched, bool ALIGN_EPI = false, bool SP2 = false>
; __device__ __forceinline__ void gemm_phase(PG8_LAS unsigned char* lds, const Gemm g, const Sched& S, const Epi& E, const int wave0) {
;     ...
;             PG8_LDA(At, 1, 1); PG8_STAGE(PG8_SB(1, 0), b3, voffB); PG8_STAGE(PG8_SB(1, 1), b3 + hstepB, voffB); PG8_STAGE(PG8_SA(1, 0), a3, voffA);
;             PG8_WAIT_V(8); PG8_WAIT_L(0); PG8_BAR; PG8_MMA(1, 0, At, B0); PG8_MMA(1, 1, At, B1); PG8_BAR; PG8_SCHED;
	s_add_i32 s58, s61, s89
	v_lshl_add_u64 v[206:207], v[206:207], 0, s[64:65]
	s_mov_b32 m0, s58
	ds_read_b128 v[178:181], v148 offset:49152
	ds_read_b128 v[182:185], v148 offset:50176
	ds_read_b128 v[186:189], v148 offset:51200
	ds_read_b128 v[190:193], v148 offset:52224
	ds_read_b128 v[194:197], v148 offset:53248
	ds_read_b128 v[198:201], v148 offset:54272
	ds_read_b128 v[202:205], v148 offset:55296
	ds_read_b128 v[224:227], v148 offset:56320
	global_load_lds_dwordx4 v[206:207], off
	v_lshl_add_u64 v[206:207], v[228:229], 0, s[64:65]
	s_add_i32 m0, s58, 0x2000
	s_add_i32 s58, s83, s89
	global_load_lds_dwordx4 v[206:207], off
	v_lshl_add_u64 v[206:207], v[230:231], 0, s[64:65]
	s_mov_b32 m0, s58
	s_nop 0
	global_load_lds_dwordx4 v[206:207], off
	v_lshl_add_u64 v[206:207], v[232:233], 0, s[64:65]
	s_add_i32 m0, s58, 0x2000
	s_nop 0
	global_load_lds_dwordx4 v[206:207], off
	v_lshl_add_u64 v[206:207], v[234:235], 0, s[64:65]
	s_mov_b32 m0, s95
	s_nop 0
	global_load_lds_dwordx4 v[206:207], off
	v_lshl_add_u64 v[206:207], v[238:239], 0, s[64:65]
	s_mov_b32 m0, s82
	s_nop 0
	global_load_lds_dwordx4 v[206:207], off
	s_waitcnt vmcnt(8)
	s_waitcnt lgkmcnt(0)
	s_barrier
	s_setprio 1
	s_waitcnt lgkmcnt(0)
	v_mfma_f32_16x16x32_bf16 v[62:65], v[142:145], v[178:181], v[62:65]
	v_mfma_f32_16x16x32_bf16 v[58:61], v[154:157], v[178:181], v[58:61]
	v_mfma_f32_16x16x32_bf16 v[46:49], v[142:145], v[186:189], v[46:49]
	v_mfma_f32_16x16x32_bf16 v[42:45], v[154:157], v[186:189], v[42:45]
	v_mfma_f32_16x16x32_bf16 v[30:33], v[142:145], v[194:197], v[30:33]
	v_mfma_f32_16x16x32_bf16 v[26:29], v[154:157], v[194:197], v[26:29]
	v_mfma_f32_16x16x32_bf16 v[14:17], v[142:145], v[202:205], v[14:17]
	v_mfma_f32_16x16x32_bf16 v[10:13], v[154:157], v[202:205], v[10:13]
	v_mfma_f32_16x16x32_bf16 v[62:65], v[150:153], v[182:185], v[62:65]
	v_mfma_f32_16x16x32_bf16 v[58:61], v[158:161], v[182:185], v[58:61]
	v_mfma_f32_16x16x32_bf16 v[46:49], v[150:153], v[190:193], v[46:49]
	v_mfma_f32_16x16x32_bf16 v[42:45], v[158:161], v[190:193], v[42:45]
	v_mfma_f32_16x16x32_bf16 v[30:33], v[150:153], v[198:201], v[30:33]
	v_mfma_f32_16x16x32_bf16 v[26:29], v[158:161], v[198:201], v[26:29]
	v_mfma_f32_16x16x32_bf16 v[14:17], v[150:153], v[224:227], v[14:17]
	v_mfma_f32_16x16x32_bf16 v[10:13], v[158:161], v[224:227], v[10:13]
	v_mfma_f32_16x16x32_bf16 v[54:57], v[162:165], v[178:181], v[54:57]
	v_mfma_f32_16x16x32_bf16 v[50:53], v[170:173], v[178:181], v[50:53]
	v_mfma_f32_16x16x32_bf16 v[38:41], v[162:165], v[186:189], v[38:41]
	v_mfma_f32_16x16x32_bf16 v[34:37], v[170:173], v[186:189], v[34:37]
	v_mfma_f32_16x16x32_bf16 v[22:25], v[162:165], v[194:197], v[22:25]
	v_mfma_f32_16x16x32_bf16 v[18:21], v[170:173], v[194:197], v[18:21]
	v_mfma_f32_16x16x32_bf16 v[6:9], v[162:165], v[202:205], v[6:9]
	v_mfma_f32_16x16x32_bf16 v[2:5], v[170:173], v[202:205], v[2:5]
	v_mfma_f32_16x16x32_bf16 v[54:57], v[166:169], v[182:185], v[54:57]
	v_mfma_f32_16x16x32_bf16 v[50:53], v[174:177], v[182:185], v[50:53]
	v_mfma_f32_16x16x32_bf16 v[38:41], v[166:169], v[190:193], v[38:41]
	v_mfma_f32_16x16x32_bf16 v[34:37], v[174:177], v[190:193], v[34:37]
	v_mfma_f32_16x16x32_bf16 v[22:25], v[166:169], v[198:201], v[22:25]
	v_mfma_f32_16x16x32_bf16 v[18:21], v[174:177], v[198:201], v[18:21]
	v_mfma_f32_16x16x32_bf16 v[6:9], v[166:169], v[224:227], v[6:9]
	v_mfma_f32_16x16x32_bf16 v[2:5], v[174:177], v[224:227], v[2:5]
	s_setprio 0
	s_barrier
	s_add_u32 s84, s84, 0x100
	s_addc_u32 s87, s87, 0
	s_add_u32 s76, s76, 0x100
	s_addc_u32 s77, s77, 0
	s_cmp_ge_i32 vcc_lo, s5
	s_mov_b32 s88, vcc_lo
	s_cbranch_scc0 .LBB0_879

; #define PG8_STAGE(bufoff, gbase, voff) do { _Pragma("unroll") for (int _i = 0; _i < 2; ++_i) \
;         __builtin_amdgcn_global_load_lds((const unsigned*)((const char*)(gbase) + (voff)[_i]), (PG8_LAS unsigned*)(lds + (bufoff) + ldsw + _i * 8192), 16, 0, 0); } while (0)
; #define PG8_LDA(dst, b, h) do { _Pragma("unroll") for (int m = 0; m < 4; ++m) _Pragma("unroll") for (int k = 0; k < 2; ++k) dst[m][k] = *(const PG8_LAS bf16x8*)(lds + PG8_SA(b, h) + aoff + m * 2048 + k * 1024); } while (0)
; #define PG8_LDB(dst, b, h) do { _Pragma("unroll") for (int n = 0; n < 2; ++n) _Pragma("unroll") for (int k = 0; k < 2; ++k) dst[n][k] = *(const PG8_LAS bf16x8*)(lds + PG8_SB(b, h) + boff + n * 2048 + k * 1024); } while (0)
; #define PG8_MMA(ai, bj, At, Bt) do { __builtin_amdgcn_s_setprio(1); _Pragma("unroll") for (int m = 0; m < 4; ++m) _Pragma("unroll") for (int n = 0; n < 2; ++n) _Pragma("unroll") for (int k = 0; k < 2; ++k) \
;         acc[ai][bj][m][n] = __builtin_amdgcn_mfma_f32_16x16x32_bf16(Bt[n][k], At[m][k], acc[ai][bj][m][n], 0, 0, 0); __builtin_amdgcn_s_setprio(0); } while (0)
; #define PG8_WAIT_V(n) asm volatile("s_waitcnt vmcnt(" #n ")" ::: "memory")
; #define PG8_BAR __builtin_amdgcn_s_barrier()
; template <class Epi, class Sched, bool ALIGN_EPI = false, bool SP2 = false>
; __device__ __forceinline__ void gemm_phase(PG8_LAS unsigned char* lds, const Gemm g, const Sched& S, const Epi& E, const int wave0) {
;     ...
;         for (int t = 0; t < nt; t += 2) {
;             const bool last = (t == nt - 2);
;             const char* a1 = cA + (size_t)(t + 1) * kstep;
;             const char* a2 = last ? nA : cA + (size_t)(t + 2) * kstep; const char* b2 = last ? nB : cB + (size_t)(t + 2) * kstep;
;             const char* a3 = a2 + kstep; const char* b3 = b2 + kstep;
;             if (last && has_next) S.a_ready(nxt);
;             if constexpr (SP2) {
;             PG8_LDB(B0, 0, 0); PG8_LDB(B1, 0, 1); PG8_SCHED; PG8_LDA(At, 0, 0); PG8_STAGE(PG8_SA(1, 1), a1 + hstepA, voffA);
;             PG8_WAIT_V(8); PG8_WAIT_L(0); PG8_BAR; PG8_MMA(0, 0, At, B0); PG8_MMA(0, 1, At, B1); PG8_BAR; PG8_SCHED;
;             PG8_LDA(At, 0, 1); PG8_STAGE(PG8_SB(0, 0), b2, voffB); PG8_STAGE(PG8_SB(0, 1), b2 + hstepB, voffB); PG8_STAGE(PG8_SA(0, 0), a2, voffA);
;             PG8_WAIT_V(8); PG8_WAIT_L(0); PG8_BAR; PG8_MMA(1, 0, At, B0); PG8_MMA(1, 1, At, B1); PG8_BAR; PG8_SCHED;
.LBB0_1174:
	s_add_i32 s89, s60, 2
	s_add_u32 s90, s58, 0x80
	s_addc_u32 s61, s59, 0
	s_add_i32 s92, 0, 0x10000
	s_cmp_eq_u32 s75, s60
	s_cselect_b32 s61, s43, s61
	s_cselect_b32 s60, s42, s90
	v_add_u32_e32 v145, s92, v142
	s_cselect_b32 s91, s57, s88
	s_cselect_b32 s90, s56, s87
	s_add_i32 s93, 0, 0x14000
	ds_read_b128 v[146:149], v145
	ds_read_b128 v[150:153], v145 offset:1024
	ds_read_b128 v[154:157], v145 offset:2048
	ds_read_b128 v[158:161], v145 offset:3072
	v_add_u32_e32 v145, s93, v142
	ds_read_b128 v[162:165], v145
	ds_read_b128 v[166:169], v145 offset:1024
	ds_read_b128 v[170:173], v145 offset:2048
	ds_read_b128 v[174:177], v145 offset:3072
	v_lshl_add_u64 v[206:207], s[58:59], 0, v[140:141]
	s_add_i32 m0, s30, 0xc000
	ds_read_b128 v[178:181], v144
	ds_read_b128 v[182:185], v144 offset:1024
	ds_read_b128 v[186:189], v144 offset:2048
	ds_read_b128 v[190:193], v144 offset:3072
	ds_read_b128 v[194:197], v144 offset:4096
	ds_read_b128 v[198:201], v144 offset:5120
	ds_read_b128 v[202:205], v144 offset:6144
	ds_read_b128 v[224:227], v144 offset:7168
	global_load_lds_dwordx4 v[206:207], off
	v_lshl_add_u64 v[206:207], s[58:59], 0, v[138:139]
	s_add_i32 m0, s30, 0xe000
	s_nop 0
	global_load_lds_dwordx4 v[206:207], off
	s_waitcnt vmcnt(8)
	s_waitcnt lgkmcnt(0)
	s_barrier
	s_setprio 1
	s_waitcnt lgkmcnt(0)
	v_mfma_f32_16x16x32_bf16 v[122:125], v[146:149], v[178:181], v[122:125]
	v_mfma_f32_16x16x32_bf16 v[126:129], v[154:157], v[178:181], v[126:129]
	v_mfma_f32_16x16x32_bf16 v[110:113], v[146:149], v[186:189], v[110:113]
	v_mfma_f32_16x16x32_bf16 v[106:109], v[154:157], v[186:189], v[106:109]
	v_mfma_f32_16x16x32_bf16 v[94:97], v[146:149], v[194:197], v[94:97]
	v_mfma_f32_16x16x32_bf16 v[90:93], v[154:157], v[194:197], v[90:93]
	v_mfma_f32_16x16x32_bf16 v[78:81], v[146:149], v[202:205], v[78:81]
	v_mfma_f32_16x16x32_bf16 v[74:77], v[154:157], v[202:205], v[74:77]
	v_mfma_f32_16x16x32_bf16 v[122:125], v[150:153], v[182:185], v[122:125]
	v_mfma_f32_16x16x32_bf16 v[126:129], v[158:161], v[182:185], v[126:129]
	v_mfma_f32_16x16x32_bf16 v[110:113], v[150:153], v[190:193], v[110:113]
	v_mfma_f32_16x16x32_bf16 v[106:109], v[158:161], v[190:193], v[106:109]
	v_mfma_f32_16x16x32_bf16 v[94:97], v[150:153], v[198:201], v[94:97]
	v_mfma_f32_16x16x32_bf16 v[90:93], v[158:161], v[198:201], v[90:93]
	v_mfma_f32_16x16x32_bf16 v[78:81], v[150:153], v[224:227], v[78:81]
	v_mfma_f32_16x16x32_bf16 v[74:77], v[158:161], v[224:227], v[74:77]
	v_mfma_f32_16x16x32_bf16 v[118:121], v[162:165], v[178:181], v[118:121]
	v_mfma_f32_16x16x32_bf16 v[114:117], v[170:173], v[178:181], v[114:117]
	v_mfma_f32_16x16x32_bf16 v[102:105], v[162:165], v[186:189], v[102:105]
	v_mfma_f32_16x16x32_bf16 v[98:101], v[170:173], v[186:189], v[98:101]
	v_mfma_f32_16x16x32_bf16 v[86:89], v[162:165], v[194:197], v[86:89]
	v_mfma_f32_16x16x32_bf16 v[82:85], v[170:173], v[194:197], v[82:85]
	v_mfma_f32_16x16x32_bf16 v[70:73], v[162:165], v[202:205], v[70:73]
	v_mfma_f32_16x16x32_bf16 v[66:69], v[170:173], v[202:205], v[66:69]
	v_mfma_f32_16x16x32_bf16 v[118:121], v[166:169], v[182:185], v[118:121]
	v_mfma_f32_16x16x32_bf16 v[114:117], v[174:177], v[182:185], v[114:117]
	v_mfma_f32_16x16x32_bf16 v[102:105], v[166:169], v[190:193], v[102:105]
	v_mfma_f32_16x16x32_bf16 v[98:101], v[174:177], v[190:193], v[98:101]
	v_mfma_f32_16x16x32_bf16 v[86:89], v[166:169], v[198:201], v[86:89]
	v_mfma_f32_16x16x32_bf16 v[82:85], v[174:177], v[198:201], v[82:85]
	v_mfma_f32_16x16x32_bf16 v[70:73], v[166:169], v[224:227], v[70:73]
	v_mfma_f32_16x16x32_bf16 v[66:69], v[174:177], v[224:227], v[66:69]
	s_setprio 0
	s_barrier
	s_add_i32 s92, s92, s5
	v_lshl_add_u64 v[206:207], s[90:91], 0, v[134:135]
	s_mov_b32 m0, s92
	ds_read_b128 v[178:181], v144 offset:16384
	ds_read_b128 v[182:185], v144 offset:17408
	ds_read_b128 v[186:189], v144 offset:18432
	ds_read_b128 v[190:193], v144 offset:19456
	ds_read_b128 v[194:197], v144 offset:20480
	ds_read_b128 v[198:201], v144 offset:21504
	ds_read_b128 v[202:205], v144 offset:22528
	ds_read_b128 v[224:227], v144 offset:23552
	global_load_lds_dwordx4 v[206:207], off
	s_add_i32 m0, s92, 0x2000
	v_lshl_add_u64 v[228:229], s[90:91], 0, v[130:131]
	s_add_u32 s90, s90, s22
	s_addc_u32 s91, s91, s23
	s_add_i32 s92, s93, s5
	global_load_lds_dwordx4 v[228:229], off
	v_lshl_add_u64 v[230:231], s[90:91], 0, v[134:135]
	s_mov_b32 m0, s92
	v_lshl_add_u64 v[232:233], s[90:91], 0, v[130:131]
	global_load_lds_dwordx4 v[230:231], off
	s_add_i32 m0, s92, 0x2000
	v_lshl_add_u64 v[234:235], s[60:61], 0, v[136:137]
	global_load_lds_dwordx4 v[232:233], off
	s_mov_b32 m0, s30
	v_lshl_add_u64 v[238:239], s[60:61], 0, v[132:133]
	global_load_lds_dwordx4 v[234:235], off
	s_mov_b32 m0, s48
	s_nop 0
	global_load_lds_dwordx4 v[238:239], off
	s_waitcnt vmcnt(8)
	s_waitcnt lgkmcnt(0)
	s_barrier
; #define PG8_STAGE(bufoff, gbase, voff) do { _Pragma("unroll") for (int _i = 0; _i < 2; ++_i) \
;         __builtin_amdgcn_global_load_lds((const unsigned*)((const char*)(gbase) + (voff)[_i]), (PG8_LAS unsigned*)(lds + (bufoff) + ldsw + _i * 8192), 16, 0, 0); } while (0)
; #define PG8_LDA(dst, b, h) do { _Pragma("unroll") for (int m = 0; m < 4; ++m) _Pragma("unroll") for (int k = 0; k < 2; ++k) dst[m][k] = *(const PG8_LAS bf16x8*)(lds + PG8_SA(b, h) + aoff + m * 2048 + k * 1024); } while (0)
; #define PG8_LDB(dst, b, h) do { _Pragma("unroll") for (int n = 0; n < 2; ++n) _Pragma("unroll") for (int k = 0; k < 2; ++k) dst[n][k] = *(const PG8_LAS bf16x8*)(lds + PG8_SB(b, h) + boff + n * 2048 + k * 1024); } while (0)
; #define PG8_MMA(ai, bj, At, Bt) do { __builtin_amdgcn_s_setprio(1); _Pragma("unroll") for (int m = 0; m < 4; ++m) _Pragma("unroll") for (int n = 0; n < 2; ++n) _Pragma("unroll") for (int k = 0; k < 2; ++k) \
;         acc[ai][bj][m][n] = __builtin_amdgcn_mfma_f32_16x16x32_bf16(Bt[n][k], At[m][k], acc[ai][bj][m][n], 0, 0, 0); __builtin_amdgcn_s_setprio(0); } while (0)
; #define PG8_WAIT_V(n) asm volatile("s_waitcnt vmcnt(" #n ")" ::: "memory")
; #define PG8_WAIT_L(n) asm volatile("s_waitcnt lgkmcnt(" #n ")" ::: "memory")
; #define PG8_BAR __builtin_amdgcn_s_barrier()
; #define PG8_SCHED __builtin_amdgcn_sched_barrier(0)
; template <class Epi, class Sched, bool ALIGN_EPI = false, bool SP2 = false>
; __device__ __forceinline__ void gemm_phase(PG8_LAS unsigned char* lds, const Gemm g, const Sched& S, const Epi& E, const int wave0) {
;     ...
;             PG8_WAIT_V(8); PG8_WAIT_L(0); PG8_BAR; PG8_MMA(1, 0, At, B0); PG8_MMA(1, 1, At, B1); PG8_BAR; PG8_SCHED;
;             PG8_LDB(B0, 1, 0); PG8_LDB(B1, 1, 1); PG8_SCHED; PG8_LDA(At, 1, 0); PG8_STAGE(PG8_SA(0, 1), a2 + hstepA, voffA);
;             PG8_WAIT_V(8); PG8_WAIT_L(0); PG8_BAR; PG8_MMA(0, 0, At, B0); PG8_MMA(0, 1, At, B1); PG8_BAR; PG8_SCHED;
	s_setprio 1
	s_waitcnt lgkmcnt(0)
	v_mfma_f32_16x16x32_bf16 v[62:65], v[146:149], v[178:181], v[62:65]
	v_mfma_f32_16x16x32_bf16 v[58:61], v[154:157], v[178:181], v[58:61]
	v_mfma_f32_16x16x32_bf16 v[46:49], v[146:149], v[186:189], v[46:49]
	v_mfma_f32_16x16x32_bf16 v[42:45], v[154:157], v[186:189], v[42:45]
	v_mfma_f32_16x16x32_bf16 v[30:33], v[146:149], v[194:197], v[30:33]
	v_mfma_f32_16x16x32_bf16 v[26:29], v[154:157], v[194:197], v[26:29]
	v_mfma_f32_16x16x32_bf16 v[14:17], v[146:149], v[202:205], v[14:17]
	v_mfma_f32_16x16x32_bf16 v[10:13], v[154:157], v[202:205], v[10:13]
	v_mfma_f32_16x16x32_bf16 v[62:65], v[150:153], v[182:185], v[62:65]
	v_mfma_f32_16x16x32_bf16 v[58:61], v[158:161], v[182:185], v[58:61]
	v_mfma_f32_16x16x32_bf16 v[46:49], v[150:153], v[190:193], v[46:49]
	v_mfma_f32_16x16x32_bf16 v[42:45], v[158:161], v[190:193], v[42:45]
	v_mfma_f32_16x16x32_bf16 v[30:33], v[150:153], v[198:201], v[30:33]
	v_mfma_f32_16x16x32_bf16 v[26:29], v[158:161], v[198:201], v[26:29]
	v_mfma_f32_16x16x32_bf16 v[14:17], v[150:153], v[224:227], v[14:17]
	v_mfma_f32_16x16x32_bf16 v[10:13], v[158:161], v[224:227], v[10:13]
	v_mfma_f32_16x16x32_bf16 v[54:57], v[162:165], v[178:181], v[54:57]
	v_mfma_f32_16x16x32_bf16 v[50:53], v[170:173], v[178:181], v[50:53]
	v_mfma_f32_16x16x32_bf16 v[38:41], v[162:165], v[186:189], v[38:41]
	v_mfma_f32_16x16x32_bf16 v[34:37], v[170:173], v[186:189], v[34:37]
	v_mfma_f32_16x16x32_bf16 v[22:25], v[162:165], v[194:197], v[22:25]
	v_mfma_f32_16x16x32_bf16 v[18:21], v[170:173], v[194:197], v[18:21]
	v_mfma_f32_16x16x32_bf16 v[6:9], v[162:165], v[202:205], v[6:9]
	v_mfma_f32_16x16x32_bf16 v[2:5], v[170:173], v[202:205], v[2:5]
	v_mfma_f32_16x16x32_bf16 v[54:57], v[166:169], v[182:185], v[54:57]
	v_mfma_f32_16x16x32_bf16 v[50:53], v[174:177], v[182:185], v[50:53]
	v_mfma_f32_16x16x32_bf16 v[38:41], v[166:169], v[190:193], v[38:41]
	v_mfma_f32_16x16x32_bf16 v[34:37], v[174:177], v[190:193], v[34:37]
	v_mfma_f32_16x16x32_bf16 v[22:25], v[166:169], v[198:201], v[22:25]
	v_mfma_f32_16x16x32_bf16 v[18:21], v[174:177], v[198:201], v[18:21]
	v_mfma_f32_16x16x32_bf16 v[6:9], v[166:169], v[224:227], v[6:9]
	v_mfma_f32_16x16x32_bf16 v[2:5], v[174:177], v[224:227], v[2:5]
	s_setprio 0
	s_barrier
	s_add_i32 s90, 0, 0x18000
	v_add_u32_e32 v145, s90, v142
	s_add_i32 s91, 0, 0x1c000
	ds_read_b128 v[146:149], v145
	ds_read_b128 v[150:153], v145 offset:1024
	ds_read_b128 v[154:157], v145 offset:2048
	ds_read_b128 v[158:161], v145 offset:3072
	v_add_u32_e32 v145, s91, v142
	ds_read_b128 v[162:165], v145
	ds_read_b128 v[166:169], v145 offset:1024
	ds_read_b128 v[170:173], v145 offset:2048
	ds_read_b128 v[174:177], v145 offset:3072
	s_add_u32 s60, s60, s20
	s_addc_u32 s61, s61, s21
	s_mov_b32 m0, s70
	v_lshl_add_u64 v[240:241], s[60:61], 0, v[136:137]
	ds_read_b128 v[178:181], v144 offset:32768
	ds_read_b128 v[182:185], v144 offset:33792
	ds_read_b128 v[186:189], v144 offset:34816
	ds_read_b128 v[190:193], v144 offset:35840
	ds_read_b128 v[194:197], v144 offset:36864
	ds_read_b128 v[198:201], v144 offset:37888
	ds_read_b128 v[202:205], v144 offset:38912
	ds_read_b128 v[224:227], v144 offset:39936
	global_load_lds_dwordx4 v[240:241], off
	v_lshl_add_u64 v[240:241], s[60:61], 0, v[132:133]
	s_mov_b32 m0, s71
	s_nop 0
	global_load_lds_dwordx4 v[240:241], off
	s_waitcnt vmcnt(8)
	s_waitcnt lgkmcnt(0)
	s_barrier
	s_setprio 1
	s_waitcnt lgkmcnt(0)
	v_mfma_f32_16x16x32_bf16 v[122:125], v[146:149], v[178:181], v[122:125]
	v_mfma_f32_16x16x32_bf16 v[126:129], v[154:157], v[178:181], v[126:129]
	v_mfma_f32_16x16x32_bf16 v[110:113], v[146:149], v[186:189], v[110:113]
	v_mfma_f32_16x16x32_bf16 v[106:109], v[154:157], v[186:189], v[106:109]
	v_mfma_f32_16x16x32_bf16 v[94:97], v[146:149], v[194:197], v[94:97]
	v_mfma_f32_16x16x32_bf16 v[90:93], v[154:157], v[194:197], v[90:93]
	v_mfma_f32_16x16x32_bf16 v[78:81], v[146:149], v[202:205], v[78:81]
	v_mfma_f32_16x16x32_bf16 v[74:77], v[154:157], v[202:205], v[74:77]
	v_mfma_f32_16x16x32_bf16 v[122:125], v[150:153], v[182:185], v[122:125]
	v_mfma_f32_16x16x32_bf16 v[126:129], v[158:161], v[182:185], v[126:129]
	v_mfma_f32_16x16x32_bf16 v[110:113], v[150:153], v[190:193], v[110:113]
	v_mfma_f32_16x16x32_bf16 v[106:109], v[158:161], v[190:193], v[106:109]
	v_mfma_f32_16x16x32_bf16 v[94:97], v[150:153], v[198:201], v[94:97]
	v_mfma_f32_16x16x32_bf16 v[90:93], v[158:161], v[198:201], v[90:93]
	v_mfma_f32_16x16x32_bf16 v[78:81], v[150:153], v[224:227], v[78:81]
	v_mfma_f32_16x16x32_bf16 v[74:77], v[158:161], v[224:227], v[74:77]
	v_mfma_f32_16x16x32_bf16 v[118:121], v[162:165], v[178:181], v[118:121]
	v_mfma_f32_16x16x32_bf16 v[114:117], v[170:173], v[178:181], v[114:117]
	v_mfma_f32_16x16x32_bf16 v[102:105], v[162:165], v[186:189], v[102:105]
	v_mfma_f32_16x16x32_bf16 v[98:101], v[170:173], v[186:189], v[98:101]
	v_mfma_f32_16x16x32_bf16 v[86:89], v[162:165], v[194:197], v[86:89]
	v_mfma_f32_16x16x32_bf16 v[82:85], v[170:173], v[194:197], v[82:85]
	v_mfma_f32_16x16x32_bf16 v[70:73], v[162:165], v[202:205], v[70:73]
	v_mfma_f32_16x16x32_bf16 v[66:69], v[170:173], v[202:205], v[66:69]
	v_mfma_f32_16x16x32_bf16 v[118:121], v[166:169], v[182:185], v[118:121]
	v_mfma_f32_16x16x32_bf16 v[114:117], v[174:177], v[182:185], v[114:117]
	v_mfma_f32_16x16x32_bf16 v[102:105], v[166:169], v[190:193], v[102:105]
	v_mfma_f32_16x16x32_bf16 v[98:101], v[174:177], v[190:193], v[98:101]
	v_mfma_f32_16x16x32_bf16 v[86:89], v[166:169], v[198:201], v[86:89]
	v_mfma_f32_16x16x32_bf16 v[82:85], v[174:177], v[198:201], v[82:85]
	v_mfma_f32_16x16x32_bf16 v[70:73], v[166:169], v[224:227], v[70:73]
	v_mfma_f32_16x16x32_bf16 v[66:69], v[174:177], v[224:227], v[66:69]
	s_setprio 0
	s_barrier
; #define PG8_STAGE(bufoff, gbase, voff) do { _Pragma("unroll") for (int _i = 0; _i < 2; ++_i) \
;         __builtin_amdgcn_global_load_lds((const unsigned*)((const char*)(gbase) + (voff)[_i]), (PG8_LAS unsigned*)(lds + (bufoff) + ldsw + _i * 8192), 16, 0, 0); } while (0)
; #define PG8_LDA(dst, b, h) do { _Pragma("unroll") for (int m = 0; m < 4; ++m) _Pragma("unroll") for (int k = 0; k < 2; ++k) dst[m][k] = *(const PG8_LAS bf16x8*)(lds + PG8_SA(b, h) + aoff + m * 2048 + k * 1024); } while (0)
; #define PG8_MMA(ai, bj, At, Bt) do { __builtin_amdgcn_s_setprio(1); _Pragma("unroll") for (int m = 0; m < 4; ++m) _Pragma("unroll") for (int n = 0; n < 2; ++n) _Pragma("unroll") for (int k = 0; k < 2; ++k) \
;         acc[ai][bj][m][n] = __builtin_amdgcn_mfma_f32_16x16x32_bf16(Bt[n][k], At[m][k], acc[ai][bj][m][n], 0, 0, 0); __builtin_amdgcn_s_setprio(0); } while (0)
; #define PG8_WAIT_V(n) asm volatile("s_waitcnt vmcnt(" #n ")" ::: "memory")
; #define PG8_WAIT_L(n) asm volatile("s_waitcnt lgkmcnt(" #n ")" ::: "memory")
; #define PG8_BAR __builtin_amdgcn_s_barrier()
; #define PG8_SCHED __builtin_amdgcn_sched_barrier(0)
; template <class Epi, class Sched, bool ALIGN_EPI = false, bool SP2 = false>
; __device__ __forceinline__ void gemm_phase(PG8_LAS unsigned char* lds, const Gemm g, const Sched& S, const Epi& E, const int wave0) {
;     ...
;             PG8_LDA(At, 1, 1); PG8_STAGE(PG8_SB(1, 0), b3, voffB); PG8_STAGE(PG8_SB(1, 1), b3 + hstepB, voffB); PG8_STAGE(PG8_SA(1, 0), a3, voffA);
;             PG8_WAIT_V(8); PG8_WAIT_L(0); PG8_BAR; PG8_MMA(1, 0, At, B0); PG8_MMA(1, 1, At, B1); PG8_BAR; PG8_SCHED;
	s_add_i32 s60, s90, s5
	v_lshl_add_u64 v[206:207], v[206:207], 0, s[64:65]
	s_mov_b32 m0, s60
	ds_read_b128 v[178:181], v144 offset:49152
	ds_read_b128 v[182:185], v144 offset:50176
	ds_read_b128 v[186:189], v144 offset:51200
	ds_read_b128 v[190:193], v144 offset:52224
	ds_read_b128 v[194:197], v144 offset:53248
	ds_read_b128 v[198:201], v144 offset:54272
	ds_read_b128 v[202:205], v144 offset:55296
	ds_read_b128 v[224:227], v144 offset:56320
	global_load_lds_dwordx4 v[206:207], off
	v_lshl_add_u64 v[206:207], v[228:229], 0, s[64:65]
	s_add_i32 m0, s60, 0x2000
	s_add_i32 s60, s91, s5
	global_load_lds_dwordx4 v[206:207], off
	v_lshl_add_u64 v[206:207], v[230:231], 0, s[64:65]
	s_mov_b32 m0, s60
	s_nop 0
	global_load_lds_dwordx4 v[206:207], off
	v_lshl_add_u64 v[206:207], v[232:233], 0, s[64:65]
	s_add_i32 m0, s60, 0x2000
	s_nop 0
	global_load_lds_dwordx4 v[206:207], off
	v_lshl_add_u64 v[206:207], v[234:235], 0, s[64:65]
	s_mov_b32 m0, s73
	s_nop 0
	global_load_lds_dwordx4 v[206:207], off
	v_lshl_add_u64 v[206:207], v[238:239], 0, s[64:65]
	s_mov_b32 m0, s74
	s_nop 0
	global_load_lds_dwordx4 v[206:207], off
	s_waitcnt vmcnt(8)
	s_waitcnt lgkmcnt(0)
	s_barrier
	s_setprio 1
	s_waitcnt lgkmcnt(0)
	v_mfma_f32_16x16x32_bf16 v[62:65], v[146:149], v[178:181], v[62:65]
	v_mfma_f32_16x16x32_bf16 v[58:61], v[154:157], v[178:181], v[58:61]
	v_mfma_f32_16x16x32_bf16 v[46:49], v[146:149], v[186:189], v[46:49]
	v_mfma_f32_16x16x32_bf16 v[42:45], v[154:157], v[186:189], v[42:45]
	v_mfma_f32_16x16x32_bf16 v[30:33], v[146:149], v[194:197], v[30:33]
	v_mfma_f32_16x16x32_bf16 v[26:29], v[154:157], v[194:197], v[26:29]
	v_mfma_f32_16x16x32_bf16 v[14:17], v[146:149], v[202:205], v[14:17]
	v_mfma_f32_16x16x32_bf16 v[10:13], v[154:157], v[202:205], v[10:13]
	v_mfma_f32_16x16x32_bf16 v[62:65], v[150:153], v[182:185], v[62:65]
	v_mfma_f32_16x16x32_bf16 v[58:61], v[158:161], v[182:185], v[58:61]
	v_mfma_f32_16x16x32_bf16 v[46:49], v[150:153], v[190:193], v[46:49]
	v_mfma_f32_16x16x32_bf16 v[42:45], v[158:161], v[190:193], v[42:45]
	v_mfma_f32_16x16x32_bf16 v[30:33], v[150:153], v[198:201], v[30:33]
	v_mfma_f32_16x16x32_bf16 v[26:29], v[158:161], v[198:201], v[26:29]
	v_mfma_f32_16x16x32_bf16 v[14:17], v[150:153], v[224:227], v[14:17]
	v_mfma_f32_16x16x32_bf16 v[10:13], v[158:161], v[224:227], v[10:13]
	v_mfma_f32_16x16x32_bf16 v[54:57], v[162:165], v[178:181], v[54:57]
	v_mfma_f32_16x16x32_bf16 v[50:53], v[170:173], v[178:181], v[50:53]
	v_mfma_f32_16x16x32_bf16 v[38:41], v[162:165], v[186:189], v[38:41]
	v_mfma_f32_16x16x32_bf16 v[34:37], v[170:173], v[186:189], v[34:37]
	v_mfma_f32_16x16x32_bf16 v[22:25], v[162:165], v[194:197], v[22:25]
	v_mfma_f32_16x16x32_bf16 v[18:21], v[170:173], v[194:197], v[18:21]
	v_mfma_f32_16x16x32_bf16 v[6:9], v[162:165], v[202:205], v[6:9]
	v_mfma_f32_16x16x32_bf16 v[2:5], v[170:173], v[202:205], v[2:5]
	v_mfma_f32_16x16x32_bf16 v[54:57], v[166:169], v[182:185], v[54:57]
	v_mfma_f32_16x16x32_bf16 v[50:53], v[174:177], v[182:185], v[50:53]
	v_mfma_f32_16x16x32_bf16 v[38:41], v[166:169], v[190:193], v[38:41]
	v_mfma_f32_16x16x32_bf16 v[34:37], v[174:177], v[190:193], v[34:37]
	v_mfma_f32_16x16x32_bf16 v[22:25], v[166:169], v[198:201], v[22:25]
	v_mfma_f32_16x16x32_bf16 v[18:21], v[174:177], v[198:201], v[18:21]
	v_mfma_f32_16x16x32_bf16 v[6:9], v[166:169], v[224:227], v[6:9]
	v_mfma_f32_16x16x32_bf16 v[2:5], v[174:177], v[224:227], v[2:5]
	s_setprio 0
	s_barrier
	s_add_u32 s87, s87, 0x100
	s_addc_u32 s88, s88, 0
	s_add_u32 s58, s58, 0x100
	s_addc_u32 s59, s59, 0
	s_cmp_ge_i32 s89, s72
	s_mov_b32 s60, s89
	s_cbranch_scc0 .LBB0_1174
	v_readlane_b32 s90, v255, 5

; #define PG8_STAGE(bufoff, gbase, voff) do { _Pragma("unroll") for (int _i = 0; _i < 2; ++_i) \
;         __builtin_amdgcn_global_load_lds((const unsigned*)((const char*)(gbase) + (voff)[_i]), (PG8_LAS unsigned*)(lds + (bufoff) + ldsw + _i * 8192), 16, 0, 0); } while (0)
; #define PG8_LDA(dst, b, h) do { _Pragma("unroll") for (int m = 0; m < 4; ++m) _Pragma("unroll") for (int k = 0; k < 2; ++k) dst[m][k] = *(const PG8_LAS bf16x8*)(lds + PG8_SA(b, h) + aoff + m * 2048 + k * 1024); } while (0)
; #define PG8_LDB(dst, b, h) do { _Pragma("unroll") for (int n = 0; n < 2; ++n) _Pragma("unroll") for (int k = 0; k < 2; ++k) dst[n][k] = *(const PG8_LAS bf16x8*)(lds + PG8_SB(b, h) + boff + n * 2048 + k * 1024); } while (0)
; #define PG8_MMA(ai, bj, At, Bt) do { __builtin_amdgcn_s_setprio(1); _Pragma("unroll") for (int m = 0; m < 4; ++m) _Pragma("unroll") for (int n = 0; n < 2; ++n) _Pragma("unroll") for (int k = 0; k < 2; ++k) \
;         acc[ai][bj][m][n] = __builtin_amdgcn_mfma_f32_16x16x32_bf16(Bt[n][k], At[m][k], acc[ai][bj][m][n], 0, 0, 0); __builtin_amdgcn_s_setprio(0); } while (0)
; #define PG8_WAIT_V(n) asm volatile("s_waitcnt vmcnt(" #n ")" ::: "memory")
; #define PG8_BAR __builtin_amdgcn_s_barrier()
; template <class Epi, class Sched, bool ALIGN_EPI = false, bool SP2 = false>
; __device__ __forceinline__ void gemm_phase(PG8_LAS unsigned char* lds, const Gemm g, const Sched& S, const Epi& E, const int wave0) {
;     ...
;         for (int t = 0; t < nt; t += 2) {
;             const bool last = (t == nt - 2);
;             const char* a1 = cA + (size_t)(t + 1) * kstep;
;             const char* a2 = last ? nA : cA + (size_t)(t + 2) * kstep; const char* b2 = last ? nB : cB + (size_t)(t + 2) * kstep;
;             const char* a3 = a2 + kstep; const char* b3 = b2 + kstep;
;             if (last && has_next) S.a_ready(nxt);
;             if constexpr (SP2) {
;             PG8_LDB(B0, 0, 0); PG8_LDB(B1, 0, 1); PG8_SCHED; PG8_LDA(At, 0, 0); PG8_STAGE(PG8_SA(1, 1), a1 + hstepA, voffA);
;             PG8_WAIT_V(8); PG8_WAIT_L(0); PG8_BAR; PG8_MMA(0, 0, At, B0); PG8_MMA(0, 1, At, B1); PG8_BAR; PG8_SCHED;
;             PG8_LDA(At, 0, 1); PG8_STAGE(PG8_SB(0, 0), b2, voffB); PG8_STAGE(PG8_SB(0, 1), b2 + hstepB, voffB); PG8_STAGE(PG8_SA(0, 0), a2, voffA);
;             PG8_WAIT_V(8); PG8_WAIT_L(0); PG8_BAR; PG8_MMA(1, 0, At, B0); PG8_MMA(1, 1, At, B1); PG8_BAR; PG8_SCHED;
.LBB0_1421:
	s_add_i32 s93, s72, 2
	s_add_u32 s94, s70, 0x80
	s_addc_u32 s73, s71, 0
	s_add_i32 s96, 0, 0x10000
	s_cmp_eq_u32 s83, s72
	s_cselect_b32 s73, s43, s73
	s_cselect_b32 s72, s42, s94
	s_cselect_b32 s95, s61, s92
	s_cselect_b32 s94, s60, s91
	s_add_i32 s97, 0, 0x14000
	v_add_u32_e32 v142, s96, v226
	v_add_u32_e32 v158, s97, v226
	ds_read_b128 v[130:133], v142
	ds_read_b128 v[134:137], v142 offset:1024
	ds_read_b128 v[138:141], v142 offset:2048
	ds_read_b128 v[142:145], v142 offset:3072
	ds_read_b128 v[146:149], v158
	ds_read_b128 v[150:153], v158 offset:1024
	ds_read_b128 v[154:157], v158 offset:2048
	ds_read_b128 v[158:161], v158 offset:3072
	v_lshl_add_u64 v[206:207], s[70:71], 0, v[196:197]
	s_add_i32 m0, s30, 0xc000
	ds_read_b128 v[162:165], v228
	ds_read_b128 v[166:169], v228 offset:1024
	ds_read_b128 v[170:173], v228 offset:2048
	ds_read_b128 v[174:177], v228 offset:3072
	ds_read_b128 v[178:181], v228 offset:4096
	ds_read_b128 v[182:185], v228 offset:5120
	ds_read_b128 v[198:201], v228 offset:6144
	ds_read_b128 v[202:205], v228 offset:7168
	global_load_lds_dwordx4 v[206:207], off
	v_lshl_add_u64 v[206:207], s[70:71], 0, v[194:195]
	s_add_i32 m0, s30, 0xe000
	s_nop 0
	global_load_lds_dwordx4 v[206:207], off
	s_waitcnt vmcnt(8)
	s_waitcnt lgkmcnt(0)
	s_barrier
	s_setprio 1
	s_waitcnt lgkmcnt(0)
	v_mfma_f32_16x16x32_bf16 v[122:125], v[130:133], v[162:165], v[122:125]
	v_mfma_f32_16x16x32_bf16 v[126:129], v[138:141], v[162:165], v[126:129]
	v_mfma_f32_16x16x32_bf16 v[110:113], v[130:133], v[170:173], v[110:113]
	v_mfma_f32_16x16x32_bf16 v[106:109], v[138:141], v[170:173], v[106:109]
	v_mfma_f32_16x16x32_bf16 v[94:97], v[130:133], v[178:181], v[94:97]
	v_mfma_f32_16x16x32_bf16 v[90:93], v[138:141], v[178:181], v[90:93]
	v_mfma_f32_16x16x32_bf16 v[78:81], v[130:133], v[198:201], v[78:81]
	v_mfma_f32_16x16x32_bf16 v[74:77], v[138:141], v[198:201], v[74:77]
	v_mfma_f32_16x16x32_bf16 v[122:125], v[134:137], v[166:169], v[122:125]
	v_mfma_f32_16x16x32_bf16 v[126:129], v[142:145], v[166:169], v[126:129]
	v_mfma_f32_16x16x32_bf16 v[110:113], v[134:137], v[174:177], v[110:113]
	v_mfma_f32_16x16x32_bf16 v[106:109], v[142:145], v[174:177], v[106:109]
	v_mfma_f32_16x16x32_bf16 v[94:97], v[134:137], v[182:185], v[94:97]
	v_mfma_f32_16x16x32_bf16 v[90:93], v[142:145], v[182:185], v[90:93]
	v_mfma_f32_16x16x32_bf16 v[78:81], v[134:137], v[202:205], v[78:81]
	v_mfma_f32_16x16x32_bf16 v[74:77], v[142:145], v[202:205], v[74:77]
	v_mfma_f32_16x16x32_bf16 v[118:121], v[146:149], v[162:165], v[118:121]
	v_mfma_f32_16x16x32_bf16 v[114:117], v[154:157], v[162:165], v[114:117]
	v_mfma_f32_16x16x32_bf16 v[102:105], v[146:149], v[170:173], v[102:105]
	v_mfma_f32_16x16x32_bf16 v[98:101], v[154:157], v[170:173], v[98:101]
	v_mfma_f32_16x16x32_bf16 v[86:89], v[146:149], v[178:181], v[86:89]
	v_mfma_f32_16x16x32_bf16 v[82:85], v[154:157], v[178:181], v[82:85]
	v_mfma_f32_16x16x32_bf16 v[70:73], v[146:149], v[198:201], v[70:73]
	v_mfma_f32_16x16x32_bf16 v[66:69], v[154:157], v[198:201], v[66:69]
	v_mfma_f32_16x16x32_bf16 v[118:121], v[150:153], v[166:169], v[118:121]
	v_mfma_f32_16x16x32_bf16 v[114:117], v[158:161], v[166:169], v[114:117]
	v_mfma_f32_16x16x32_bf16 v[102:105], v[150:153], v[174:177], v[102:105]
	v_mfma_f32_16x16x32_bf16 v[98:101], v[158:161], v[174:177], v[98:101]
	v_mfma_f32_16x16x32_bf16 v[86:89], v[150:153], v[182:185], v[86:89]
	v_mfma_f32_16x16x32_bf16 v[82:85], v[158:161], v[182:185], v[82:85]
	v_mfma_f32_16x16x32_bf16 v[70:73], v[150:153], v[202:205], v[70:73]
	v_mfma_f32_16x16x32_bf16 v[66:69], v[158:161], v[202:205], v[66:69]
	s_setprio 0
	s_barrier
	s_add_i32 s96, s96, s5
	v_lshl_add_u64 v[206:207], s[94:95], 0, v[190:191]
	s_mov_b32 m0, s96
	ds_read_b128 v[162:165], v228 offset:16384
	ds_read_b128 v[166:169], v228 offset:17408
	ds_read_b128 v[170:173], v228 offset:18432
	ds_read_b128 v[174:177], v228 offset:19456
	ds_read_b128 v[178:181], v228 offset:20480
	ds_read_b128 v[182:185], v228 offset:21504
	ds_read_b128 v[198:201], v228 offset:22528
	ds_read_b128 v[202:205], v228 offset:23552
	global_load_lds_dwordx4 v[206:207], off
	s_add_i32 m0, s96, 0x2000
	v_lshl_add_u64 v[224:225], s[94:95], 0, v[186:187]
	s_add_u32 s94, s94, s20
	s_addc_u32 s95, s95, s21
	s_add_i32 s96, s97, s5
	global_load_lds_dwordx4 v[224:225], off
	v_lshl_add_u64 v[230:231], s[94:95], 0, v[190:191]
	s_mov_b32 m0, s96
	v_lshl_add_u64 v[232:233], s[94:95], 0, v[186:187]
	global_load_lds_dwordx4 v[230:231], off
	s_add_i32 m0, s96, 0x2000
	v_lshl_add_u64 v[234:235], s[72:73], 0, v[192:193]
	global_load_lds_dwordx4 v[232:233], off
	s_mov_b32 m0, s30
	v_lshl_add_u64 v[238:239], s[72:73], 0, v[188:189]
	global_load_lds_dwordx4 v[234:235], off
	s_mov_b32 m0, s48
	s_nop 0
	global_load_lds_dwordx4 v[238:239], off
	s_waitcnt vmcnt(8)
	s_waitcnt lgkmcnt(0)
	s_barrier
; #define PG8_STAGE(bufoff, gbase, voff) do { _Pragma("unroll") for (int _i = 0; _i < 2; ++_i) \
;         __builtin_amdgcn_global_load_lds((const unsigned*)((const char*)(gbase) + (voff)[_i]), (PG8_LAS unsigned*)(lds + (bufoff) + ldsw + _i * 8192), 16, 0, 0); } while (0)
; #define PG8_LDA(dst, b, h) do { _Pragma("unroll") for (int m = 0; m < 4; ++m) _Pragma("unroll") for (int k = 0; k < 2; ++k) dst[m][k] = *(const PG8_LAS bf16x8*)(lds + PG8_SA(b, h) + aoff + m * 2048 + k * 1024); } while (0)
; #define PG8_LDB(dst, b, h) do { _Pragma("unroll") for (int n = 0; n < 2; ++n) _Pragma("unroll") for (int k = 0; k < 2; ++k) dst[n][k] = *(const PG8_LAS bf16x8*)(lds + PG8_SB(b, h) + boff + n * 2048 + k * 1024); } while (0)
; #define PG8_MMA(ai, bj, At, Bt) do { __builtin_amdgcn_s_setprio(1); _Pragma("unroll") for (int m = 0; m < 4; ++m) _Pragma("unroll") for (int n = 0; n < 2; ++n) _Pragma("unroll") for (int k = 0; k < 2; ++k) \
;         acc[ai][bj][m][n] = __builtin_amdgcn_mfma_f32_16x16x32_bf16(Bt[n][k], At[m][k], acc[ai][bj][m][n], 0, 0, 0); __builtin_amdgcn_s_setprio(0); } while (0)
; #define PG8_WAIT_V(n) asm volatile("s_waitcnt vmcnt(" #n ")" ::: "memory")
; #define PG8_WAIT_L(n) asm volatile("s_waitcnt lgkmcnt(" #n ")" ::: "memory")
; #define PG8_BAR __builtin_amdgcn_s_barrier()
; #define PG8_SCHED __builtin_amdgcn_sched_barrier(0)
; template <class Epi, class Sched, bool ALIGN_EPI = false, bool SP2 = false>
; __device__ __forceinline__ void gemm_phase(PG8_LAS unsigned char* lds, const Gemm g, const Sched& S, const Epi& E, const int wave0) {
;     ...
;             PG8_WAIT_V(8); PG8_WAIT_L(0); PG8_BAR; PG8_MMA(1, 0, At, B0); PG8_MMA(1, 1, At, B1); PG8_BAR; PG8_SCHED;
;             PG8_LDB(B0, 1, 0); PG8_LDB(B1, 1, 1); PG8_SCHED; PG8_LDA(At, 1, 0); PG8_STAGE(PG8_SA(0, 1), a2 + hstepA, voffA);
;             PG8_WAIT_V(8); PG8_WAIT_L(0); PG8_BAR; PG8_MMA(0, 0, At, B0); PG8_MMA(0, 1, At, B1); PG8_BAR; PG8_SCHED;
	s_setprio 1
	s_waitcnt lgkmcnt(0)
	v_mfma_f32_16x16x32_bf16 v[62:65], v[130:133], v[162:165], v[62:65]
	v_mfma_f32_16x16x32_bf16 v[58:61], v[138:141], v[162:165], v[58:61]
	v_mfma_f32_16x16x32_bf16 v[46:49], v[130:133], v[170:173], v[46:49]
	v_mfma_f32_16x16x32_bf16 v[42:45], v[138:141], v[170:173], v[42:45]
	v_mfma_f32_16x16x32_bf16 v[30:33], v[130:133], v[178:181], v[30:33]
	v_mfma_f32_16x16x32_bf16 v[26:29], v[138:141], v[178:181], v[26:29]
	v_mfma_f32_16x16x32_bf16 v[14:17], v[130:133], v[198:201], v[14:17]
	v_mfma_f32_16x16x32_bf16 v[10:13], v[138:141], v[198:201], v[10:13]
	v_mfma_f32_16x16x32_bf16 v[62:65], v[134:137], v[166:169], v[62:65]
	v_mfma_f32_16x16x32_bf16 v[58:61], v[142:145], v[166:169], v[58:61]
	v_mfma_f32_16x16x32_bf16 v[46:49], v[134:137], v[174:177], v[46:49]
	v_mfma_f32_16x16x32_bf16 v[42:45], v[142:145], v[174:177], v[42:45]
	v_mfma_f32_16x16x32_bf16 v[30:33], v[134:137], v[182:185], v[30:33]
	v_mfma_f32_16x16x32_bf16 v[26:29], v[142:145], v[182:185], v[26:29]
	v_mfma_f32_16x16x32_bf16 v[14:17], v[134:137], v[202:205], v[14:17]
	v_mfma_f32_16x16x32_bf16 v[10:13], v[142:145], v[202:205], v[10:13]
	v_mfma_f32_16x16x32_bf16 v[54:57], v[146:149], v[162:165], v[54:57]
	v_mfma_f32_16x16x32_bf16 v[50:53], v[154:157], v[162:165], v[50:53]
	v_mfma_f32_16x16x32_bf16 v[38:41], v[146:149], v[170:173], v[38:41]
	v_mfma_f32_16x16x32_bf16 v[34:37], v[154:157], v[170:173], v[34:37]
	v_mfma_f32_16x16x32_bf16 v[22:25], v[146:149], v[178:181], v[22:25]
	v_mfma_f32_16x16x32_bf16 v[18:21], v[154:157], v[178:181], v[18:21]
	v_mfma_f32_16x16x32_bf16 v[6:9], v[146:149], v[198:201], v[6:9]
	v_mfma_f32_16x16x32_bf16 v[2:5], v[154:157], v[198:201], v[2:5]
	v_mfma_f32_16x16x32_bf16 v[54:57], v[150:153], v[166:169], v[54:57]
	v_mfma_f32_16x16x32_bf16 v[50:53], v[158:161], v[166:169], v[50:53]
	v_mfma_f32_16x16x32_bf16 v[38:41], v[150:153], v[174:177], v[38:41]
	v_mfma_f32_16x16x32_bf16 v[34:37], v[158:161], v[174:177], v[34:37]
	v_mfma_f32_16x16x32_bf16 v[22:25], v[150:153], v[182:185], v[22:25]
	v_mfma_f32_16x16x32_bf16 v[18:21], v[158:161], v[182:185], v[18:21]
	v_mfma_f32_16x16x32_bf16 v[6:9], v[150:153], v[202:205], v[6:9]
	v_mfma_f32_16x16x32_bf16 v[2:5], v[158:161], v[202:205], v[2:5]
	s_setprio 0
	s_barrier
	s_add_i32 s94, 0, 0x18000
	s_add_i32 s95, 0, 0x1c000
	v_add_u32_e32 v142, s94, v226
	v_add_u32_e32 v158, s95, v226
	ds_read_b128 v[130:133], v142
	ds_read_b128 v[134:137], v142 offset:1024
	ds_read_b128 v[138:141], v142 offset:2048
	ds_read_b128 v[142:145], v142 offset:3072
	ds_read_b128 v[146:149], v158
	ds_read_b128 v[150:153], v158 offset:1024
	ds_read_b128 v[154:157], v158 offset:2048
	ds_read_b128 v[158:161], v158 offset:3072
	s_add_u32 s72, s72, s18
	s_addc_u32 s73, s73, s19
	s_mov_b32 m0, s74
	v_lshl_add_u64 v[240:241], s[72:73], 0, v[192:193]
	ds_read_b128 v[162:165], v228 offset:32768
	ds_read_b128 v[166:169], v228 offset:33792
	ds_read_b128 v[170:173], v228 offset:34816
	ds_read_b128 v[174:177], v228 offset:35840
	ds_read_b128 v[178:181], v228 offset:36864
	ds_read_b128 v[182:185], v228 offset:37888
	ds_read_b128 v[198:201], v228 offset:38912
	ds_read_b128 v[202:205], v228 offset:39936
	global_load_lds_dwordx4 v[240:241], off
	v_lshl_add_u64 v[240:241], s[72:73], 0, v[188:189]
	s_mov_b32 m0, s75
	s_nop 0
	global_load_lds_dwordx4 v[240:241], off
	s_waitcnt vmcnt(8)
	s_waitcnt lgkmcnt(0)
	s_barrier
	s_setprio 1
	s_waitcnt lgkmcnt(0)
	v_mfma_f32_16x16x32_bf16 v[122:125], v[130:133], v[162:165], v[122:125]
	v_mfma_f32_16x16x32_bf16 v[126:129], v[138:141], v[162:165], v[126:129]
	v_mfma_f32_16x16x32_bf16 v[110:113], v[130:133], v[170:173], v[110:113]
	v_mfma_f32_16x16x32_bf16 v[106:109], v[138:141], v[170:173], v[106:109]
	v_mfma_f32_16x16x32_bf16 v[94:97], v[130:133], v[178:181], v[94:97]
	v_mfma_f32_16x16x32_bf16 v[90:93], v[138:141], v[178:181], v[90:93]
	v_mfma_f32_16x16x32_bf16 v[78:81], v[130:133], v[198:201], v[78:81]
	v_mfma_f32_16x16x32_bf16 v[74:77], v[138:141], v[198:201], v[74:77]
	v_mfma_f32_16x16x32_bf16 v[122:125], v[134:137], v[166:169], v[122:125]
	v_mfma_f32_16x16x32_bf16 v[126:129], v[142:145], v[166:169], v[126:129]
	v_mfma_f32_16x16x32_bf16 v[110:113], v[134:137], v[174:177], v[110:113]
	v_mfma_f32_16x16x32_bf16 v[106:109], v[142:145], v[174:177], v[106:109]
	v_mfma_f32_16x16x32_bf16 v[94:97], v[134:137], v[182:185], v[94:97]
	v_mfma_f32_16x16x32_bf16 v[90:93], v[142:145], v[182:185], v[90:93]
	v_mfma_f32_16x16x32_bf16 v[78:81], v[134:137], v[202:205], v[78:81]
	v_mfma_f32_16x16x32_bf16 v[74:77], v[142:145], v[202:205], v[74:77]
	v_mfma_f32_16x16x32_bf16 v[118:121], v[146:149], v[162:165], v[118:121]
	v_mfma_f32_16x16x32_bf16 v[114:117], v[154:157], v[162:165], v[114:117]
	v_mfma_f32_16x16x32_bf16 v[102:105], v[146:149], v[170:173], v[102:105]
	v_mfma_f32_16x16x32_bf16 v[98:101], v[154:157], v[170:173], v[98:101]
	v_mfma_f32_16x16x32_bf16 v[86:89], v[146:149], v[178:181], v[86:89]
	v_mfma_f32_16x16x32_bf16 v[82:85], v[154:157], v[178:181], v[82:85]
	v_mfma_f32_16x16x32_bf16 v[70:73], v[146:149], v[198:201], v[70:73]
	v_mfma_f32_16x16x32_bf16 v[66:69], v[154:157], v[198:201], v[66:69]
	v_mfma_f32_16x16x32_bf16 v[118:121], v[150:153], v[166:169], v[118:121]
	v_mfma_f32_16x16x32_bf16 v[114:117], v[158:161], v[166:169], v[114:117]
	v_mfma_f32_16x16x32_bf16 v[102:105], v[150:153], v[174:177], v[102:105]
	v_mfma_f32_16x16x32_bf16 v[98:101], v[158:161], v[174:177], v[98:101]
	v_mfma_f32_16x16x32_bf16 v[86:89], v[150:153], v[182:185], v[86:89]
	v_mfma_f32_16x16x32_bf16 v[82:85], v[158:161], v[182:185], v[82:85]
	v_mfma_f32_16x16x32_bf16 v[70:73], v[150:153], v[202:205], v[70:73]
	v_mfma_f32_16x16x32_bf16 v[66:69], v[158:161], v[202:205], v[66:69]
	s_setprio 0
	s_barrier
; #define PG8_STAGE(bufoff, gbase, voff) do { _Pragma("unroll") for (int _i = 0; _i < 2; ++_i) \
;         __builtin_amdgcn_global_load_lds((const unsigned*)((const char*)(gbase) + (voff)[_i]), (PG8_LAS unsigned*)(lds + (bufoff) + ldsw + _i * 8192), 16, 0, 0); } while (0)
; #define PG8_LDA(dst, b, h) do { _Pragma("unroll") for (int m = 0; m < 4; ++m) _Pragma("unroll") for (int k = 0; k < 2; ++k) dst[m][k] = *(const PG8_LAS bf16x8*)(lds + PG8_SA(b, h) + aoff + m * 2048 + k * 1024); } while (0)
; #define PG8_MMA(ai, bj, At, Bt) do { __builtin_amdgcn_s_setprio(1); _Pragma("unroll") for (int m = 0; m < 4; ++m) _Pragma("unroll") for (int n = 0; n < 2; ++n) _Pragma("unroll") for (int k = 0; k < 2; ++k) \
;         acc[ai][bj][m][n] = __builtin_amdgcn_mfma_f32_16x16x32_bf16(Bt[n][k], At[m][k], acc[ai][bj][m][n], 0, 0, 0); __builtin_amdgcn_s_setprio(0); } while (0)
; #define PG8_WAIT_V(n) asm volatile("s_waitcnt vmcnt(" #n ")" ::: "memory")
; #define PG8_WAIT_L(n) asm volatile("s_waitcnt lgkmcnt(" #n ")" ::: "memory")
; #define PG8_BAR __builtin_amdgcn_s_barrier()
; #define PG8_SCHED __builtin_amdgcn_sched_barrier(0)
; template <class Epi, class Sched, bool ALIGN_EPI = false, bool SP2 = false>
; __device__ __forceinline__ void gemm_phase(PG8_LAS unsigned char* lds, const Gemm g, const Sched& S, const Epi& E, const int wave0) {
;     ...
;             PG8_LDA(At, 1, 1); PG8_STAGE(PG8_SB(1, 0), b3, voffB); PG8_STAGE(PG8_SB(1, 1), b3 + hstepB, voffB); PG8_STAGE(PG8_SA(1, 0), a3, voffA);
;             PG8_WAIT_V(8); PG8_WAIT_L(0); PG8_BAR; PG8_MMA(1, 0, At, B0); PG8_MMA(1, 1, At, B1); PG8_BAR; PG8_SCHED;
	s_add_i32 s72, s94, s5
	v_lshl_add_u64 v[206:207], v[206:207], 0, s[64:65]
	s_mov_b32 m0, s72
	ds_read_b128 v[162:165], v228 offset:49152
	ds_read_b128 v[166:169], v228 offset:50176
	ds_read_b128 v[170:173], v228 offset:51200
	ds_read_b128 v[174:177], v228 offset:52224
	ds_read_b128 v[178:181], v228 offset:53248
	ds_read_b128 v[182:185], v228 offset:54272
	ds_read_b128 v[198:201], v228 offset:55296
	ds_read_b128 v[202:205], v228 offset:56320
	global_load_lds_dwordx4 v[206:207], off
	v_lshl_add_u64 v[206:207], v[224:225], 0, s[64:65]
	s_add_i32 m0, s72, 0x2000
	s_add_i32 s72, s95, s5
	global_load_lds_dwordx4 v[206:207], off
	v_lshl_add_u64 v[206:207], v[230:231], 0, s[64:65]
	s_mov_b32 m0, s72
	s_nop 0
	global_load_lds_dwordx4 v[206:207], off
	v_lshl_add_u64 v[206:207], v[232:233], 0, s[64:65]
	s_add_i32 m0, s72, 0x2000
	s_nop 0
	global_load_lds_dwordx4 v[206:207], off
	v_lshl_add_u64 v[206:207], v[234:235], 0, s[64:65]
	s_mov_b32 m0, s77
	s_nop 0
	global_load_lds_dwordx4 v[206:207], off
	v_lshl_add_u64 v[206:207], v[238:239], 0, s[64:65]
	s_mov_b32 m0, s82
	s_nop 0
	global_load_lds_dwordx4 v[206:207], off
	s_waitcnt vmcnt(8)
	s_waitcnt lgkmcnt(0)
	s_barrier
	s_setprio 1
	s_waitcnt lgkmcnt(0)
	v_mfma_f32_16x16x32_bf16 v[62:65], v[130:133], v[162:165], v[62:65]
	v_mfma_f32_16x16x32_bf16 v[58:61], v[138:141], v[162:165], v[58:61]
	v_mfma_f32_16x16x32_bf16 v[46:49], v[130:133], v[170:173], v[46:49]
	v_mfma_f32_16x16x32_bf16 v[42:45], v[138:141], v[170:173], v[42:45]
	v_mfma_f32_16x16x32_bf16 v[30:33], v[130:133], v[178:181], v[30:33]
	v_mfma_f32_16x16x32_bf16 v[26:29], v[138:141], v[178:181], v[26:29]
	v_mfma_f32_16x16x32_bf16 v[14:17], v[130:133], v[198:201], v[14:17]
	v_mfma_f32_16x16x32_bf16 v[10:13], v[138:141], v[198:201], v[10:13]
	v_mfma_f32_16x16x32_bf16 v[62:65], v[134:137], v[166:169], v[62:65]
	v_mfma_f32_16x16x32_bf16 v[58:61], v[142:145], v[166:169], v[58:61]
	v_mfma_f32_16x16x32_bf16 v[46:49], v[134:137], v[174:177], v[46:49]
	v_mfma_f32_16x16x32_bf16 v[42:45], v[142:145], v[174:177], v[42:45]
	v_mfma_f32_16x16x32_bf16 v[30:33], v[134:137], v[182:185], v[30:33]
	v_mfma_f32_16x16x32_bf16 v[26:29], v[142:145], v[182:185], v[26:29]
	v_mfma_f32_16x16x32_bf16 v[14:17], v[134:137], v[202:205], v[14:17]
	v_mfma_f32_16x16x32_bf16 v[10:13], v[142:145], v[202:205], v[10:13]
	v_mfma_f32_16x16x32_bf16 v[54:57], v[146:149], v[162:165], v[54:57]
	v_mfma_f32_16x16x32_bf16 v[50:53], v[154:157], v[162:165], v[50:53]
	v_mfma_f32_16x16x32_bf16 v[38:41], v[146:149], v[170:173], v[38:41]
	v_mfma_f32_16x16x32_bf16 v[34:37], v[154:157], v[170:173], v[34:37]
	v_mfma_f32_16x16x32_bf16 v[22:25], v[146:149], v[178:181], v[22:25]
	v_mfma_f32_16x16x32_bf16 v[18:21], v[154:157], v[178:181], v[18:21]
	v_mfma_f32_16x16x32_bf16 v[6:9], v[146:149], v[198:201], v[6:9]
	v_mfma_f32_16x16x32_bf16 v[2:5], v[154:157], v[198:201], v[2:5]
	v_mfma_f32_16x16x32_bf16 v[54:57], v[150:153], v[166:169], v[54:57]
	v_mfma_f32_16x16x32_bf16 v[50:53], v[158:161], v[166:169], v[50:53]
	v_mfma_f32_16x16x32_bf16 v[38:41], v[150:153], v[174:177], v[38:41]
	v_mfma_f32_16x16x32_bf16 v[34:37], v[158:161], v[174:177], v[34:37]
	v_mfma_f32_16x16x32_bf16 v[22:25], v[150:153], v[182:185], v[22:25]
	v_mfma_f32_16x16x32_bf16 v[18:21], v[158:161], v[182:185], v[18:21]
	v_mfma_f32_16x16x32_bf16 v[6:9], v[150:153], v[202:205], v[6:9]
	v_mfma_f32_16x16x32_bf16 v[2:5], v[158:161], v[202:205], v[2:5]
	s_setprio 0
	s_barrier
	s_add_u32 s91, s91, 0x100
	s_addc_u32 s92, s92, 0
	s_add_u32 s70, s70, 0x100
	s_addc_u32 s71, s71, 0
	s_cmp_ge_i32 s93, s76
	s_mov_b32 s72, s93
	s_cbranch_scc0 .LBB0_1421
	v_readlane_b32 s96, v255, 16
	v_readlane_b32 s94, v255, 15
	v_readlane_b32 s97, v255, 17
	v_readlane_b32 s95, v255, 18

; #define PG8_STAGE(bufoff, gbase, voff) do { _Pragma("unroll") for (int _i = 0; _i < 2; ++_i) \
;         __builtin_amdgcn_global_load_lds((const unsigned*)((const char*)(gbase) + (voff)[_i]), (PG8_LAS unsigned*)(lds + (bufoff) + ldsw + _i * 8192), 16, 0, 0); } while (0)
; #define PG8_LDA(dst, b, h) do { _Pragma("unroll") for (int m = 0; m < 4; ++m) _Pragma("unroll") for (int k = 0; k < 2; ++k) dst[m][k] = *(const PG8_LAS bf16x8*)(lds + PG8_SA(b, h) + aoff + m * 2048 + k * 1024); } while (0)
; #define PG8_LDB(dst, b, h) do { _Pragma("unroll") for (int n = 0; n < 2; ++n) _Pragma("unroll") for (int k = 0; k < 2; ++k) dst[n][k] = *(const PG8_LAS bf16x8*)(lds + PG8_SB(b, h) + boff + n * 2048 + k * 1024); } while (0)
; #define PG8_MMA(ai, bj, At, Bt) do { __builtin_amdgcn_s_setprio(1); _Pragma("unroll") for (int m = 0; m < 4; ++m) _Pragma("unroll") for (int n = 0; n < 2; ++n) _Pragma("unroll") for (int k = 0; k < 2; ++k) \
;         acc[ai][bj][m][n] = __builtin_amdgcn_mfma_f32_16x16x32_bf16(Bt[n][k], At[m][k], acc[ai][bj][m][n], 0, 0, 0); __builtin_amdgcn_s_setprio(0); } while (0)
; #define PG8_WAIT_V(n) asm volatile("s_waitcnt vmcnt(" #n ")" ::: "memory")
; #define PG8_BAR __builtin_amdgcn_s_barrier()
; template <class Epi, class Sched, bool ALIGN_EPI = false, bool SP2 = false>
; __device__ __forceinline__ void gemm_phase(PG8_LAS unsigned char* lds, const Gemm g, const Sched& S, const Epi& E, const int wave0) {
;     ...
;         for (int t = 0; t < nt; t += 2) {
;             const bool last = (t == nt - 2);
;             const char* a1 = cA + (size_t)(t + 1) * kstep;
;             const char* a2 = last ? nA : cA + (size_t)(t + 2) * kstep; const char* b2 = last ? nB : cB + (size_t)(t + 2) * kstep;
;             const char* a3 = a2 + kstep; const char* b3 = b2 + kstep;
;             if (last && has_next) S.a_ready(nxt);
;             if constexpr (SP2) {
;             PG8_LDB(B0, 0, 0); PG8_LDB(B1, 0, 1); PG8_SCHED; PG8_LDA(At, 0, 0); PG8_STAGE(PG8_SA(1, 1), a1 + hstepA, voffA);
;             PG8_WAIT_V(8); PG8_WAIT_L(0); PG8_BAR; PG8_MMA(0, 0, At, B0); PG8_MMA(0, 1, At, B1); PG8_BAR; PG8_SCHED;
;             PG8_LDA(At, 0, 1); PG8_STAGE(PG8_SB(0, 0), b2, voffB); PG8_STAGE(PG8_SB(0, 1), b2 + hstepB, voffB); PG8_STAGE(PG8_SA(0, 0), a2, voffA);
;             PG8_WAIT_V(8); PG8_WAIT_L(0); PG8_BAR; PG8_MMA(1, 0, At, B0); PG8_MMA(1, 1, At, B1); PG8_BAR; PG8_SCHED;
.LBB0_1501:
	s_add_i32 s87, s58, 2
	s_add_u32 s88, s56, 0x80
	s_addc_u32 s59, s57, 0
	s_add_i32 s90, 0, 0x10000
	s_cmp_eq_u32 s73, s58
	s_cselect_b32 s59, s41, s59
	s_cselect_b32 s58, s40, s88
	v_add_u32_e32 v157, s90, v154
	s_cselect_b32 s89, s55, s84
	s_cselect_b32 s88, s54, s83
	s_add_i32 s91, 0, 0x14000
	ds_read_b128 v[142:145], v157
	ds_read_b128 v[146:149], v157 offset:1024
	ds_read_b128 v[150:153], v157 offset:2048
	ds_read_b128 v[158:161], v157 offset:3072
	v_add_u32_e32 v157, s91, v154
	ds_read_b128 v[162:165], v157
	ds_read_b128 v[166:169], v157 offset:1024
	ds_read_b128 v[170:173], v157 offset:2048
	ds_read_b128 v[174:177], v157 offset:3072
	v_lshl_add_u64 v[206:207], s[56:57], 0, v[140:141]
	s_add_i32 m0, s30, 0xc000
	ds_read_b128 v[178:181], v156
	ds_read_b128 v[182:185], v156 offset:1024
	ds_read_b128 v[186:189], v156 offset:2048
	ds_read_b128 v[190:193], v156 offset:3072
	ds_read_b128 v[194:197], v156 offset:4096
	ds_read_b128 v[198:201], v156 offset:5120
	ds_read_b128 v[202:205], v156 offset:6144
	ds_read_b128 v[224:227], v156 offset:7168
	global_load_lds_dwordx4 v[206:207], off
	v_lshl_add_u64 v[206:207], s[56:57], 0, v[138:139]
	s_add_i32 m0, s30, 0xe000
	s_nop 0
	global_load_lds_dwordx4 v[206:207], off
	s_waitcnt vmcnt(8)
	s_waitcnt lgkmcnt(0)
	s_barrier
	s_setprio 1
	s_waitcnt lgkmcnt(0)
	v_mfma_f32_16x16x32_bf16 v[122:125], v[142:145], v[178:181], v[122:125]
	v_mfma_f32_16x16x32_bf16 v[126:129], v[150:153], v[178:181], v[126:129]
	v_mfma_f32_16x16x32_bf16 v[110:113], v[142:145], v[186:189], v[110:113]
	v_mfma_f32_16x16x32_bf16 v[106:109], v[150:153], v[186:189], v[106:109]
	v_mfma_f32_16x16x32_bf16 v[94:97], v[142:145], v[194:197], v[94:97]
	v_mfma_f32_16x16x32_bf16 v[90:93], v[150:153], v[194:197], v[90:93]
	v_mfma_f32_16x16x32_bf16 v[78:81], v[142:145], v[202:205], v[78:81]
	v_mfma_f32_16x16x32_bf16 v[74:77], v[150:153], v[202:205], v[74:77]
	v_mfma_f32_16x16x32_bf16 v[122:125], v[146:149], v[182:185], v[122:125]
	v_mfma_f32_16x16x32_bf16 v[126:129], v[158:161], v[182:185], v[126:129]
	v_mfma_f32_16x16x32_bf16 v[110:113], v[146:149], v[190:193], v[110:113]
	v_mfma_f32_16x16x32_bf16 v[106:109], v[158:161], v[190:193], v[106:109]
	v_mfma_f32_16x16x32_bf16 v[94:97], v[146:149], v[198:201], v[94:97]
	v_mfma_f32_16x16x32_bf16 v[90:93], v[158:161], v[198:201], v[90:93]
	v_mfma_f32_16x16x32_bf16 v[78:81], v[146:149], v[224:227], v[78:81]
	v_mfma_f32_16x16x32_bf16 v[74:77], v[158:161], v[224:227], v[74:77]
	v_mfma_f32_16x16x32_bf16 v[118:121], v[162:165], v[178:181], v[118:121]
	v_mfma_f32_16x16x32_bf16 v[114:117], v[170:173], v[178:181], v[114:117]
	v_mfma_f32_16x16x32_bf16 v[102:105], v[162:165], v[186:189], v[102:105]
	v_mfma_f32_16x16x32_bf16 v[98:101], v[170:173], v[186:189], v[98:101]
	v_mfma_f32_16x16x32_bf16 v[86:89], v[162:165], v[194:197], v[86:89]
	v_mfma_f32_16x16x32_bf16 v[82:85], v[170:173], v[194:197], v[82:85]
	v_mfma_f32_16x16x32_bf16 v[70:73], v[162:165], v[202:205], v[70:73]
	v_mfma_f32_16x16x32_bf16 v[66:69], v[170:173], v[202:205], v[66:69]
	v_mfma_f32_16x16x32_bf16 v[118:121], v[166:169], v[182:185], v[118:121]
	v_mfma_f32_16x16x32_bf16 v[114:117], v[174:177], v[182:185], v[114:117]
	v_mfma_f32_16x16x32_bf16 v[102:105], v[166:169], v[190:193], v[102:105]
	v_mfma_f32_16x16x32_bf16 v[98:101], v[174:177], v[190:193], v[98:101]
	v_mfma_f32_16x16x32_bf16 v[86:89], v[166:169], v[198:201], v[86:89]
	v_mfma_f32_16x16x32_bf16 v[82:85], v[174:177], v[198:201], v[82:85]
	v_mfma_f32_16x16x32_bf16 v[70:73], v[166:169], v[224:227], v[70:73]
	v_mfma_f32_16x16x32_bf16 v[66:69], v[174:177], v[224:227], v[66:69]
	s_setprio 0
	s_barrier
	s_add_i32 s90, s90, s5
	v_lshl_add_u64 v[206:207], s[88:89], 0, v[134:135]
	s_mov_b32 m0, s90
	ds_read_b128 v[178:181], v156 offset:16384
	ds_read_b128 v[182:185], v156 offset:17408
	ds_read_b128 v[186:189], v156 offset:18432
	ds_read_b128 v[190:193], v156 offset:19456
	ds_read_b128 v[194:197], v156 offset:20480
	ds_read_b128 v[198:201], v156 offset:21504
	ds_read_b128 v[202:205], v156 offset:22528
	ds_read_b128 v[224:227], v156 offset:23552
	global_load_lds_dwordx4 v[206:207], off
	s_add_i32 m0, s90, 0x2000
	v_lshl_add_u64 v[228:229], s[88:89], 0, v[130:131]
	s_add_u32 s88, s88, s20
	s_addc_u32 s89, s89, s21
	s_add_i32 s90, s91, s5
	global_load_lds_dwordx4 v[228:229], off
	v_lshl_add_u64 v[230:231], s[88:89], 0, v[134:135]
	s_mov_b32 m0, s90
	v_lshl_add_u64 v[232:233], s[88:89], 0, v[130:131]
	global_load_lds_dwordx4 v[230:231], off
	s_add_i32 m0, s90, 0x2000
	v_lshl_add_u64 v[234:235], s[58:59], 0, v[136:137]
	global_load_lds_dwordx4 v[232:233], off
	s_mov_b32 m0, s30
	v_lshl_add_u64 v[238:239], s[58:59], 0, v[132:133]
	global_load_lds_dwordx4 v[234:235], off
	s_mov_b32 m0, s48
	s_nop 0
	global_load_lds_dwordx4 v[238:239], off
	s_waitcnt vmcnt(8)
	s_waitcnt lgkmcnt(0)
	s_barrier
; #define PG8_STAGE(bufoff, gbase, voff) do { _Pragma("unroll") for (int _i = 0; _i < 2; ++_i) \
;         __builtin_amdgcn_global_load_lds((const unsigned*)((const char*)(gbase) + (voff)[_i]), (PG8_LAS unsigned*)(lds + (bufoff) + ldsw + _i * 8192), 16, 0, 0); } while (0)
; #define PG8_LDA(dst, b, h) do { _Pragma("unroll") for (int m = 0; m < 4; ++m) _Pragma("unroll") for (int k = 0; k < 2; ++k) dst[m][k] = *(const PG8_LAS bf16x8*)(lds + PG8_SA(b, h) + aoff + m * 2048 + k * 1024); } while (0)
; #define PG8_LDB(dst, b, h) do { _Pragma("unroll") for (int n = 0; n < 2; ++n) _Pragma("unroll") for (int k = 0; k < 2; ++k) dst[n][k] = *(const PG8_LAS bf16x8*)(lds + PG8_SB(b, h) + boff + n * 2048 + k * 1024); } while (0)
; #define PG8_MMA(ai, bj, At, Bt) do { __builtin_amdgcn_s_setprio(1); _Pragma("unroll") for (int m = 0; m < 4; ++m) _Pragma("unroll") for (int n = 0; n < 2; ++n) _Pragma("unroll") for (int k = 0; k < 2; ++k) \
;         acc[ai][bj][m][n] = __builtin_amdgcn_mfma_f32_16x16x32_bf16(Bt[n][k], At[m][k], acc[ai][bj][m][n], 0, 0, 0); __builtin_amdgcn_s_setprio(0); } while (0)
; #define PG8_WAIT_V(n) asm volatile("s_waitcnt vmcnt(" #n ")" ::: "memory")
; #define PG8_WAIT_L(n) asm volatile("s_waitcnt lgkmcnt(" #n ")" ::: "memory")
; #define PG8_BAR __builtin_amdgcn_s_barrier()
; #define PG8_SCHED __builtin_amdgcn_sched_barrier(0)
; template <class Epi, class Sched, bool ALIGN_EPI = false, bool SP2 = false>
; __device__ __forceinline__ void gemm_phase(PG8_LAS unsigned char* lds, const Gemm g, const Sched& S, const Epi& E, const int wave0) {
;     ...
;             PG8_WAIT_V(8); PG8_WAIT_L(0); PG8_BAR; PG8_MMA(1, 0, At, B0); PG8_MMA(1, 1, At, B1); PG8_BAR; PG8_SCHED;
;             PG8_LDB(B0, 1, 0); PG8_LDB(B1, 1, 1); PG8_SCHED; PG8_LDA(At, 1, 0); PG8_STAGE(PG8_SA(0, 1), a2 + hstepA, voffA);
;             PG8_WAIT_V(8); PG8_WAIT_L(0); PG8_BAR; PG8_MMA(0, 0, At, B0); PG8_MMA(0, 1, At, B1); PG8_BAR; PG8_SCHED;
	s_setprio 1
	s_waitcnt lgkmcnt(0)
	v_mfma_f32_16x16x32_bf16 v[62:65], v[142:145], v[178:181], v[62:65]
	v_mfma_f32_16x16x32_bf16 v[58:61], v[150:153], v[178:181], v[58:61]
	v_mfma_f32_16x16x32_bf16 v[46:49], v[142:145], v[186:189], v[46:49]
	v_mfma_f32_16x16x32_bf16 v[42:45], v[150:153], v[186:189], v[42:45]
	v_mfma_f32_16x16x32_bf16 v[30:33], v[142:145], v[194:197], v[30:33]
	v_mfma_f32_16x16x32_bf16 v[26:29], v[150:153], v[194:197], v[26:29]
	v_mfma_f32_16x16x32_bf16 v[14:17], v[142:145], v[202:205], v[14:17]
	v_mfma_f32_16x16x32_bf16 v[10:13], v[150:153], v[202:205], v[10:13]
	v_mfma_f32_16x16x32_bf16 v[62:65], v[146:149], v[182:185], v[62:65]
	v_mfma_f32_16x16x32_bf16 v[58:61], v[158:161], v[182:185], v[58:61]
	v_mfma_f32_16x16x32_bf16 v[46:49], v[146:149], v[190:193], v[46:49]
	v_mfma_f32_16x16x32_bf16 v[42:45], v[158:161], v[190:193], v[42:45]
	v_mfma_f32_16x16x32_bf16 v[30:33], v[146:149], v[198:201], v[30:33]
	v_mfma_f32_16x16x32_bf16 v[26:29], v[158:161], v[198:201], v[26:29]
	v_mfma_f32_16x16x32_bf16 v[14:17], v[146:149], v[224:227], v[14:17]
	v_mfma_f32_16x16x32_bf16 v[10:13], v[158:161], v[224:227], v[10:13]
	v_mfma_f32_16x16x32_bf16 v[54:57], v[162:165], v[178:181], v[54:57]
	v_mfma_f32_16x16x32_bf16 v[50:53], v[170:173], v[178:181], v[50:53]
	v_mfma_f32_16x16x32_bf16 v[38:41], v[162:165], v[186:189], v[38:41]
	v_mfma_f32_16x16x32_bf16 v[34:37], v[170:173], v[186:189], v[34:37]
	v_mfma_f32_16x16x32_bf16 v[22:25], v[162:165], v[194:197], v[22:25]
	v_mfma_f32_16x16x32_bf16 v[18:21], v[170:173], v[194:197], v[18:21]
	v_mfma_f32_16x16x32_bf16 v[6:9], v[162:165], v[202:205], v[6:9]
	v_mfma_f32_16x16x32_bf16 v[2:5], v[170:173], v[202:205], v[2:5]
	v_mfma_f32_16x16x32_bf16 v[54:57], v[166:169], v[182:185], v[54:57]
	v_mfma_f32_16x16x32_bf16 v[50:53], v[174:177], v[182:185], v[50:53]
	v_mfma_f32_16x16x32_bf16 v[38:41], v[166:169], v[190:193], v[38:41]
	v_mfma_f32_16x16x32_bf16 v[34:37], v[174:177], v[190:193], v[34:37]
	v_mfma_f32_16x16x32_bf16 v[22:25], v[166:169], v[198:201], v[22:25]
	v_mfma_f32_16x16x32_bf16 v[18:21], v[174:177], v[198:201], v[18:21]
	v_mfma_f32_16x16x32_bf16 v[6:9], v[166:169], v[224:227], v[6:9]
	v_mfma_f32_16x16x32_bf16 v[2:5], v[174:177], v[224:227], v[2:5]
	s_setprio 0
	s_barrier
	s_add_i32 s88, 0, 0x18000
	v_add_u32_e32 v157, s88, v154
	s_add_i32 s89, 0, 0x1c000
	ds_read_b128 v[142:145], v157
	ds_read_b128 v[146:149], v157 offset:1024
	ds_read_b128 v[150:153], v157 offset:2048
	ds_read_b128 v[158:161], v157 offset:3072
	v_add_u32_e32 v157, s89, v154
	ds_read_b128 v[162:165], v157
	ds_read_b128 v[166:169], v157 offset:1024
	ds_read_b128 v[170:173], v157 offset:2048
	ds_read_b128 v[174:177], v157 offset:3072
	s_add_u32 s58, s58, s18
	s_addc_u32 s59, s59, s19
	s_mov_b32 m0, s60
	v_lshl_add_u64 v[240:241], s[58:59], 0, v[136:137]
	ds_read_b128 v[178:181], v156 offset:32768
	ds_read_b128 v[182:185], v156 offset:33792
	ds_read_b128 v[186:189], v156 offset:34816
	ds_read_b128 v[190:193], v156 offset:35840
	ds_read_b128 v[194:197], v156 offset:36864
	ds_read_b128 v[198:201], v156 offset:37888
	ds_read_b128 v[202:205], v156 offset:38912
	ds_read_b128 v[224:227], v156 offset:39936
	global_load_lds_dwordx4 v[240:241], off
	v_lshl_add_u64 v[240:241], s[58:59], 0, v[132:133]
	s_mov_b32 m0, s61
	s_nop 0
	global_load_lds_dwordx4 v[240:241], off
	s_waitcnt vmcnt(8)
	s_waitcnt lgkmcnt(0)
	s_barrier
	s_setprio 1
	s_waitcnt lgkmcnt(0)
	v_mfma_f32_16x16x32_bf16 v[122:125], v[142:145], v[178:181], v[122:125]
	v_mfma_f32_16x16x32_bf16 v[126:129], v[150:153], v[178:181], v[126:129]
	v_mfma_f32_16x16x32_bf16 v[110:113], v[142:145], v[186:189], v[110:113]
	v_mfma_f32_16x16x32_bf16 v[106:109], v[150:153], v[186:189], v[106:109]
	v_mfma_f32_16x16x32_bf16 v[94:97], v[142:145], v[194:197], v[94:97]
	v_mfma_f32_16x16x32_bf16 v[90:93], v[150:153], v[194:197], v[90:93]
	v_mfma_f32_16x16x32_bf16 v[78:81], v[142:145], v[202:205], v[78:81]
	v_mfma_f32_16x16x32_bf16 v[74:77], v[150:153], v[202:205], v[74:77]
	v_mfma_f32_16x16x32_bf16 v[122:125], v[146:149], v[182:185], v[122:125]
	v_mfma_f32_16x16x32_bf16 v[126:129], v[158:161], v[182:185], v[126:129]
	v_mfma_f32_16x16x32_bf16 v[110:113], v[146:149], v[190:193], v[110:113]
	v_mfma_f32_16x16x32_bf16 v[106:109], v[158:161], v[190:193], v[106:109]
	v_mfma_f32_16x16x32_bf16 v[94:97], v[146:149], v[198:201], v[94:97]
	v_mfma_f32_16x16x32_bf16 v[90:93], v[158:161], v[198:201], v[90:93]
	v_mfma_f32_16x16x32_bf16 v[78:81], v[146:149], v[224:227], v[78:81]
	v_mfma_f32_16x16x32_bf16 v[74:77], v[158:161], v[224:227], v[74:77]
	v_mfma_f32_16x16x32_bf16 v[118:121], v[162:165], v[178:181], v[118:121]
	v_mfma_f32_16x16x32_bf16 v[114:117], v[170:173], v[178:181], v[114:117]
	v_mfma_f32_16x16x32_bf16 v[102:105], v[162:165], v[186:189], v[102:105]
	v_mfma_f32_16x16x32_bf16 v[98:101], v[170:173], v[186:189], v[98:101]
	v_mfma_f32_16x16x32_bf16 v[86:89], v[162:165], v[194:197], v[86:89]
	v_mfma_f32_16x16x32_bf16 v[82:85], v[170:173], v[194:197], v[82:85]
	v_mfma_f32_16x16x32_bf16 v[70:73], v[162:165], v[202:205], v[70:73]
	v_mfma_f32_16x16x32_bf16 v[66:69], v[170:173], v[202:205], v[66:69]
	v_mfma_f32_16x16x32_bf16 v[118:121], v[166:169], v[182:185], v[118:121]
	v_mfma_f32_16x16x32_bf16 v[114:117], v[174:177], v[182:185], v[114:117]
	v_mfma_f32_16x16x32_bf16 v[102:105], v[166:169], v[190:193], v[102:105]
	v_mfma_f32_16x16x32_bf16 v[98:101], v[174:177], v[190:193], v[98:101]
	v_mfma_f32_16x16x32_bf16 v[86:89], v[166:169], v[198:201], v[86:89]
	v_mfma_f32_16x16x32_bf16 v[82:85], v[174:177], v[198:201], v[82:85]
	v_mfma_f32_16x16x32_bf16 v[70:73], v[166:169], v[224:227], v[70:73]
	v_mfma_f32_16x16x32_bf16 v[66:69], v[174:177], v[224:227], v[66:69]
	s_setprio 0
	s_barrier
; #define PG8_STAGE(bufoff, gbase, voff) do { _Pragma("unroll") for (int _i = 0; _i < 2; ++_i) \
;         __builtin_amdgcn_global_load_lds((const unsigned*)((const char*)(gbase) + (voff)[_i]), (PG8_LAS unsigned*)(lds + (bufoff) + ldsw + _i * 8192), 16, 0, 0); } while (0)
; #define PG8_LDA(dst, b, h) do { _Pragma("unroll") for (int m = 0; m < 4; ++m) _Pragma("unroll") for (int k = 0; k < 2; ++k) dst[m][k] = *(const PG8_LAS bf16x8*)(lds + PG8_SA(b, h) + aoff + m * 2048 + k * 1024); } while (0)
; #define PG8_MMA(ai, bj, At, Bt) do { __builtin_amdgcn_s_setprio(1); _Pragma("unroll") for (int m = 0; m < 4; ++m) _Pragma("unroll") for (int n = 0; n < 2; ++n) _Pragma("unroll") for (int k = 0; k < 2; ++k) \
;         acc[ai][bj][m][n] = __builtin_amdgcn_mfma_f32_16x16x32_bf16(Bt[n][k], At[m][k], acc[ai][bj][m][n], 0, 0, 0); __builtin_amdgcn_s_setprio(0); } while (0)
; #define PG8_WAIT_V(n) asm volatile("s_waitcnt vmcnt(" #n ")" ::: "memory")
; #define PG8_WAIT_L(n) asm volatile("s_waitcnt lgkmcnt(" #n ")" ::: "memory")
; #define PG8_BAR __builtin_amdgcn_s_barrier()
; #define PG8_SCHED __builtin_amdgcn_sched_barrier(0)
; template <class Epi, class Sched, bool ALIGN_EPI = false, bool SP2 = false>
; __device__ __forceinline__ void gemm_phase(PG8_LAS unsigned char* lds, const Gemm g, const Sched& S, const Epi& E, const int wave0) {
;     ...
;             PG8_LDA(At, 1, 1); PG8_STAGE(PG8_SB(1, 0), b3, voffB); PG8_STAGE(PG8_SB(1, 1), b3 + hstepB, voffB); PG8_STAGE(PG8_SA(1, 0), a3, voffA);
;             PG8_WAIT_V(8); PG8_WAIT_L(0); PG8_BAR; PG8_MMA(1, 0, At, B0); PG8_MMA(1, 1, At, B1); PG8_BAR; PG8_SCHED;
	s_add_i32 s58, s88, s5
	v_lshl_add_u64 v[206:207], v[206:207], 0, s[64:65]
	s_mov_b32 m0, s58
	ds_read_b128 v[178:181], v156 offset:49152
	ds_read_b128 v[182:185], v156 offset:50176
	ds_read_b128 v[186:189], v156 offset:51200
	ds_read_b128 v[190:193], v156 offset:52224
	ds_read_b128 v[194:197], v156 offset:53248
	ds_read_b128 v[198:201], v156 offset:54272
	ds_read_b128 v[202:205], v156 offset:55296
	ds_read_b128 v[224:227], v156 offset:56320
	global_load_lds_dwordx4 v[206:207], off
	v_lshl_add_u64 v[206:207], v[228:229], 0, s[64:65]
	s_add_i32 m0, s58, 0x2000
	s_add_i32 s58, s89, s5
	global_load_lds_dwordx4 v[206:207], off
	v_lshl_add_u64 v[206:207], v[230:231], 0, s[64:65]
	s_mov_b32 m0, s58
	s_nop 0
	global_load_lds_dwordx4 v[206:207], off
	v_lshl_add_u64 v[206:207], v[232:233], 0, s[64:65]
	s_add_i32 m0, s58, 0x2000
	s_nop 0
	global_load_lds_dwordx4 v[206:207], off
	v_lshl_add_u64 v[206:207], v[234:235], 0, s[64:65]
	s_mov_b32 m0, s71
	s_nop 0
	global_load_lds_dwordx4 v[206:207], off
	v_lshl_add_u64 v[206:207], v[238:239], 0, s[64:65]
	s_mov_b32 m0, s72
	s_nop 0
	global_load_lds_dwordx4 v[206:207], off
	s_waitcnt vmcnt(8)
	s_waitcnt lgkmcnt(0)
	s_barrier
	s_setprio 1
	s_waitcnt lgkmcnt(0)
	v_mfma_f32_16x16x32_bf16 v[62:65], v[142:145], v[178:181], v[62:65]
	v_mfma_f32_16x16x32_bf16 v[58:61], v[150:153], v[178:181], v[58:61]
	v_mfma_f32_16x16x32_bf16 v[46:49], v[142:145], v[186:189], v[46:49]
	v_mfma_f32_16x16x32_bf16 v[42:45], v[150:153], v[186:189], v[42:45]
	v_mfma_f32_16x16x32_bf16 v[30:33], v[142:145], v[194:197], v[30:33]
	v_mfma_f32_16x16x32_bf16 v[26:29], v[150:153], v[194:197], v[26:29]
	v_mfma_f32_16x16x32_bf16 v[14:17], v[142:145], v[202:205], v[14:17]
	v_mfma_f32_16x16x32_bf16 v[10:13], v[150:153], v[202:205], v[10:13]
	v_mfma_f32_16x16x32_bf16 v[62:65], v[146:149], v[182:185], v[62:65]
	v_mfma_f32_16x16x32_bf16 v[58:61], v[158:161], v[182:185], v[58:61]
	v_mfma_f32_16x16x32_bf16 v[46:49], v[146:149], v[190:193], v[46:49]
	v_mfma_f32_16x16x32_bf16 v[42:45], v[158:161], v[190:193], v[42:45]
	v_mfma_f32_16x16x32_bf16 v[30:33], v[146:149], v[198:201], v[30:33]
	v_mfma_f32_16x16x32_bf16 v[26:29], v[158:161], v[198:201], v[26:29]
	v_mfma_f32_16x16x32_bf16 v[14:17], v[146:149], v[224:227], v[14:17]
	v_mfma_f32_16x16x32_bf16 v[10:13], v[158:161], v[224:227], v[10:13]
	v_mfma_f32_16x16x32_bf16 v[54:57], v[162:165], v[178:181], v[54:57]
	v_mfma_f32_16x16x32_bf16 v[50:53], v[170:173], v[178:181], v[50:53]
	v_mfma_f32_16x16x32_bf16 v[38:41], v[162:165], v[186:189], v[38:41]
	v_mfma_f32_16x16x32_bf16 v[34:37], v[170:173], v[186:189], v[34:37]
	v_mfma_f32_16x16x32_bf16 v[22:25], v[162:165], v[194:197], v[22:25]
	v_mfma_f32_16x16x32_bf16 v[18:21], v[170:173], v[194:197], v[18:21]
	v_mfma_f32_16x16x32_bf16 v[6:9], v[162:165], v[202:205], v[6:9]
	v_mfma_f32_16x16x32_bf16 v[2:5], v[170:173], v[202:205], v[2:5]
	v_mfma_f32_16x16x32_bf16 v[54:57], v[166:169], v[182:185], v[54:57]
	v_mfma_f32_16x16x32_bf16 v[50:53], v[174:177], v[182:185], v[50:53]
	v_mfma_f32_16x16x32_bf16 v[38:41], v[166:169], v[190:193], v[38:41]
	v_mfma_f32_16x16x32_bf16 v[34:37], v[174:177], v[190:193], v[34:37]
	v_mfma_f32_16x16x32_bf16 v[22:25], v[166:169], v[198:201], v[22:25]
	v_mfma_f32_16x16x32_bf16 v[18:21], v[174:177], v[198:201], v[18:21]
	v_mfma_f32_16x16x32_bf16 v[6:9], v[166:169], v[224:227], v[6:9]
	v_mfma_f32_16x16x32_bf16 v[2:5], v[174:177], v[224:227], v[2:5]
	s_setprio 0
	s_barrier
	s_add_u32 s83, s83, 0x100
	s_addc_u32 s84, s84, 0
	s_add_u32 s56, s56, 0x100
	s_addc_u32 s57, s57, 0
	s_cmp_ge_i32 s87, s70
	s_mov_b32 s58, s87
	s_cbranch_scc0 .LBB0_1501
	v_readlane_b32 s90, v255, 24
	v_readlane_b32 s91, v255, 25

; #define PG8_STAGE(bufoff, gbase, voff) do { _Pragma("unroll") for (int _i = 0; _i < 2; ++_i) \
;         __builtin_amdgcn_global_load_lds((const unsigned*)((const char*)(gbase) + (voff)[_i]), (PG8_LAS unsigned*)(lds + (bufoff) + ldsw + _i * 8192), 16, 0, 0); } while (0)
; #define PG8_LDA(dst, b, h) do { _Pragma("unroll") for (int m = 0; m < 4; ++m) _Pragma("unroll") for (int k = 0; k < 2; ++k) dst[m][k] = *(const PG8_LAS bf16x8*)(lds + PG8_SA(b, h) + aoff + m * 2048 + k * 1024); } while (0)
; #define PG8_LDB(dst, b, h) do { _Pragma("unroll") for (int n = 0; n < 2; ++n) _Pragma("unroll") for (int k = 0; k < 2; ++k) dst[n][k] = *(const PG8_LAS bf16x8*)(lds + PG8_SB(b, h) + boff + n * 2048 + k * 1024); } while (0)
; #define PG8_MMA(ai, bj, At, Bt) do { __builtin_amdgcn_s_setprio(1); _Pragma("unroll") for (int m = 0; m < 4; ++m) _Pragma("unroll") for (int n = 0; n < 2; ++n) _Pragma("unroll") for (int k = 0; k < 2; ++k) \
;         acc[ai][bj][m][n] = __builtin_amdgcn_mfma_f32_16x16x32_bf16(Bt[n][k], At[m][k], acc[ai][bj][m][n], 0, 0, 0); __builtin_amdgcn_s_setprio(0); } while (0)
; #define PG8_WAIT_V(n) asm volatile("s_waitcnt vmcnt(" #n ")" ::: "memory")
; #define PG8_BAR __builtin_amdgcn_s_barrier()
; template <class Epi, class Sched, bool ALIGN_EPI = false, bool SP2 = false>
; __device__ __forceinline__ void gemm_phase(PG8_LAS unsigned char* lds, const Gemm g, const Sched& S, const Epi& E, const int wave0) {
;     ...
;         for (int t = 0; t < nt; t += 2) {
;             const bool last = (t == nt - 2);
;             const char* a1 = cA + (size_t)(t + 1) * kstep;
;             const char* a2 = last ? nA : cA + (size_t)(t + 2) * kstep; const char* b2 = last ? nB : cB + (size_t)(t + 2) * kstep;
;             const char* a3 = a2 + kstep; const char* b3 = b2 + kstep;
;             if (last && has_next) S.a_ready(nxt);
;             if constexpr (SP2) {
;             PG8_LDB(B0, 0, 0); PG8_LDB(B1, 0, 1); PG8_SCHED; PG8_LDA(At, 0, 0); PG8_STAGE(PG8_SA(1, 1), a1 + hstepA, voffA);
;             PG8_WAIT_V(8); PG8_WAIT_L(0); PG8_BAR; PG8_MMA(0, 0, At, B0); PG8_MMA(0, 1, At, B1); PG8_BAR; PG8_SCHED;
;             PG8_LDA(At, 0, 1); PG8_STAGE(PG8_SB(0, 0), b2, voffB); PG8_STAGE(PG8_SB(0, 1), b2 + hstepB, voffB); PG8_STAGE(PG8_SA(0, 0), a2, voffA);
;             PG8_WAIT_V(8); PG8_WAIT_L(0); PG8_BAR; PG8_MMA(1, 0, At, B0); PG8_MMA(1, 1, At, B1); PG8_BAR; PG8_SCHED;
.LBB0_1634:
	s_add_i32 s89, s60, 2
	s_add_u32 s90, s58, 0x80
	s_addc_u32 s61, s59, 0
	s_add_i32 s92, 0, 0x10000
	s_cmp_eq_u32 s76, s60
	s_cselect_b32 s61, s41, s61
	s_cselect_b32 s60, s40, s90
	s_cselect_b32 s91, s57, s88
	s_cselect_b32 s90, s56, s84
	s_add_i32 s93, 0, 0x14000
	v_add_u32_e32 v154, s92, v172
	v_add_u32_e32 v170, s93, v172
	ds_read_b128 v[130:133], v154
	ds_read_b128 v[134:137], v154 offset:1024
	ds_read_b128 v[150:153], v154 offset:2048
	ds_read_b128 v[154:157], v154 offset:3072
	ds_read_b128 v[158:161], v170
	ds_read_b128 v[162:165], v170 offset:1024
	ds_read_b128 v[166:169], v170 offset:2048
	ds_read_b128 v[176:179], v170 offset:3072
	v_lshl_add_u64 v[170:171], s[58:59], 0, v[148:149]
	s_add_i32 m0, s30, 0xc000
	ds_read_b128 v[180:183], v175
	ds_read_b128 v[184:187], v175 offset:1024
	ds_read_b128 v[188:191], v175 offset:2048
	ds_read_b128 v[192:195], v175 offset:3072
	ds_read_b128 v[196:199], v175 offset:4096
	ds_read_b128 v[200:203], v175 offset:5120
	ds_read_b128 v[204:207], v175 offset:6144
	ds_read_b128 v[224:227], v175 offset:7168
	global_load_lds_dwordx4 v[170:171], off
	v_lshl_add_u64 v[170:171], s[58:59], 0, v[146:147]
	s_add_i32 m0, s30, 0xe000
	s_nop 0
	global_load_lds_dwordx4 v[170:171], off
	s_waitcnt vmcnt(8)
	s_waitcnt lgkmcnt(0)
	s_barrier
	s_setprio 1
	s_waitcnt lgkmcnt(0)
	v_mfma_f32_16x16x32_bf16 v[126:129], v[130:133], v[180:183], v[126:129]
	v_mfma_f32_16x16x32_bf16 v[122:125], v[150:153], v[180:183], v[122:125]
	v_mfma_f32_16x16x32_bf16 v[110:113], v[130:133], v[188:191], v[110:113]
	v_mfma_f32_16x16x32_bf16 v[106:109], v[150:153], v[188:191], v[106:109]
	v_mfma_f32_16x16x32_bf16 v[94:97], v[130:133], v[196:199], v[94:97]
	v_mfma_f32_16x16x32_bf16 v[90:93], v[150:153], v[196:199], v[90:93]
	v_mfma_f32_16x16x32_bf16 v[78:81], v[130:133], v[204:207], v[78:81]
	v_mfma_f32_16x16x32_bf16 v[74:77], v[150:153], v[204:207], v[74:77]
	v_mfma_f32_16x16x32_bf16 v[126:129], v[134:137], v[184:187], v[126:129]
	v_mfma_f32_16x16x32_bf16 v[122:125], v[154:157], v[184:187], v[122:125]
	v_mfma_f32_16x16x32_bf16 v[110:113], v[134:137], v[192:195], v[110:113]
	v_mfma_f32_16x16x32_bf16 v[106:109], v[154:157], v[192:195], v[106:109]
	v_mfma_f32_16x16x32_bf16 v[94:97], v[134:137], v[200:203], v[94:97]
	v_mfma_f32_16x16x32_bf16 v[90:93], v[154:157], v[200:203], v[90:93]
	v_mfma_f32_16x16x32_bf16 v[78:81], v[134:137], v[224:227], v[78:81]
	v_mfma_f32_16x16x32_bf16 v[74:77], v[154:157], v[224:227], v[74:77]
	v_mfma_f32_16x16x32_bf16 v[118:121], v[158:161], v[180:183], v[118:121]
	v_mfma_f32_16x16x32_bf16 v[114:117], v[166:169], v[180:183], v[114:117]
	v_mfma_f32_16x16x32_bf16 v[102:105], v[158:161], v[188:191], v[102:105]
	v_mfma_f32_16x16x32_bf16 v[98:101], v[166:169], v[188:191], v[98:101]
	v_mfma_f32_16x16x32_bf16 v[86:89], v[158:161], v[196:199], v[86:89]
	v_mfma_f32_16x16x32_bf16 v[82:85], v[166:169], v[196:199], v[82:85]
	v_mfma_f32_16x16x32_bf16 v[70:73], v[158:161], v[204:207], v[70:73]
	v_mfma_f32_16x16x32_bf16 v[66:69], v[166:169], v[204:207], v[66:69]
	v_mfma_f32_16x16x32_bf16 v[118:121], v[162:165], v[184:187], v[118:121]
	v_mfma_f32_16x16x32_bf16 v[114:117], v[176:179], v[184:187], v[114:117]
	v_mfma_f32_16x16x32_bf16 v[102:105], v[162:165], v[192:195], v[102:105]
	v_mfma_f32_16x16x32_bf16 v[98:101], v[176:179], v[192:195], v[98:101]
	v_mfma_f32_16x16x32_bf16 v[86:89], v[162:165], v[200:203], v[86:89]
	v_mfma_f32_16x16x32_bf16 v[82:85], v[176:179], v[200:203], v[82:85]
	v_mfma_f32_16x16x32_bf16 v[70:73], v[162:165], v[224:227], v[70:73]
	v_mfma_f32_16x16x32_bf16 v[66:69], v[176:179], v[224:227], v[66:69]
	s_setprio 0
	s_barrier
	s_add_i32 s92, s92, s5
	v_lshl_add_u64 v[170:171], s[90:91], 0, v[142:143]
	s_mov_b32 m0, s92
	ds_read_b128 v[180:183], v175 offset:16384
	ds_read_b128 v[184:187], v175 offset:17408
	ds_read_b128 v[188:191], v175 offset:18432
	ds_read_b128 v[192:195], v175 offset:19456
	ds_read_b128 v[196:199], v175 offset:20480
	ds_read_b128 v[200:203], v175 offset:21504
	ds_read_b128 v[204:207], v175 offset:22528
	ds_read_b128 v[224:227], v175 offset:23552
	global_load_lds_dwordx4 v[170:171], off
	s_add_i32 m0, s92, 0x2000
	v_lshl_add_u64 v[228:229], s[90:91], 0, v[138:139]
	s_add_u32 s90, s90, s20
	s_addc_u32 s91, s91, s21
	s_add_i32 s92, s93, s5
	global_load_lds_dwordx4 v[228:229], off
	v_lshl_add_u64 v[230:231], s[90:91], 0, v[142:143]
	s_mov_b32 m0, s92
	v_lshl_add_u64 v[232:233], s[90:91], 0, v[138:139]
	global_load_lds_dwordx4 v[230:231], off
	s_add_i32 m0, s92, 0x2000
	v_lshl_add_u64 v[234:235], s[60:61], 0, v[144:145]
	global_load_lds_dwordx4 v[232:233], off
	s_mov_b32 m0, s30
	v_lshl_add_u64 v[236:237], s[60:61], 0, v[140:141]
	global_load_lds_dwordx4 v[234:235], off
	s_mov_b32 m0, s70
	s_nop 0
	global_load_lds_dwordx4 v[236:237], off
	s_waitcnt vmcnt(8)
	s_waitcnt lgkmcnt(0)
	s_barrier
; #define PG8_STAGE(bufoff, gbase, voff) do { _Pragma("unroll") for (int _i = 0; _i < 2; ++_i) \
;         __builtin_amdgcn_global_load_lds((const unsigned*)((const char*)(gbase) + (voff)[_i]), (PG8_LAS unsigned*)(lds + (bufoff) + ldsw + _i * 8192), 16, 0, 0); } while (0)
; #define PG8_LDA(dst, b, h) do { _Pragma("unroll") for (int m = 0; m < 4; ++m) _Pragma("unroll") for (int k = 0; k < 2; ++k) dst[m][k] = *(const PG8_LAS bf16x8*)(lds + PG8_SA(b, h) + aoff + m * 2048 + k * 1024); } while (0)
; #define PG8_LDB(dst, b, h) do { _Pragma("unroll") for (int n = 0; n < 2; ++n) _Pragma("unroll") for (int k = 0; k < 2; ++k) dst[n][k] = *(const PG8_LAS bf16x8*)(lds + PG8_SB(b, h) + boff + n * 2048 + k * 1024); } while (0)
; #define PG8_MMA(ai, bj, At, Bt) do { __builtin_amdgcn_s_setprio(1); _Pragma("unroll") for (int m = 0; m < 4; ++m) _Pragma("unroll") for (int n = 0; n < 2; ++n) _Pragma("unroll") for (int k = 0; k < 2; ++k) \
;         acc[ai][bj][m][n] = __builtin_amdgcn_mfma_f32_16x16x32_bf16(Bt[n][k], At[m][k], acc[ai][bj][m][n], 0, 0, 0); __builtin_amdgcn_s_setprio(0); } while (0)
; #define PG8_WAIT_V(n) asm volatile("s_waitcnt vmcnt(" #n ")" ::: "memory")
; #define PG8_WAIT_L(n) asm volatile("s_waitcnt lgkmcnt(" #n ")" ::: "memory")
; #define PG8_BAR __builtin_amdgcn_s_barrier()
; #define PG8_SCHED __builtin_amdgcn_sched_barrier(0)
; template <class Epi, class Sched, bool ALIGN_EPI = false, bool SP2 = false>
; __device__ __forceinline__ void gemm_phase(PG8_LAS unsigned char* lds, const Gemm g, const Sched& S, const Epi& E, const int wave0) {
;     ...
;             PG8_WAIT_V(8); PG8_WAIT_L(0); PG8_BAR; PG8_MMA(1, 0, At, B0); PG8_MMA(1, 1, At, B1); PG8_BAR; PG8_SCHED;
;             PG8_LDB(B0, 1, 0); PG8_LDB(B1, 1, 1); PG8_SCHED; PG8_LDA(At, 1, 0); PG8_STAGE(PG8_SA(0, 1), a2 + hstepA, voffA);
;             PG8_WAIT_V(8); PG8_WAIT_L(0); PG8_BAR; PG8_MMA(0, 0, At, B0); PG8_MMA(0, 1, At, B1); PG8_BAR; PG8_SCHED;
	s_setprio 1
	s_waitcnt lgkmcnt(0)
	v_mfma_f32_16x16x32_bf16 v[62:65], v[130:133], v[180:183], v[62:65]
	v_mfma_f32_16x16x32_bf16 v[58:61], v[150:153], v[180:183], v[58:61]
	v_mfma_f32_16x16x32_bf16 v[46:49], v[130:133], v[188:191], v[46:49]
	v_mfma_f32_16x16x32_bf16 v[42:45], v[150:153], v[188:191], v[42:45]
	v_mfma_f32_16x16x32_bf16 v[30:33], v[130:133], v[196:199], v[30:33]
	v_mfma_f32_16x16x32_bf16 v[26:29], v[150:153], v[196:199], v[26:29]
	v_mfma_f32_16x16x32_bf16 v[14:17], v[130:133], v[204:207], v[14:17]
	v_mfma_f32_16x16x32_bf16 v[10:13], v[150:153], v[204:207], v[10:13]
	v_mfma_f32_16x16x32_bf16 v[62:65], v[134:137], v[184:187], v[62:65]
	v_mfma_f32_16x16x32_bf16 v[58:61], v[154:157], v[184:187], v[58:61]
	v_mfma_f32_16x16x32_bf16 v[46:49], v[134:137], v[192:195], v[46:49]
	v_mfma_f32_16x16x32_bf16 v[42:45], v[154:157], v[192:195], v[42:45]
	v_mfma_f32_16x16x32_bf16 v[30:33], v[134:137], v[200:203], v[30:33]
	v_mfma_f32_16x16x32_bf16 v[26:29], v[154:157], v[200:203], v[26:29]
	v_mfma_f32_16x16x32_bf16 v[14:17], v[134:137], v[224:227], v[14:17]
	v_mfma_f32_16x16x32_bf16 v[10:13], v[154:157], v[224:227], v[10:13]
	v_mfma_f32_16x16x32_bf16 v[54:57], v[158:161], v[180:183], v[54:57]
	v_mfma_f32_16x16x32_bf16 v[50:53], v[166:169], v[180:183], v[50:53]
	v_mfma_f32_16x16x32_bf16 v[38:41], v[158:161], v[188:191], v[38:41]
	v_mfma_f32_16x16x32_bf16 v[34:37], v[166:169], v[188:191], v[34:37]
	v_mfma_f32_16x16x32_bf16 v[22:25], v[158:161], v[196:199], v[22:25]
	v_mfma_f32_16x16x32_bf16 v[18:21], v[166:169], v[196:199], v[18:21]
	v_mfma_f32_16x16x32_bf16 v[6:9], v[158:161], v[204:207], v[6:9]
	v_mfma_f32_16x16x32_bf16 v[2:5], v[166:169], v[204:207], v[2:5]
	v_mfma_f32_16x16x32_bf16 v[54:57], v[162:165], v[184:187], v[54:57]
	v_mfma_f32_16x16x32_bf16 v[50:53], v[176:179], v[184:187], v[50:53]
	v_mfma_f32_16x16x32_bf16 v[38:41], v[162:165], v[192:195], v[38:41]
	v_mfma_f32_16x16x32_bf16 v[34:37], v[176:179], v[192:195], v[34:37]
	v_mfma_f32_16x16x32_bf16 v[22:25], v[162:165], v[200:203], v[22:25]
	v_mfma_f32_16x16x32_bf16 v[18:21], v[176:179], v[200:203], v[18:21]
	v_mfma_f32_16x16x32_bf16 v[6:9], v[162:165], v[224:227], v[6:9]
	v_mfma_f32_16x16x32_bf16 v[2:5], v[176:179], v[224:227], v[2:5]
	s_setprio 0
	s_barrier
	s_add_i32 s90, 0, 0x18000
	s_add_i32 s91, 0, 0x1c000
	v_add_u32_e32 v154, s90, v172
	v_add_u32_e32 v176, s91, v172
	ds_read_b128 v[130:133], v154
	ds_read_b128 v[134:137], v154 offset:1024
	ds_read_b128 v[150:153], v154 offset:2048
	ds_read_b128 v[154:157], v154 offset:3072
	ds_read_b128 v[158:161], v176
	ds_read_b128 v[162:165], v176 offset:1024
	ds_read_b128 v[166:169], v176 offset:2048
	ds_read_b128 v[176:179], v176 offset:3072
	s_add_u32 s60, s60, s6
	s_addc_u32 s61, s61, s7
	s_mov_b32 m0, s71
	v_lshl_add_u64 v[238:239], s[60:61], 0, v[144:145]
	ds_read_b128 v[180:183], v175 offset:32768
	ds_read_b128 v[184:187], v175 offset:33792
	ds_read_b128 v[188:191], v175 offset:34816
	ds_read_b128 v[192:195], v175 offset:35840
	ds_read_b128 v[196:199], v175 offset:36864
	ds_read_b128 v[200:203], v175 offset:37888
	ds_read_b128 v[204:207], v175 offset:38912
	ds_read_b128 v[224:227], v175 offset:39936
	global_load_lds_dwordx4 v[238:239], off
	v_lshl_add_u64 v[238:239], s[60:61], 0, v[140:141]
	s_mov_b32 m0, s72
	s_nop 0
	global_load_lds_dwordx4 v[238:239], off
	s_waitcnt vmcnt(8)
	s_waitcnt lgkmcnt(0)
	s_barrier
	s_setprio 1
	s_waitcnt lgkmcnt(0)
	v_mfma_f32_16x16x32_bf16 v[126:129], v[130:133], v[180:183], v[126:129]
	v_mfma_f32_16x16x32_bf16 v[122:125], v[150:153], v[180:183], v[122:125]
	v_mfma_f32_16x16x32_bf16 v[110:113], v[130:133], v[188:191], v[110:113]
	v_mfma_f32_16x16x32_bf16 v[106:109], v[150:153], v[188:191], v[106:109]
	v_mfma_f32_16x16x32_bf16 v[94:97], v[130:133], v[196:199], v[94:97]
	v_mfma_f32_16x16x32_bf16 v[90:93], v[150:153], v[196:199], v[90:93]
	v_mfma_f32_16x16x32_bf16 v[78:81], v[130:133], v[204:207], v[78:81]
	v_mfma_f32_16x16x32_bf16 v[74:77], v[150:153], v[204:207], v[74:77]
	v_mfma_f32_16x16x32_bf16 v[126:129], v[134:137], v[184:187], v[126:129]
	v_mfma_f32_16x16x32_bf16 v[122:125], v[154:157], v[184:187], v[122:125]
	v_mfma_f32_16x16x32_bf16 v[110:113], v[134:137], v[192:195], v[110:113]
	v_mfma_f32_16x16x32_bf16 v[106:109], v[154:157], v[192:195], v[106:109]
	v_mfma_f32_16x16x32_bf16 v[94:97], v[134:137], v[200:203], v[94:97]
	v_mfma_f32_16x16x32_bf16 v[90:93], v[154:157], v[200:203], v[90:93]
	v_mfma_f32_16x16x32_bf16 v[78:81], v[134:137], v[224:227], v[78:81]
	v_mfma_f32_16x16x32_bf16 v[74:77], v[154:157], v[224:227], v[74:77]
	v_mfma_f32_16x16x32_bf16 v[118:121], v[158:161], v[180:183], v[118:121]
	v_mfma_f32_16x16x32_bf16 v[114:117], v[166:169], v[180:183], v[114:117]
	v_mfma_f32_16x16x32_bf16 v[102:105], v[158:161], v[188:191], v[102:105]
	v_mfma_f32_16x16x32_bf16 v[98:101], v[166:169], v[188:191], v[98:101]
	v_mfma_f32_16x16x32_bf16 v[86:89], v[158:161], v[196:199], v[86:89]
	v_mfma_f32_16x16x32_bf16 v[82:85], v[166:169], v[196:199], v[82:85]
	v_mfma_f32_16x16x32_bf16 v[70:73], v[158:161], v[204:207], v[70:73]
	v_mfma_f32_16x16x32_bf16 v[66:69], v[166:169], v[204:207], v[66:69]
	v_mfma_f32_16x16x32_bf16 v[118:121], v[162:165], v[184:187], v[118:121]
	v_mfma_f32_16x16x32_bf16 v[114:117], v[176:179], v[184:187], v[114:117]
	v_mfma_f32_16x16x32_bf16 v[102:105], v[162:165], v[192:195], v[102:105]
	v_mfma_f32_16x16x32_bf16 v[98:101], v[176:179], v[192:195], v[98:101]
	v_mfma_f32_16x16x32_bf16 v[86:89], v[162:165], v[200:203], v[86:89]
	v_mfma_f32_16x16x32_bf16 v[82:85], v[176:179], v[200:203], v[82:85]
	v_mfma_f32_16x16x32_bf16 v[70:73], v[162:165], v[224:227], v[70:73]
	v_mfma_f32_16x16x32_bf16 v[66:69], v[176:179], v[224:227], v[66:69]
	s_setprio 0
	s_barrier
; #define PG8_STAGE(bufoff, gbase, voff) do { _Pragma("unroll") for (int _i = 0; _i < 2; ++_i) \
;         __builtin_amdgcn_global_load_lds((const unsigned*)((const char*)(gbase) + (voff)[_i]), (PG8_LAS unsigned*)(lds + (bufoff) + ldsw + _i * 8192), 16, 0, 0); } while (0)
; #define PG8_LDA(dst, b, h) do { _Pragma("unroll") for (int m = 0; m < 4; ++m) _Pragma("unroll") for (int k = 0; k < 2; ++k) dst[m][k] = *(const PG8_LAS bf16x8*)(lds + PG8_SA(b, h) + aoff + m * 2048 + k * 1024); } while (0)
; #define PG8_MMA(ai, bj, At, Bt) do { __builtin_amdgcn_s_setprio(1); _Pragma("unroll") for (int m = 0; m < 4; ++m) _Pragma("unroll") for (int n = 0; n < 2; ++n) _Pragma("unroll") for (int k = 0; k < 2; ++k) \
;         acc[ai][bj][m][n] = __builtin_amdgcn_mfma_f32_16x16x32_bf16(Bt[n][k], At[m][k], acc[ai][bj][m][n], 0, 0, 0); __builtin_amdgcn_s_setprio(0); } while (0)
; #define PG8_WAIT_V(n) asm volatile("s_waitcnt vmcnt(" #n ")" ::: "memory")
; #define PG8_WAIT_L(n) asm volatile("s_waitcnt lgkmcnt(" #n ")" ::: "memory")
; #define PG8_BAR __builtin_amdgcn_s_barrier()
; #define PG8_SCHED __builtin_amdgcn_sched_barrier(0)
; template <class Epi, class Sched, bool ALIGN_EPI = false, bool SP2 = false>
; __device__ __forceinline__ void gemm_phase(PG8_LAS unsigned char* lds, const Gemm g, const Sched& S, const Epi& E, const int wave0) {
;     ...
;             PG8_LDA(At, 1, 1); PG8_STAGE(PG8_SB(1, 0), b3, voffB); PG8_STAGE(PG8_SB(1, 1), b3 + hstepB, voffB); PG8_STAGE(PG8_SA(1, 0), a3, voffA);
;             PG8_WAIT_V(8); PG8_WAIT_L(0); PG8_BAR; PG8_MMA(1, 0, At, B0); PG8_MMA(1, 1, At, B1); PG8_BAR; PG8_SCHED;
	s_add_i32 s60, s90, s5
	v_lshl_add_u64 v[170:171], v[170:171], 0, s[64:65]
	s_mov_b32 m0, s60
	ds_read_b128 v[180:183], v175 offset:49152
	ds_read_b128 v[184:187], v175 offset:50176
	ds_read_b128 v[188:191], v175 offset:51200
	ds_read_b128 v[192:195], v175 offset:52224
	ds_read_b128 v[196:199], v175 offset:53248
	ds_read_b128 v[200:203], v175 offset:54272
	ds_read_b128 v[204:207], v175 offset:55296
	ds_read_b128 v[224:227], v175 offset:56320
	global_load_lds_dwordx4 v[170:171], off
	v_lshl_add_u64 v[170:171], v[228:229], 0, s[64:65]
	s_add_i32 m0, s60, 0x2000
	s_add_i32 s60, s91, s5
	global_load_lds_dwordx4 v[170:171], off
	v_lshl_add_u64 v[170:171], v[230:231], 0, s[64:65]
	s_mov_b32 m0, s60
	s_nop 0
	global_load_lds_dwordx4 v[170:171], off
	v_lshl_add_u64 v[170:171], v[232:233], 0, s[64:65]
	s_add_i32 m0, s60, 0x2000
	s_nop 0
	global_load_lds_dwordx4 v[170:171], off
	v_lshl_add_u64 v[170:171], v[234:235], 0, s[64:65]
	s_mov_b32 m0, s74
	s_nop 0
	global_load_lds_dwordx4 v[170:171], off
	v_lshl_add_u64 v[170:171], v[236:237], 0, s[64:65]
	s_mov_b32 m0, s75
	s_nop 0
	global_load_lds_dwordx4 v[170:171], off
	s_waitcnt vmcnt(8)
	s_waitcnt lgkmcnt(0)
	s_barrier
	s_setprio 1
	s_waitcnt lgkmcnt(0)
	v_mfma_f32_16x16x32_bf16 v[62:65], v[130:133], v[180:183], v[62:65]
	v_mfma_f32_16x16x32_bf16 v[58:61], v[150:153], v[180:183], v[58:61]
	v_mfma_f32_16x16x32_bf16 v[46:49], v[130:133], v[188:191], v[46:49]
	v_mfma_f32_16x16x32_bf16 v[42:45], v[150:153], v[188:191], v[42:45]
	v_mfma_f32_16x16x32_bf16 v[30:33], v[130:133], v[196:199], v[30:33]
	v_mfma_f32_16x16x32_bf16 v[26:29], v[150:153], v[196:199], v[26:29]
	v_mfma_f32_16x16x32_bf16 v[14:17], v[130:133], v[204:207], v[14:17]
	v_mfma_f32_16x16x32_bf16 v[10:13], v[150:153], v[204:207], v[10:13]
	v_mfma_f32_16x16x32_bf16 v[62:65], v[134:137], v[184:187], v[62:65]
	v_mfma_f32_16x16x32_bf16 v[58:61], v[154:157], v[184:187], v[58:61]
	v_mfma_f32_16x16x32_bf16 v[46:49], v[134:137], v[192:195], v[46:49]
	v_mfma_f32_16x16x32_bf16 v[42:45], v[154:157], v[192:195], v[42:45]
	v_mfma_f32_16x16x32_bf16 v[30:33], v[134:137], v[200:203], v[30:33]
	v_mfma_f32_16x16x32_bf16 v[26:29], v[154:157], v[200:203], v[26:29]
	v_mfma_f32_16x16x32_bf16 v[14:17], v[134:137], v[224:227], v[14:17]
	v_mfma_f32_16x16x32_bf16 v[10:13], v[154:157], v[224:227], v[10:13]
	v_mfma_f32_16x16x32_bf16 v[54:57], v[158:161], v[180:183], v[54:57]
	v_mfma_f32_16x16x32_bf16 v[50:53], v[166:169], v[180:183], v[50:53]
	v_mfma_f32_16x16x32_bf16 v[38:41], v[158:161], v[188:191], v[38:41]
	v_mfma_f32_16x16x32_bf16 v[34:37], v[166:169], v[188:191], v[34:37]
	v_mfma_f32_16x16x32_bf16 v[22:25], v[158:161], v[196:199], v[22:25]
	v_mfma_f32_16x16x32_bf16 v[18:21], v[166:169], v[196:199], v[18:21]
	v_mfma_f32_16x16x32_bf16 v[6:9], v[158:161], v[204:207], v[6:9]
	v_mfma_f32_16x16x32_bf16 v[2:5], v[166:169], v[204:207], v[2:5]
	v_mfma_f32_16x16x32_bf16 v[54:57], v[162:165], v[184:187], v[54:57]
	v_mfma_f32_16x16x32_bf16 v[50:53], v[176:179], v[184:187], v[50:53]
	v_mfma_f32_16x16x32_bf16 v[38:41], v[162:165], v[192:195], v[38:41]
	v_mfma_f32_16x16x32_bf16 v[34:37], v[176:179], v[192:195], v[34:37]
	v_mfma_f32_16x16x32_bf16 v[22:25], v[162:165], v[200:203], v[22:25]
	v_mfma_f32_16x16x32_bf16 v[18:21], v[176:179], v[200:203], v[18:21]
	v_mfma_f32_16x16x32_bf16 v[6:9], v[162:165], v[224:227], v[6:9]
	v_mfma_f32_16x16x32_bf16 v[2:5], v[176:179], v[224:227], v[2:5]
	s_setprio 0
	s_barrier
	s_add_u32 s84, s84, 0x100
	s_addc_u32 s88, s88, 0
	s_add_u32 s58, s58, 0x100
	s_addc_u32 s59, s59, 0
	s_cmp_ge_i32 s89, s73
	s_mov_b32 s60, s89
	s_cbranch_scc0 .LBB0_1634
	v_readlane_b32 s90, v255, 24
	v_readlane_b32 s91, v255, 25

; #define PL_LOAD(RB, TAB, SE, BB) do { _Pragma("unroll") for (int _q = 0; _q < 16; ++_q) { \
;         const unsigned _pw = (unsigned)__builtin_amdgcn_readlane((int)(SE), (BB) * 8 + (_q >> 1)); const unsigned _idx = (_q & 1) ? (_pw >> 16) : (_pw & 0xffffu); \
;         (RB)[_q] = *(const v4u*)((TAB) + (size_t)_idx * 1024 + 16 * lane); } } while (0)
; #define U_RANGE(T, P, RLO, RHI, BLO, BHI) PL_RANGE4(T, P, RLO, RHI, BLO, BHI)
; #define U_RANGE(T, P, RLO, RHI, BLO, BHI) PL_RANGE(T, P, 2, RLO, RHI, BLO, BHI)
; #define U_ADV() do { ++lb; if (lb >= lbh) { ++lt; if (lt < 16) { U_RANGE(lt, ps, _r0, _r1, _b0, _b1); lb = _b0; lbh = _b1; (void)_r0; (void)_r1; seL = sIdx[lt * 64 + lane]; } } } while (0)
; #define U_SETC() do { ct = lt; cb = lb; { U_RANGE(ct, ps, _r0, _r1, _b0, _b1); crl = _r0; crh = _r1; cbl = _b0; (void)_b1; } } while (0)
; __device__ __forceinline__ void peer_unit(Frame& F, const Args& a, int layer, int unit, bool last) {
;     ...
;     for (int ps = DBG_U0; ps < UPASS; ++ps) {
;         int lt = 0, lb, lbh; { U_RANGE(lt, ps, r0, r1, b0_, b1_); lb = b0_; lbh = b1_; (void)r0; (void)r1; }
;         unsigned seL = sIdx[lane];
;         long xlo = 0, xhi = 0; const bool dsel = ((lane >> 2) & 3) == (lane >> 4); const unsigned char* N8 = (const unsigned char*)(F.ws + WS_N8); v4u nnx = *(const v4u*)(N8 + tokb * 1024 + 16 * lane);
;         int ct, cb, crl = 0, crh = 0, cbl = 0;
;     ...
;         PL_LOAD(ra, U8, seL, lb);
;         U_SETC(); U_ADV();
.LBB0_1729:
	v_readlane_b32 s5, v248, 0
	s_and_b32 s6, s5, 0xff
	s_add_i32 s6, s6, 15
	s_and_b32 s6, s6, 0x1f0
	s_min_u32 s30, s6, 0x80
	s_bfe_u32 s6, s5, 0x80008
	s_bfe_u32 s5, s5, 0x80010
	s_add_i32 s6, s6, 15
	s_add_i32 s5, s5, 15
	s_and_b32 s6, s6, 0x1f0
	s_and_b32 s5, s5, 0x1f0
	s_min_u32 s48, s6, 0x80
	s_min_u32 s5, s5, 0x80
	s_cmp_eq_u32 s3, 2
	s_cselect_b64 s[6:7], -1, 0
	s_and_b64 s[46:47], s[6:7], exec
	s_cselect_b32 s54, s48, s5
	s_cselect_b32 s5, s5, 0x80
	s_cmp_eq_u32 s3, 1
	s_cselect_b64 s[52:53], -1, 0
	s_and_b64 s[46:47], s[52:53], exec
	s_cselect_b32 s46, s30, s54
	s_cselect_b32 s5, s48, s5
	s_lshr_b32 s47, s46, 4
	s_min_u32 s47, s47, 7
	s_cmp_eq_u32 s3, 0
	ds_read_b32 v153, v247
	s_cselect_b64 s[54:55], -1, 0
	s_and_b64 s[56:57], s[54:55], exec
	s_cselect_b32 s48, 0, s47
	s_cselect_b32 s61, s30, s5
	s_lshl_b32 s5, s48, 3
	s_waitcnt lgkmcnt(0)
	v_readlane_b32 s47, v153, s5
	s_lshl_b32 s30, s47, 10
	s_and_b32 s30, s30, 0x3fffc00
	s_waitcnt vmcnt(15)
	v_lshl_add_u64 v[72:73], v[140:141], 0, s[30:31]
	s_bfe_u32 s30, s47, 0x100010
	s_lshl_b32 s30, s30, 10
	s_waitcnt vmcnt(14)
	v_lshl_add_u64 v[76:77], v[140:141], 0, s[30:31]
	s_or_b32 s30, s5, 1
	v_readlane_b32 s47, v153, s30
	s_lshl_b32 s30, s47, 10
	s_and_b32 s30, s30, 0x3fffc00
	s_waitcnt vmcnt(13)
	v_lshl_add_u64 v[80:81], v[140:141], 0, s[30:31]
	s_bfe_u32 s30, s47, 0x100010
	s_lshl_b32 s30, s30, 10
	s_waitcnt vmcnt(12)
	v_lshl_add_u64 v[84:85], v[140:141], 0, s[30:31]
	s_or_b32 s30, s5, 2
	v_readlane_b32 s47, v153, s30
	s_lshl_b32 s30, s47, 10
	s_and_b32 s30, s30, 0x3fffc00
	s_waitcnt vmcnt(11)
	v_lshl_add_u64 v[88:89], v[140:141], 0, s[30:31]
	s_bfe_u32 s30, s47, 0x100010
	s_lshl_b32 s30, s30, 10
	s_waitcnt vmcnt(10)
	v_lshl_add_u64 v[92:93], v[140:141], 0, s[30:31]
	s_or_b32 s30, s5, 3
	v_readlane_b32 s47, v153, s30
	s_lshl_b32 s30, s47, 10
	s_and_b32 s30, s30, 0x3fffc00
	s_waitcnt vmcnt(9)
	v_lshl_add_u64 v[96:97], v[140:141], 0, s[30:31]
	s_bfe_u32 s30, s47, 0x100010
	s_lshl_b32 s30, s30, 10
	s_waitcnt vmcnt(8)
	v_lshl_add_u64 v[100:101], v[140:141], 0, s[30:31]
	s_or_b32 s30, s5, 4
	v_readlane_b32 s47, v153, s30
	s_lshl_b32 s30, s47, 10
	s_and_b32 s30, s30, 0x3fffc00
	s_waitcnt vmcnt(7)
	v_lshl_add_u64 v[104:105], v[140:141], 0, s[30:31]
	s_bfe_u32 s30, s47, 0x100010
	s_lshl_b32 s30, s30, 10
	s_waitcnt vmcnt(6)
	v_lshl_add_u64 v[108:109], v[140:141], 0, s[30:31]
	s_or_b32 s30, s5, 5
	v_readlane_b32 s47, v153, s30
	s_lshl_b32 s30, s47, 10
	s_and_b32 s30, s30, 0x3fffc00
	s_waitcnt vmcnt(5)
	v_lshl_add_u64 v[112:113], v[140:141], 0, s[30:31]
	s_bfe_u32 s30, s47, 0x100010
	s_lshl_b32 s30, s30, 10
	s_waitcnt vmcnt(4)
	v_lshl_add_u64 v[116:117], v[140:141], 0, s[30:31]
	s_or_b32 s30, s5, 6
	v_readlane_b32 s47, v153, s30
	s_lshl_b32 s30, s47, 10
	s_and_b32 s30, s30, 0x3fffc00
	s_waitcnt vmcnt(3)
	v_lshl_add_u64 v[120:121], v[140:141], 0, s[30:31]
	s_bfe_u32 s30, s47, 0x100010
	s_or_b32 s5, s5, 7
	s_lshl_b32 s30, s30, 10
	v_readlane_b32 s5, v153, s5
	s_waitcnt vmcnt(2)
	v_lshl_add_u64 v[124:125], v[140:141], 0, s[30:31]
	s_lshl_b32 s30, s5, 10
	s_and_b32 s30, s30, 0x3fffc00
	s_bfe_u32 s5, s5, 0x100010
	s_waitcnt vmcnt(1)
	v_lshl_add_u64 v[128:129], v[140:141], 0, s[30:31]
	s_lshl_b32 s30, s5, 10
	s_waitcnt vmcnt(0)
	v_lshl_add_u64 v[132:133], v[140:141], 0, s[30:31]
	global_load_dwordx4 v[68:71], v[142:143], off
	global_load_dwordx4 v[72:75], v[72:73], off
	global_load_dwordx4 v[76:79], v[76:77], off
	global_load_dwordx4 v[80:83], v[80:81], off
	global_load_dwordx4 v[84:87], v[84:85], off
	global_load_dwordx4 v[88:91], v[88:89], off
	global_load_dwordx4 v[92:95], v[92:93], off
	global_load_dwordx4 v[96:99], v[96:97], off
	global_load_dwordx4 v[100:103], v[100:101], off
	global_load_dwordx4 v[104:107], v[104:105], off
	global_load_dwordx4 v[108:111], v[108:109], off
	global_load_dwordx4 v[112:115], v[112:113], off
	global_load_dwordx4 v[116:119], v[116:117], off
	global_load_dwordx4 v[120:123], v[120:121], off
	global_load_dwordx4 v[124:127], v[124:125], off
	global_load_dwordx4 v[128:131], v[128:129], off
	s_add_i32 s60, s48, 1
	global_load_dwordx4 v[132:135], v[132:133], off
	s_lshr_b32 s5, s61, 4
	s_cmp_gt_u32 s5, s60
	s_cbranch_scc1 .LBB0_1731
	v_readlane_b32 s5, v248, 1
	s_and_b32 s30, s5, 0xff
	s_bfe_u32 s47, s5, 0x80008
	s_bfe_u32 s5, s5, 0x80010
	s_add_i32 s30, s30, 15
	s_add_i32 s47, s47, 15
	s_add_i32 s5, s5, 15
	s_and_b32 s30, s30, 0x1f0
	s_and_b32 s47, s47, 0x1f0
	s_and_b32 s5, s5, 0x1f0
	s_min_u32 s30, s30, 0x80
	s_min_u32 s47, s47, 0x80
	s_min_u32 s5, s5, 0x80
	s_and_b64 s[56:57], s[6:7], exec
	s_cselect_b32 s58, s47, s5
	s_and_b64 s[56:57], s[52:53], exec
	s_cselect_b32 s58, s30, s58
	s_and_b64 s[56:57], s[6:7], exec
	s_cselect_b32 s5, s5, 0x80
	s_and_b64 s[56:57], s[52:53], exec
	s_cselect_b32 s5, s47, s5
	s_and_b64 s[56:57], s[54:55], exec
	s_cselect_b32 s5, s30, s5
	s_lshr_b32 s30, s58, 4
	s_min_u32 s30, s30, 7
	ds_read_b32 v153, v247 offset:256
	s_and_b64 s[56:57], s[54:55], exec
	s_cselect_b32 s60, 0, s30
	s_lshr_b32 s5, s5, 4
	s_add_i32 s30, s60, 1
	s_mov_b32 s59, 1
	s_max_u32 s5, s5, s30
	s_branch .LBB0_1732

; #define PL_LOAD(RB, TAB, SE, BB) do { _Pragma("unroll") for (int _q = 0; _q < 16; ++_q) { \
;         const unsigned _pw = (unsigned)__builtin_amdgcn_readlane((int)(SE), (BB) * 8 + (_q >> 1)); const unsigned _idx = (_q & 1) ? (_pw >> 16) : (_pw & 0xffffu); \
;         (RB)[_q] = *(const v4u*)((TAB) + (size_t)_idx * 1024 + 16 * lane); } } while (0)
; __device__ __forceinline__ void peer_unit(Frame& F, const Args& a, int layer, int unit, bool last) {
;     ...
;             if (lt < 16) PL_LOAD(rb, U8, seL, lb);
.LBB0_1735:
	s_cmp_gt_i32 s59, 15
	s_cbranch_scc1 .Lpu_skip1
	s_lshl_b32 s46, s60, 3
	s_waitcnt lgkmcnt(0)
	v_readlane_b32 s47, v153, s46
	s_lshl_b32 s30, s47, 10
	s_and_b32 s30, s30, 0x3fffc00
	v_lshl_add_u64 v[4:5], v[140:141], 0, s[30:31]
	s_bfe_u32 s30, s47, 0x100010
	s_lshl_b32 s30, s30, 10
	v_lshl_add_u64 v[8:9], v[140:141], 0, s[30:31]
	s_or_b32 s30, s46, 1
	v_readlane_b32 s47, v153, s30
	s_lshl_b32 s30, s47, 10
	s_and_b32 s30, s30, 0x3fffc00
	v_lshl_add_u64 v[12:13], v[140:141], 0, s[30:31]
	s_bfe_u32 s30, s47, 0x100010
	s_lshl_b32 s30, s30, 10
	v_lshl_add_u64 v[16:17], v[140:141], 0, s[30:31]
	s_or_b32 s30, s46, 2
	v_readlane_b32 s47, v153, s30
	s_lshl_b32 s30, s47, 10
	s_and_b32 s30, s30, 0x3fffc00
	v_lshl_add_u64 v[20:21], v[140:141], 0, s[30:31]
	s_bfe_u32 s30, s47, 0x100010
	s_lshl_b32 s30, s30, 10
	v_lshl_add_u64 v[24:25], v[140:141], 0, s[30:31]
	s_or_b32 s30, s46, 3
	v_readlane_b32 s47, v153, s30
	s_lshl_b32 s30, s47, 10
	s_and_b32 s30, s30, 0x3fffc00
	v_lshl_add_u64 v[28:29], v[140:141], 0, s[30:31]
	s_bfe_u32 s30, s47, 0x100010
	s_lshl_b32 s30, s30, 10
	v_lshl_add_u64 v[32:33], v[140:141], 0, s[30:31]
	s_or_b32 s30, s46, 4
	v_readlane_b32 s47, v153, s30
	s_lshl_b32 s30, s47, 10
	s_and_b32 s30, s30, 0x3fffc00
	v_lshl_add_u64 v[36:37], v[140:141], 0, s[30:31]
	s_bfe_u32 s30, s47, 0x100010
	s_lshl_b32 s30, s30, 10
	v_lshl_add_u64 v[40:41], v[140:141], 0, s[30:31]
	s_or_b32 s30, s46, 5
	v_readlane_b32 s47, v153, s30
	s_lshl_b32 s30, s47, 10
	s_and_b32 s30, s30, 0x3fffc00
	v_lshl_add_u64 v[44:45], v[140:141], 0, s[30:31]
	s_bfe_u32 s30, s47, 0x100010
	s_lshl_b32 s30, s30, 10
	v_lshl_add_u64 v[48:49], v[140:141], 0, s[30:31]
	s_or_b32 s30, s46, 6
	v_readlane_b32 s47, v153, s30
	s_lshl_b32 s30, s47, 10
	s_and_b32 s30, s30, 0x3fffc00
	v_lshl_add_u64 v[52:53], v[140:141], 0, s[30:31]
	s_bfe_u32 s30, s47, 0x100010
	s_lshl_b32 s30, s30, 10
	v_lshl_add_u64 v[56:57], v[140:141], 0, s[30:31]
	s_or_b32 s30, s46, 7
	v_readlane_b32 s46, v153, s30
	s_lshl_b32 s30, s46, 10
	s_and_b32 s30, s30, 0x3fffc00
	v_lshl_add_u64 v[60:61], v[140:141], 0, s[30:31]
	s_bfe_u32 s30, s46, 0x100010
	s_lshl_b32 s30, s30, 10
	v_lshl_add_u64 v[64:65], v[140:141], 0, s[30:31]
	global_load_dwordx4 v[4:7], v[4:5], off
	global_load_dwordx4 v[8:11], v[8:9], off
	global_load_dwordx4 v[12:15], v[12:13], off
	global_load_dwordx4 v[16:19], v[16:17], off
	global_load_dwordx4 v[20:23], v[20:21], off
	global_load_dwordx4 v[24:27], v[24:25], off
	global_load_dwordx4 v[28:31], v[28:29], off
	global_load_dwordx4 v[32:35], v[32:33], off
	global_load_dwordx4 v[36:39], v[36:37], off
	global_load_dwordx4 v[40:43], v[40:41], off
	global_load_dwordx4 v[44:47], v[44:45], off
	global_load_dwordx4 v[48:51], v[48:49], off
	global_load_dwordx4 v[52:55], v[52:53], off
	global_load_dwordx4 v[56:59], v[56:57], off
	global_load_dwordx4 v[60:63], v[60:61], off
	global_load_dwordx4 v[64:67], v[64:65], off
	s_branch .Lpu_go1

; #define PL_LOAD(RB, TAB, SE, BB) do { _Pragma("unroll") for (int _q = 0; _q < 16; ++_q) { \
;         const unsigned _pw = (unsigned)__builtin_amdgcn_readlane((int)(SE), (BB) * 8 + (_q >> 1)); const unsigned _idx = (_q & 1) ? (_pw >> 16) : (_pw & 0xffffu); \
;         (RB)[_q] = *(const v4u*)((TAB) + (size_t)_idx * 1024 + 16 * lane); } } while (0)
; __device__ __forceinline__ void peer_unit(Frame& F, const Args& a, int layer, int unit, bool last) {
;     ...
;             if (lt < 16) PL_LOAD(ra, U8, seL, lb);
.LBB0_1756:
	s_cmp_gt_i32 s58, 15
	s_cbranch_scc1 .LBB0_1758
	s_lshl_b32 s47, s48, 3
	s_waitcnt lgkmcnt(0)
	v_readlane_b32 s56, v153, s47
	s_lshl_b32 s30, s56, 10
	s_and_b32 s30, s30, 0x3fffc00
	v_lshl_add_u64 v[72:73], v[140:141], 0, s[30:31]
	s_bfe_u32 s30, s56, 0x100010
	s_lshl_b32 s30, s30, 10
	v_lshl_add_u64 v[76:77], v[140:141], 0, s[30:31]
	s_or_b32 s30, s47, 1
	v_readlane_b32 s56, v153, s30
	s_lshl_b32 s30, s56, 10
	s_and_b32 s30, s30, 0x3fffc00
	v_lshl_add_u64 v[80:81], v[140:141], 0, s[30:31]
	s_bfe_u32 s30, s56, 0x100010
	s_lshl_b32 s30, s30, 10
	v_lshl_add_u64 v[84:85], v[140:141], 0, s[30:31]
	s_or_b32 s30, s47, 2
	v_readlane_b32 s56, v153, s30
	s_lshl_b32 s30, s56, 10
	s_and_b32 s30, s30, 0x3fffc00
	v_lshl_add_u64 v[88:89], v[140:141], 0, s[30:31]
	s_bfe_u32 s30, s56, 0x100010
	s_lshl_b32 s30, s30, 10
	v_lshl_add_u64 v[92:93], v[140:141], 0, s[30:31]
	s_or_b32 s30, s47, 3
	v_readlane_b32 s56, v153, s30
	s_lshl_b32 s30, s56, 10
	s_and_b32 s30, s30, 0x3fffc00
	v_lshl_add_u64 v[96:97], v[140:141], 0, s[30:31]
	s_bfe_u32 s30, s56, 0x100010
	s_lshl_b32 s30, s30, 10
	v_lshl_add_u64 v[100:101], v[140:141], 0, s[30:31]
	s_or_b32 s30, s47, 4
	v_readlane_b32 s56, v153, s30
	s_lshl_b32 s30, s56, 10
	s_and_b32 s30, s30, 0x3fffc00
	v_lshl_add_u64 v[104:105], v[140:141], 0, s[30:31]
	s_bfe_u32 s30, s56, 0x100010
	s_lshl_b32 s30, s30, 10
	v_lshl_add_u64 v[108:109], v[140:141], 0, s[30:31]
	s_or_b32 s30, s47, 5
	v_readlane_b32 s56, v153, s30
	s_lshl_b32 s30, s56, 10
	s_and_b32 s30, s30, 0x3fffc00
	v_lshl_add_u64 v[112:113], v[140:141], 0, s[30:31]
	s_bfe_u32 s30, s56, 0x100010
	s_lshl_b32 s30, s30, 10
	v_lshl_add_u64 v[116:117], v[140:141], 0, s[30:31]
	s_or_b32 s30, s47, 6
	v_readlane_b32 s56, v153, s30
	s_lshl_b32 s30, s56, 10
	s_and_b32 s30, s30, 0x3fffc00
	v_lshl_add_u64 v[120:121], v[140:141], 0, s[30:31]
	s_bfe_u32 s30, s56, 0x100010
	s_lshl_b32 s30, s30, 10
	v_lshl_add_u64 v[124:125], v[140:141], 0, s[30:31]
	s_or_b32 s30, s47, 7
	v_readlane_b32 s47, v153, s30
	s_lshl_b32 s30, s47, 10
	s_and_b32 s30, s30, 0x3fffc00
	v_lshl_add_u64 v[128:129], v[140:141], 0, s[30:31]
	s_bfe_u32 s30, s47, 0x100010
	s_lshl_b32 s30, s30, 10
	v_lshl_add_u64 v[132:133], v[140:141], 0, s[30:31]
	global_load_dwordx4 v[72:75], v[72:73], off
	global_load_dwordx4 v[76:79], v[76:77], off
	global_load_dwordx4 v[80:83], v[80:81], off
	global_load_dwordx4 v[84:87], v[84:85], off
	global_load_dwordx4 v[88:91], v[88:89], off
	global_load_dwordx4 v[92:95], v[92:93], off
	global_load_dwordx4 v[96:99], v[96:97], off
	global_load_dwordx4 v[100:103], v[100:101], off
	global_load_dwordx4 v[104:107], v[104:105], off
	global_load_dwordx4 v[108:111], v[108:109], off
	global_load_dwordx4 v[112:115], v[112:113], off
	global_load_dwordx4 v[116:119], v[116:117], off
	global_load_dwordx4 v[120:123], v[120:121], off
	global_load_dwordx4 v[124:127], v[124:125], off
	global_load_dwordx4 v[128:131], v[128:129], off
	global_load_dwordx4 v[132:135], v[132:133], off
	s_waitcnt vmcnt(16)
	s_branch .Lpu_go2

; #define PL_LOAD(RB, TAB, SE, BB) do { _Pragma("unroll") for (int _q = 0; _q < 16; ++_q) { \
;         const unsigned _pw = (unsigned)__builtin_amdgcn_readlane((int)(SE), (BB) * 8 + (_q >> 1)); const unsigned _idx = (_q & 1) ? (_pw >> 16) : (_pw & 0xffffu); \
;         (RB)[_q] = *(const v4u*)((TAB) + (size_t)_idx * 1024 + 16 * lane); } } while (0)
; #define V_RANGE(T, P, RLO, RHI, BLO, BHI) PL_RANGE4(T, P, RLO, RHI, BLO, BHI)
; #define V_RANGE(T, P, RLO, RHI, BLO, BHI) PL_RANGE(T, P, 2, RLO, RHI, BLO, BHI)
; #define V_ADV() do { ++lb; if (lb >= lbh) { ++lt; if (lt < 16) { V_RANGE(lt, ps, _r0, _r1, _b0, _b1); lb = _b0; lbh = _b1; (void)_r0; (void)_r1; seL = sIdx[lt * 64 + lane]; } } } while (0)
; #define V_SETC() do { ct = lt; cb = lb; { V_RANGE(ct, ps, _r0, _r1, _b0, _b1); crl = _r0; crh = _r1; cbl = _b0; cbh = _b1; } } while (0)
; __device__ __forceinline__ void peer_unit(Frame& F, const Args& a, int layer, int unit, bool last) {
;     ...
;     for (int ps = DBG_V0; ps < VPASS; ++ps) {
;         int lt = 0, lb, lbh; { V_RANGE(lt, ps, r0, r1, b0_, b1_); lb = b0_; lbh = b1_; (void)r0; (void)r1; }
;         unsigned seL = sIdx[lane];
;         f32x2 out[8]; f32x4 hpre[4] = {(f32x4){0.f, 0.f, 0.f, 0.f}, (f32x4){0.f, 0.f, 0.f, 0.f}, (f32x4){0.f, 0.f, 0.f, 0.f}, (f32x4){0.f, 0.f, 0.f, 0.f}}, ac4[4]; v4u gpre[2] = {(v4u){0u, 0u, 0u, 0u}, (v4u){0u, 0u, 0u, 0u}}, p8pre = (v4u){0u, 0u, 0u, 0u}; const bf16* PWG = (const bf16*)(F.ws + WS_PW);
;         const unsigned vmask = ((lane >> 4) == ((lane & 15) >> 2)) ? (0xFFu << (8 * (lane & 3))) : 0u;
;         int ct, cb, crl = 0, crh = 0, cbl = 0, cbh = 0;
;     ...
;         PL_LOAD(ra, V8, seL, lb);
;         V_SETC(); V_ADV();
.LBB0_1781:
	v_readlane_b32 s5, v248, 0
	s_and_b32 s6, s5, 0xff
	s_add_i32 s6, s6, 15
	s_and_b32 s6, s6, 0x1f0
	s_min_u32 s30, s6, 0x80
	s_bfe_u32 s6, s5, 0x80008
	s_bfe_u32 s5, s5, 0x80010
	s_add_i32 s6, s6, 15
	s_add_i32 s5, s5, 15
	s_and_b32 s6, s6, 0x1f0
	s_and_b32 s5, s5, 0x1f0
	s_min_u32 s42, s6, 0x80
	s_min_u32 s5, s5, 0x80
	s_cmp_eq_u32 s3, 2
	s_cselect_b64 s[6:7], -1, 0
	s_and_b64 s[38:39], s[6:7], exec
	s_cselect_b32 s43, s42, s5
	s_cselect_b32 s5, s5, 0x80
	s_cmp_eq_u32 s3, 1
	s_cselect_b64 s[40:41], -1, 0
	s_and_b64 s[38:39], s[40:41], exec
	s_cselect_b32 s38, s30, s43
	s_cselect_b32 s5, s42, s5
	s_lshr_b32 s39, s38, 4
	s_min_u32 s39, s39, 7
	s_cmp_eq_u32 s3, 0
	ds_read_b32 v250, v247
	s_cselect_b64 s[42:43], -1, 0
	s_and_b64 s[44:45], s[42:43], exec
	s_cselect_b32 s56, 0, s39
	s_cselect_b32 s48, s30, s5
	s_lshl_b32 s5, s56, 3
	s_waitcnt lgkmcnt(0)
	v_readlane_b32 s39, v250, s5
	s_lshl_b32 s30, s39, 10
	s_and_b32 s30, s30, 0x3fffc00
	v_lshl_add_u64 v[2:3], v[226:227], 0, s[30:31]
	s_bfe_u32 s30, s39, 0x100010
	s_lshl_b32 s30, s30, 10
	s_waitcnt vmcnt(14)
	v_lshl_add_u64 v[72:73], v[226:227], 0, s[30:31]
	s_or_b32 s30, s5, 1
	v_readlane_b32 s39, v250, s30
	s_lshl_b32 s30, s39, 10
	s_and_b32 s30, s30, 0x3fffc00
	global_load_dwordx4 v[68:71], v[2:3], off
	global_load_dwordx4 v[72:75], v[72:73], off
	v_lshl_add_u64 v[2:3], v[226:227], 0, s[30:31]
	s_bfe_u32 s30, s39, 0x100010
	s_lshl_b32 s30, s30, 10
	s_waitcnt vmcnt(14)
	v_lshl_add_u64 v[80:81], v[226:227], 0, s[30:31]
	s_or_b32 s30, s5, 2
	v_readlane_b32 s39, v250, s30
	s_lshl_b32 s30, s39, 10
	s_and_b32 s30, s30, 0x3fffc00
	global_load_dwordx4 v[76:79], v[2:3], off
	global_load_dwordx4 v[80:83], v[80:81], off
	v_lshl_add_u64 v[2:3], v[226:227], 0, s[30:31]
	s_bfe_u32 s30, s39, 0x100010
	s_lshl_b32 s30, s30, 10
	s_waitcnt vmcnt(14)
	v_lshl_add_u64 v[88:89], v[226:227], 0, s[30:31]
	s_or_b32 s30, s5, 3
	v_readlane_b32 s39, v250, s30
	s_lshl_b32 s30, s39, 10
	s_and_b32 s30, s30, 0x3fffc00
	global_load_dwordx4 v[84:87], v[2:3], off
	global_load_dwordx4 v[88:91], v[88:89], off
	v_lshl_add_u64 v[2:3], v[226:227], 0, s[30:31]
	s_bfe_u32 s30, s39, 0x100010
	s_lshl_b32 s30, s30, 10
	s_waitcnt vmcnt(14)
	v_lshl_add_u64 v[96:97], v[226:227], 0, s[30:31]
	s_or_b32 s30, s5, 4
	v_readlane_b32 s39, v250, s30
	s_lshl_b32 s30, s39, 10
	s_and_b32 s30, s30, 0x3fffc00
	global_load_dwordx4 v[92:95], v[2:3], off
	global_load_dwordx4 v[96:99], v[96:97], off
	v_lshl_add_u64 v[2:3], v[226:227], 0, s[30:31]
	s_bfe_u32 s30, s39, 0x100010
	s_lshl_b32 s30, s30, 10
	s_waitcnt vmcnt(14)
	v_lshl_add_u64 v[104:105], v[226:227], 0, s[30:31]
	s_or_b32 s30, s5, 5
	v_readlane_b32 s39, v250, s30
	s_lshl_b32 s30, s39, 10
	s_and_b32 s30, s30, 0x3fffc00
	global_load_dwordx4 v[100:103], v[2:3], off
	global_load_dwordx4 v[104:107], v[104:105], off
	v_lshl_add_u64 v[2:3], v[226:227], 0, s[30:31]
	s_bfe_u32 s30, s39, 0x100010
	s_lshl_b32 s30, s30, 10
	s_waitcnt vmcnt(14)
	v_lshl_add_u64 v[112:113], v[226:227], 0, s[30:31]
	s_or_b32 s30, s5, 6
	v_readlane_b32 s39, v250, s30
	s_lshl_b32 s30, s39, 10
	s_and_b32 s30, s30, 0x3fffc00
	global_load_dwordx4 v[108:111], v[2:3], off
	global_load_dwordx4 v[112:115], v[112:113], off
	v_lshl_add_u64 v[2:3], v[226:227], 0, s[30:31]
	s_bfe_u32 s30, s39, 0x100010
	s_or_b32 s5, s5, 7
	s_lshl_b32 s30, s30, 10
	v_readlane_b32 s5, v250, s5
	s_waitcnt vmcnt(12)
	v_lshl_add_u64 v[116:117], v[226:227], 0, s[30:31]
	s_lshl_b32 s30, s5, 10
	s_and_b32 s30, s30, 0x3fffc00
	s_bfe_u32 s5, s5, 0x100010
	global_load_dwordx4 v[120:123], v[2:3], off
	global_load_dwordx4 v[124:127], v[116:117], off
	v_lshl_add_u64 v[2:3], v[226:227], 0, s[30:31]
	s_lshl_b32 s30, s5, 10
	v_lshl_add_u64 v[116:117], v[226:227], 0, s[30:31]
	global_load_dwordx4 v[144:147], v[2:3], off
	global_load_dwordx4 v[148:151], v[116:117], off
	s_add_i32 s59, s56, 1
	s_lshr_b32 s30, s48, 4
	s_cmp_gt_u32 s30, s59
	s_cbranch_scc1 .LBB0_1783
	v_readlane_b32 s5, v248, 1
	s_and_b32 s39, s5, 0xff
	s_bfe_u32 s44, s5, 0x80008
	s_bfe_u32 s5, s5, 0x80010
	s_add_i32 s39, s39, 15
	s_add_i32 s44, s44, 15
	s_add_i32 s5, s5, 15
	s_and_b32 s39, s39, 0x1f0
	s_and_b32 s44, s44, 0x1f0
	s_and_b32 s5, s5, 0x1f0
	s_min_u32 s39, s39, 0x80
	s_min_u32 s46, s44, 0x80
	s_min_u32 s5, s5, 0x80
	s_and_b64 s[44:45], s[6:7], exec
	s_cselect_b32 s47, s46, s5
	s_and_b64 s[44:45], s[40:41], exec
	s_cselect_b32 s47, s39, s47
	s_and_b64 s[44:45], s[6:7], exec
	s_cselect_b32 s5, s5, 0x80
	s_and_b64 s[44:45], s[40:41], exec
	s_cselect_b32 s5, s46, s5
	s_and_b64 s[44:45], s[42:43], exec
	s_cselect_b32 s5, s39, s5
	s_lshr_b32 s39, s47, 4
	s_min_u32 s39, s39, 7
	ds_read_b32 v250, v247 offset:256
	s_and_b64 s[44:45], s[42:43], exec
	s_cselect_b32 s59, 0, s39
	s_lshr_b32 s5, s5, 4
	s_add_i32 s39, s59, 1
	s_mov_b32 s57, 1
	s_max_u32 s5, s5, s39
	s_branch .LBB0_1784

; #define PL_LOAD(RB, TAB, SE, BB) do { _Pragma("unroll") for (int _q = 0; _q < 16; ++_q) { \
;         const unsigned _pw = (unsigned)__builtin_amdgcn_readlane((int)(SE), (BB) * 8 + (_q >> 1)); const unsigned _idx = (_q & 1) ? (_pw >> 16) : (_pw & 0xffffu); \
;         (RB)[_q] = *(const v4u*)((TAB) + (size_t)_idx * 1024 + 16 * lane); } } while (0)
; __device__ __forceinline__ void peer_unit(Frame& F, const Args& a, int layer, int unit, bool last) {
;     ...
;             if (lt < 16) PL_LOAD(rb, V8, seL, lb);
.LBB0_1798:
	s_cmp_gt_i32 s57, 15
	s_cbranch_scc1 .Lpv_mid_nopf
	s_lshl_b32 s38, s59, 3
	s_waitcnt lgkmcnt(0)
	v_readlane_b32 s39, v250, s38
	s_lshl_b32 s30, s39, 10
	s_and_b32 s30, s30, 0x3fffc00
	v_lshl_add_u64 v[2:3], v[226:227], 0, s[30:31]
	s_bfe_u32 s30, s39, 0x100010
	s_lshl_b32 s30, s30, 10
	v_lshl_add_u64 v[8:9], v[226:227], 0, s[30:31]
	s_or_b32 s30, s38, 1
	v_readlane_b32 s39, v250, s30
	s_lshl_b32 s30, s39, 10
	s_and_b32 s30, s30, 0x3fffc00
	global_load_dwordx4 v[4:7], v[2:3], off
	global_load_dwordx4 v[8:11], v[8:9], off
	v_lshl_add_u64 v[2:3], v[226:227], 0, s[30:31]
	s_bfe_u32 s30, s39, 0x100010
	s_lshl_b32 s30, s30, 10
	v_lshl_add_u64 v[16:17], v[226:227], 0, s[30:31]
	s_or_b32 s30, s38, 2
	v_readlane_b32 s39, v250, s30
	s_lshl_b32 s30, s39, 10
	s_and_b32 s30, s30, 0x3fffc00
	global_load_dwordx4 v[12:15], v[2:3], off
	global_load_dwordx4 v[16:19], v[16:17], off
	v_lshl_add_u64 v[2:3], v[226:227], 0, s[30:31]
	s_bfe_u32 s30, s39, 0x100010
	s_lshl_b32 s30, s30, 10
	v_lshl_add_u64 v[24:25], v[226:227], 0, s[30:31]
	s_or_b32 s30, s38, 3
	v_readlane_b32 s39, v250, s30
	s_lshl_b32 s30, s39, 10
	s_and_b32 s30, s30, 0x3fffc00
	global_load_dwordx4 v[20:23], v[2:3], off
	global_load_dwordx4 v[24:27], v[24:25], off
	v_lshl_add_u64 v[2:3], v[226:227], 0, s[30:31]
	s_bfe_u32 s30, s39, 0x100010
	s_lshl_b32 s30, s30, 10
	v_lshl_add_u64 v[32:33], v[226:227], 0, s[30:31]
	s_or_b32 s30, s38, 4
	v_readlane_b32 s39, v250, s30
	s_lshl_b32 s30, s39, 10
	s_and_b32 s30, s30, 0x3fffc00
	global_load_dwordx4 v[28:31], v[2:3], off
	global_load_dwordx4 v[32:35], v[32:33], off
	v_lshl_add_u64 v[2:3], v[226:227], 0, s[30:31]
	s_bfe_u32 s30, s39, 0x100010
	s_lshl_b32 s30, s30, 10
	v_lshl_add_u64 v[40:41], v[226:227], 0, s[30:31]
	s_or_b32 s30, s38, 5
	v_readlane_b32 s39, v250, s30
	s_lshl_b32 s30, s39, 10
	s_and_b32 s30, s30, 0x3fffc00
	global_load_dwordx4 v[36:39], v[2:3], off
	global_load_dwordx4 v[40:43], v[40:41], off
	v_lshl_add_u64 v[2:3], v[226:227], 0, s[30:31]
	s_bfe_u32 s30, s39, 0x100010
	s_lshl_b32 s30, s30, 10
	v_lshl_add_u64 v[48:49], v[226:227], 0, s[30:31]
	s_or_b32 s30, s38, 6
	v_readlane_b32 s39, v250, s30
	s_lshl_b32 s30, s39, 10
	s_and_b32 s30, s30, 0x3fffc00
	global_load_dwordx4 v[44:47], v[2:3], off
	global_load_dwordx4 v[48:51], v[48:49], off
	v_lshl_add_u64 v[2:3], v[226:227], 0, s[30:31]
	s_bfe_u32 s30, s39, 0x100010
	s_lshl_b32 s30, s30, 10
	v_lshl_add_u64 v[56:57], v[226:227], 0, s[30:31]
	s_or_b32 s30, s38, 7
	v_readlane_b32 s38, v250, s30
	s_lshl_b32 s30, s38, 10
	s_and_b32 s30, s30, 0x3fffc00
	global_load_dwordx4 v[52:55], v[2:3], off
	global_load_dwordx4 v[56:59], v[56:57], off
	v_lshl_add_u64 v[2:3], v[226:227], 0, s[30:31]
	s_bfe_u32 s30, s38, 0x100010
	s_lshl_b32 s30, s30, 10
	v_lshl_add_u64 v[64:65], v[226:227], 0, s[30:31]
	global_load_dwordx4 v[60:63], v[2:3], off
	global_load_dwordx4 v[64:67], v[64:65], off
	s_waitcnt vmcnt(16)
	s_branch .Lpv_mid_go

; #define PL_LOAD(RB, TAB, SE, BB) do { _Pragma("unroll") for (int _q = 0; _q < 16; ++_q) { \
;         const unsigned _pw = (unsigned)__builtin_amdgcn_readlane((int)(SE), (BB) * 8 + (_q >> 1)); const unsigned _idx = (_q & 1) ? (_pw >> 16) : (_pw & 0xffffu); \
;         (RB)[_q] = *(const v4u*)((TAB) + (size_t)_idx * 1024 + 16 * lane); } } while (0)
; __device__ __forceinline__ void peer_unit(Frame& F, const Args& a, int layer, int unit, bool last) {
;     ...
;             if (lt < 16) PL_LOAD(rb, V8, seL, lb);
.LBB0_1808:
	s_lshl_b32 s38, s58, 9
	s_add_i32 s38, s15, s38
	s_lshl_b32 s39, s56, 6
	s_add_i32 s38, s38, s39
	s_waitcnt vmcnt(0)
	v_mov_b32_e32 v168, s38
	ds_read_b128 v[170:173], v168
	s_cmp_gt_i32 s57, 15
	s_cbranch_scc1 .Lpv_skip1
	s_lshl_b32 s38, s59, 3
	s_waitcnt lgkmcnt(0)
	v_readlane_b32 s39, v250, s38
	s_lshl_b32 s30, s39, 10
	s_and_b32 s30, s30, 0x3fffc00
	v_lshl_add_u64 v[2:3], v[226:227], 0, s[30:31]
	s_bfe_u32 s30, s39, 0x100010
	s_lshl_b32 s30, s30, 10
	v_lshl_add_u64 v[8:9], v[226:227], 0, s[30:31]
	s_or_b32 s30, s38, 1
	v_readlane_b32 s39, v250, s30
	s_lshl_b32 s30, s39, 10
	s_and_b32 s30, s30, 0x3fffc00
	global_load_dwordx4 v[4:7], v[2:3], off
	global_load_dwordx4 v[8:11], v[8:9], off
	v_lshl_add_u64 v[2:3], v[226:227], 0, s[30:31]
	s_bfe_u32 s30, s39, 0x100010
	s_lshl_b32 s30, s30, 10
	v_lshl_add_u64 v[16:17], v[226:227], 0, s[30:31]
	s_or_b32 s30, s38, 2
	v_readlane_b32 s39, v250, s30
	s_lshl_b32 s30, s39, 10
	s_and_b32 s30, s30, 0x3fffc00
	global_load_dwordx4 v[12:15], v[2:3], off
	global_load_dwordx4 v[16:19], v[16:17], off
	v_lshl_add_u64 v[2:3], v[226:227], 0, s[30:31]
	s_bfe_u32 s30, s39, 0x100010
	s_lshl_b32 s30, s30, 10
	v_lshl_add_u64 v[24:25], v[226:227], 0, s[30:31]
	s_or_b32 s30, s38, 3
	v_readlane_b32 s39, v250, s30
	s_lshl_b32 s30, s39, 10
	s_and_b32 s30, s30, 0x3fffc00
	global_load_dwordx4 v[20:23], v[2:3], off
	global_load_dwordx4 v[24:27], v[24:25], off
	v_lshl_add_u64 v[2:3], v[226:227], 0, s[30:31]
	s_bfe_u32 s30, s39, 0x100010
	s_lshl_b32 s30, s30, 10
	v_lshl_add_u64 v[32:33], v[226:227], 0, s[30:31]
	s_or_b32 s30, s38, 4
	v_readlane_b32 s39, v250, s30
	s_lshl_b32 s30, s39, 10
	s_and_b32 s30, s30, 0x3fffc00
	global_load_dwordx4 v[28:31], v[2:3], off
	global_load_dwordx4 v[32:35], v[32:33], off
	v_lshl_add_u64 v[2:3], v[226:227], 0, s[30:31]
	s_bfe_u32 s30, s39, 0x100010
	s_lshl_b32 s30, s30, 10
	v_lshl_add_u64 v[40:41], v[226:227], 0, s[30:31]
	s_or_b32 s30, s38, 5
	v_readlane_b32 s39, v250, s30
	s_lshl_b32 s30, s39, 10
	s_and_b32 s30, s30, 0x3fffc00
	global_load_dwordx4 v[36:39], v[2:3], off
	global_load_dwordx4 v[40:43], v[40:41], off
	v_lshl_add_u64 v[2:3], v[226:227], 0, s[30:31]
	s_bfe_u32 s30, s39, 0x100010
	s_lshl_b32 s30, s30, 10
	v_lshl_add_u64 v[48:49], v[226:227], 0, s[30:31]
	s_or_b32 s30, s38, 6
	v_readlane_b32 s39, v250, s30
	s_lshl_b32 s30, s39, 10
	s_and_b32 s30, s30, 0x3fffc00
	global_load_dwordx4 v[44:47], v[2:3], off
	global_load_dwordx4 v[48:51], v[48:49], off
	v_lshl_add_u64 v[2:3], v[226:227], 0, s[30:31]
	s_bfe_u32 s30, s39, 0x100010
	s_lshl_b32 s30, s30, 10
	v_lshl_add_u64 v[56:57], v[226:227], 0, s[30:31]
	s_or_b32 s30, s38, 7
	v_readlane_b32 s38, v250, s30
	s_lshl_b32 s30, s38, 10
	s_and_b32 s30, s30, 0x3fffc00
	global_load_dwordx4 v[52:55], v[2:3], off
	global_load_dwordx4 v[56:59], v[56:57], off
	v_lshl_add_u64 v[2:3], v[226:227], 0, s[30:31]
	s_bfe_u32 s30, s38, 0x100010
	s_lshl_b32 s30, s30, 10
	v_lshl_add_u64 v[64:65], v[226:227], 0, s[30:31]
	global_load_dwordx4 v[60:63], v[2:3], off
	global_load_dwordx4 v[64:67], v[64:65], off

; #define PL_LOAD(RB, TAB, SE, BB) do { _Pragma("unroll") for (int _q = 0; _q < 16; ++_q) { \
;         const unsigned _pw = (unsigned)__builtin_amdgcn_readlane((int)(SE), (BB) * 8 + (_q >> 1)); const unsigned _idx = (_q & 1) ? (_pw >> 16) : (_pw & 0xffffu); \
;         (RB)[_q] = *(const v4u*)((TAB) + (size_t)_idx * 1024 + 16 * lane); } } while (0)
; __device__ __forceinline__ void peer_unit(Frame& F, const Args& a, int layer, int unit, bool last) {
;     ...
;             if (lt < 16) PL_LOAD(ra, V8, seL, lb);
.LBB0_1821:
	s_cmp_gt_i32 s58, 15
	s_cbranch_scc1 .LBB0_1823
	s_lshl_b32 s39, s56, 3
	s_waitcnt lgkmcnt(0)
	v_readlane_b32 s48, v250, s39
	s_lshl_b32 s30, s48, 10
	s_and_b32 s30, s30, 0x3fffc00
	v_lshl_add_u64 v[2:3], v[226:227], 0, s[30:31]
	s_bfe_u32 s30, s48, 0x100010
	s_lshl_b32 s30, s30, 10
	v_lshl_add_u64 v[72:73], v[226:227], 0, s[30:31]
	s_or_b32 s30, s39, 1
	v_readlane_b32 s48, v250, s30
	s_lshl_b32 s30, s48, 10
	s_and_b32 s30, s30, 0x3fffc00
	global_load_dwordx4 v[68:71], v[2:3], off
	global_load_dwordx4 v[72:75], v[72:73], off
	v_lshl_add_u64 v[2:3], v[226:227], 0, s[30:31]
	s_bfe_u32 s30, s48, 0x100010
	s_lshl_b32 s30, s30, 10
	v_lshl_add_u64 v[80:81], v[226:227], 0, s[30:31]
	s_or_b32 s30, s39, 2
	v_readlane_b32 s48, v250, s30
	s_lshl_b32 s30, s48, 10
	s_and_b32 s30, s30, 0x3fffc00
	global_load_dwordx4 v[76:79], v[2:3], off
	global_load_dwordx4 v[80:83], v[80:81], off
	v_lshl_add_u64 v[2:3], v[226:227], 0, s[30:31]
	s_bfe_u32 s30, s48, 0x100010
	s_lshl_b32 s30, s30, 10
	v_lshl_add_u64 v[88:89], v[226:227], 0, s[30:31]
	s_or_b32 s30, s39, 3
	v_readlane_b32 s48, v250, s30
	s_lshl_b32 s30, s48, 10
	s_and_b32 s30, s30, 0x3fffc00
	global_load_dwordx4 v[84:87], v[2:3], off
	global_load_dwordx4 v[88:91], v[88:89], off
	v_lshl_add_u64 v[2:3], v[226:227], 0, s[30:31]
	s_bfe_u32 s30, s48, 0x100010
	s_lshl_b32 s30, s30, 10
	v_lshl_add_u64 v[96:97], v[226:227], 0, s[30:31]
	s_or_b32 s30, s39, 4
	v_readlane_b32 s48, v250, s30
	s_lshl_b32 s30, s48, 10
	s_and_b32 s30, s30, 0x3fffc00
	global_load_dwordx4 v[92:95], v[2:3], off
	global_load_dwordx4 v[96:99], v[96:97], off
	v_lshl_add_u64 v[2:3], v[226:227], 0, s[30:31]
	s_bfe_u32 s30, s48, 0x100010
	s_lshl_b32 s30, s30, 10
	v_lshl_add_u64 v[104:105], v[226:227], 0, s[30:31]
	s_or_b32 s30, s39, 5
	v_readlane_b32 s48, v250, s30
	s_lshl_b32 s30, s48, 10
	s_and_b32 s30, s30, 0x3fffc00
	global_load_dwordx4 v[100:103], v[2:3], off
	global_load_dwordx4 v[104:107], v[104:105], off
	v_lshl_add_u64 v[2:3], v[226:227], 0, s[30:31]
	s_bfe_u32 s30, s48, 0x100010
	s_lshl_b32 s30, s30, 10
	v_lshl_add_u64 v[112:113], v[226:227], 0, s[30:31]
	s_or_b32 s30, s39, 6
	v_readlane_b32 s48, v250, s30
	s_lshl_b32 s30, s48, 10
	s_and_b32 s30, s30, 0x3fffc00
	global_load_dwordx4 v[108:111], v[2:3], off
	global_load_dwordx4 v[112:115], v[112:113], off
	v_lshl_add_u64 v[2:3], v[226:227], 0, s[30:31]
	s_bfe_u32 s30, s48, 0x100010
	s_lshl_b32 s30, s30, 10
	v_lshl_add_u64 v[124:125], v[226:227], 0, s[30:31]
	s_or_b32 s30, s39, 7
	v_readlane_b32 s39, v250, s30
	s_lshl_b32 s30, s39, 10
	s_and_b32 s30, s30, 0x3fffc00
	global_load_dwordx4 v[120:123], v[2:3], off
	global_load_dwordx4 v[124:127], v[124:125], off
	v_lshl_add_u64 v[2:3], v[226:227], 0, s[30:31]
	s_bfe_u32 s30, s39, 0x100010
	s_lshl_b32 s30, s30, 10
	v_lshl_add_u64 v[148:149], v[226:227], 0, s[30:31]
	global_load_dwordx4 v[144:147], v[2:3], off
	global_load_dwordx4 v[148:151], v[148:149], off
	s_waitcnt vmcnt(16)
	s_branch .Lpv_go2
